# static priority raise for waves 0-3 plus LDS-DMA issue ahead of the fragment reads in every load segment (on top of v70)
# speedup vs baseline: 1.0016x; 1.0016x over previous
.LBB0_120:
	s_add_u32 s41, s15, s18
	s_addc_u32 s42, s24, s19
	s_add_u32 s66, s18, 0x100
	s_addc_u32 s67, s19, 0
	s_cmp_eq_u32 s40, 28
	s_cselect_b64 s[70:71], -1, 0
	s_and_b64 s[2:3], s[70:71], exec
	s_cselect_b32 s69, s5, s42
	s_cselect_b32 s68, s13, s41
	s_cselect_b32 s41, 0, s66
	v_lshl_add_u64 v[198:199], v[132:133], 0, s[18:19]
	s_add_i32 m0, s92, 0xc000
	s_nop 0
	global_load_lds_dwordx4 v[198:199], off
	v_lshl_add_u64 v[198:199], v[134:135], 0, s[18:19]
	s_add_i32 m0, s92, 0xe000
	s_nop 0
	global_load_lds_dwordx4 v[198:199], off
	ds_read_b128 v[136:139], v211
	ds_read_b128 v[140:143], v211 offset:1024
	ds_read_b128 v[144:147], v211 offset:2048
	ds_read_b128 v[148:151], v211 offset:3072
	ds_read_b128 v[152:155], v212
	ds_read_b128 v[156:159], v212 offset:1024
	ds_read_b128 v[160:163], v212 offset:2048
	ds_read_b128 v[186:189], v212 offset:3072
	ds_read_b128 v[190:193], v213
	ds_read_b128 v[194:197], v213 offset:1024
	ds_read_b128 v[214:217], v213 offset:2048
	ds_read_b128 v[218:221], v213 offset:3072
	ds_read_b128 v[222:225], v213 offset:4096
	ds_read_b128 v[226:229], v213 offset:5120
	ds_read_b128 v[230:233], v213 offset:6144
	ds_read_b128 v[234:237], v213 offset:7168
	s_waitcnt vmcnt(8)
	s_waitcnt lgkmcnt(0)
	s_barrier
	s_waitcnt lgkmcnt(0)
	v_mfma_f32_16x16x32_bf16 v[128:131], v[136:139], v[190:193], v[128:131]
	v_mfma_f32_16x16x32_bf16 v[124:127], v[144:147], v[190:193], v[124:127]
	v_mfma_f32_16x16x32_bf16 v[120:123], v[136:139], v[214:217], v[120:123]
	v_mfma_f32_16x16x32_bf16 v[112:115], v[144:147], v[214:217], v[112:115]
	v_mfma_f32_16x16x32_bf16 v[104:107], v[136:139], v[222:225], v[104:107]
	v_mfma_f32_16x16x32_bf16 v[96:99], v[144:147], v[222:225], v[96:99]
	v_mfma_f32_16x16x32_bf16 v[88:91], v[136:139], v[230:233], v[88:91]
	v_mfma_f32_16x16x32_bf16 v[80:83], v[144:147], v[230:233], v[80:83]
	v_mfma_f32_16x16x32_bf16 v[128:131], v[140:143], v[194:197], v[128:131]
	v_mfma_f32_16x16x32_bf16 v[124:127], v[148:151], v[194:197], v[124:127]
	v_mfma_f32_16x16x32_bf16 v[120:123], v[140:143], v[218:221], v[120:123]
	v_mfma_f32_16x16x32_bf16 v[112:115], v[148:151], v[218:221], v[112:115]
	v_mfma_f32_16x16x32_bf16 v[104:107], v[140:143], v[226:229], v[104:107]
	v_mfma_f32_16x16x32_bf16 v[96:99], v[148:151], v[226:229], v[96:99]
	v_mfma_f32_16x16x32_bf16 v[88:91], v[140:143], v[234:237], v[88:91]
	v_mfma_f32_16x16x32_bf16 v[80:83], v[148:151], v[234:237], v[80:83]
	v_mfma_f32_16x16x32_bf16 v[116:119], v[152:155], v[190:193], v[116:119]
	v_mfma_f32_16x16x32_bf16 v[108:111], v[160:163], v[190:193], v[108:111]
	v_mfma_f32_16x16x32_bf16 v[100:103], v[152:155], v[214:217], v[100:103]
	v_mfma_f32_16x16x32_bf16 v[92:95], v[160:163], v[214:217], v[92:95]
	v_mfma_f32_16x16x32_bf16 v[84:87], v[152:155], v[222:225], v[84:87]
	v_mfma_f32_16x16x32_bf16 v[76:79], v[160:163], v[222:225], v[76:79]
	v_mfma_f32_16x16x32_bf16 v[72:75], v[152:155], v[230:233], v[72:75]
	v_mfma_f32_16x16x32_bf16 v[68:71], v[160:163], v[230:233], v[68:71]
	v_mfma_f32_16x16x32_bf16 v[116:119], v[156:159], v[194:197], v[116:119]
	v_mfma_f32_16x16x32_bf16 v[108:111], v[186:189], v[194:197], v[108:111]
	v_mfma_f32_16x16x32_bf16 v[100:103], v[156:159], v[218:221], v[100:103]
	v_mfma_f32_16x16x32_bf16 v[92:95], v[186:189], v[218:221], v[92:95]
	v_mfma_f32_16x16x32_bf16 v[84:87], v[156:159], v[226:229], v[84:87]
	v_mfma_f32_16x16x32_bf16 v[76:79], v[186:189], v[226:229], v[76:79]
	v_mfma_f32_16x16x32_bf16 v[72:75], v[156:159], v[234:237], v[72:75]
	v_mfma_f32_16x16x32_bf16 v[68:71], v[186:189], v[234:237], v[68:71]
	s_barrier
	s_add_i32 s2, s54, s96
	v_lshl_add_u64 v[198:199], s[68:69], 0, v[166:167]
	s_mov_b32 m0, s2
	s_nop 0
	global_load_lds_dwordx4 v[198:199], off
	s_add_i32 m0, s2, 0x2000
	s_add_u32 s2, s68, 0x80000
	v_lshl_add_u64 v[238:239], s[68:69], 0, v[170:171]
	s_addc_u32 s3, s69, 0
	s_add_i32 s18, s55, s96
	global_load_lds_dwordx4 v[238:239], off
	v_lshl_add_u64 v[240:241], s[2:3], 0, v[166:167]
	s_mov_b32 m0, s18
	s_nop 0
	global_load_lds_dwordx4 v[240:241], off
	v_lshl_add_u64 v[240:241], s[2:3], 0, v[170:171]
	s_add_i32 m0, s18, 0x2000
	s_and_b64 s[2:3], s[10:11], s[70:71]
	s_and_b64 s[2:3], s[2:3], exec
	s_cselect_b32 s2, s62, s16
	s_cselect_b32 s3, s63, s17
	s_add_u32 s2, s2, s41
	s_addc_u32 s3, s3, 0
	global_load_lds_dwordx4 v[240:241], off
	v_lshl_add_u64 v[240:241], s[2:3], 0, v[164:165]
	s_mov_b32 m0, s92
	v_lshl_add_u64 v[244:245], s[2:3], 0, v[168:169]
	global_load_lds_dwordx4 v[240:241], off
	s_mov_b32 m0, s52
	s_nop 0
	global_load_lds_dwordx4 v[244:245], off
	ds_read_b128 v[190:193], v213 offset:16384
	ds_read_b128 v[194:197], v213 offset:17408
	ds_read_b128 v[214:217], v213 offset:18432
	ds_read_b128 v[218:221], v213 offset:19456
	ds_read_b128 v[222:225], v213 offset:20480
	ds_read_b128 v[226:229], v213 offset:21504
	ds_read_b128 v[230:233], v213 offset:22528
	ds_read_b128 v[234:237], v213 offset:23552
	s_waitcnt vmcnt(8)
	s_waitcnt lgkmcnt(0)
	s_barrier
	s_waitcnt lgkmcnt(0)
	v_mfma_f32_16x16x32_bf16 v[64:67], v[136:139], v[190:193], v[64:67]
	v_mfma_f32_16x16x32_bf16 v[60:63], v[144:147], v[190:193], v[60:63]
	v_mfma_f32_16x16x32_bf16 v[52:55], v[136:139], v[214:217], v[52:55]
	v_mfma_f32_16x16x32_bf16 v[44:47], v[144:147], v[214:217], v[44:47]
	v_mfma_f32_16x16x32_bf16 v[36:39], v[136:139], v[222:225], v[36:39]
	v_mfma_f32_16x16x32_bf16 v[28:31], v[144:147], v[222:225], v[28:31]
	v_mfma_f32_16x16x32_bf16 v[20:23], v[136:139], v[230:233], v[20:23]
	v_mfma_f32_16x16x32_bf16 v[12:15], v[144:147], v[230:233], v[12:15]
	v_mfma_f32_16x16x32_bf16 v[64:67], v[140:143], v[194:197], v[64:67]
	v_mfma_f32_16x16x32_bf16 v[60:63], v[148:151], v[194:197], v[60:63]
	v_mfma_f32_16x16x32_bf16 v[52:55], v[140:143], v[218:221], v[52:55]
	v_mfma_f32_16x16x32_bf16 v[44:47], v[148:151], v[218:221], v[44:47]
	v_mfma_f32_16x16x32_bf16 v[36:39], v[140:143], v[226:229], v[36:39]
	v_mfma_f32_16x16x32_bf16 v[28:31], v[148:151], v[226:229], v[28:31]
	v_mfma_f32_16x16x32_bf16 v[20:23], v[140:143], v[234:237], v[20:23]
	v_mfma_f32_16x16x32_bf16 v[12:15], v[148:151], v[234:237], v[12:15]
	v_mfma_f32_16x16x32_bf16 v[56:59], v[152:155], v[190:193], v[56:59]
	v_mfma_f32_16x16x32_bf16 v[48:51], v[160:163], v[190:193], v[48:51]
	v_mfma_f32_16x16x32_bf16 v[40:43], v[152:155], v[214:217], v[40:43]
	v_mfma_f32_16x16x32_bf16 v[32:35], v[160:163], v[214:217], v[32:35]
	v_mfma_f32_16x16x32_bf16 v[24:27], v[152:155], v[222:225], v[24:27]
	v_mfma_f32_16x16x32_bf16 v[16:19], v[160:163], v[222:225], v[16:19]
	v_mfma_f32_16x16x32_bf16 v[8:11], v[152:155], v[230:233], v[8:11]
	v_mfma_f32_16x16x32_bf16 v[4:7], v[160:163], v[230:233], v[4:7]
	v_mfma_f32_16x16x32_bf16 v[56:59], v[156:159], v[194:197], v[56:59]
	v_mfma_f32_16x16x32_bf16 v[48:51], v[186:189], v[194:197], v[48:51]
	v_mfma_f32_16x16x32_bf16 v[40:43], v[156:159], v[218:221], v[40:43]
	v_mfma_f32_16x16x32_bf16 v[32:35], v[186:189], v[218:221], v[32:35]
	v_mfma_f32_16x16x32_bf16 v[24:27], v[156:159], v[226:229], v[24:27]
	v_mfma_f32_16x16x32_bf16 v[16:19], v[186:189], v[226:229], v[16:19]
	v_mfma_f32_16x16x32_bf16 v[8:11], v[156:159], v[234:237], v[8:11]
	v_mfma_f32_16x16x32_bf16 v[4:7], v[186:189], v[234:237], v[4:7]
	s_barrier
	s_add_u32 s2, s2, 0x80000
	s_addc_u32 s3, s3, 0
	s_mov_b32 m0, s53
	v_lshl_add_u64 v[246:247], s[2:3], 0, v[164:165]
	global_load_lds_dwordx4 v[246:247], off
	v_lshl_add_u64 v[246:247], s[2:3], 0, v[168:169]
	s_mov_b32 m0, s50
	s_nop 0
	global_load_lds_dwordx4 v[246:247], off
	s_add_i32 s18, 0, 0x18000
	v_add_u32_e32 v3, s18, v209
	s_add_i32 s19, 0, 0x1c000
	ds_read_b128 v[136:139], v3
	ds_read_b128 v[140:143], v3 offset:1024
	ds_read_b128 v[144:147], v3 offset:2048
	ds_read_b128 v[148:151], v3 offset:3072
	v_add_u32_e32 v3, s19, v209
	ds_read_b128 v[152:155], v3
	ds_read_b128 v[156:159], v3 offset:1024
	ds_read_b128 v[160:163], v3 offset:2048
	ds_read_b128 v[186:189], v3 offset:3072
	ds_read_b128 v[190:193], v213 offset:32768
	ds_read_b128 v[194:197], v213 offset:33792
	ds_read_b128 v[214:217], v213 offset:34816
	ds_read_b128 v[218:221], v213 offset:35840
	ds_read_b128 v[222:225], v213 offset:36864
	ds_read_b128 v[226:229], v213 offset:37888
	ds_read_b128 v[230:233], v213 offset:38912
	ds_read_b128 v[234:237], v213 offset:39936
	s_waitcnt vmcnt(8)
	s_waitcnt lgkmcnt(0)
	s_barrier
	s_waitcnt lgkmcnt(0)
	v_mfma_f32_16x16x32_bf16 v[128:131], v[136:139], v[190:193], v[128:131]
	v_mfma_f32_16x16x32_bf16 v[124:127], v[144:147], v[190:193], v[124:127]
	v_mfma_f32_16x16x32_bf16 v[120:123], v[136:139], v[214:217], v[120:123]
	v_mfma_f32_16x16x32_bf16 v[112:115], v[144:147], v[214:217], v[112:115]
	v_mfma_f32_16x16x32_bf16 v[104:107], v[136:139], v[222:225], v[104:107]
	v_mfma_f32_16x16x32_bf16 v[96:99], v[144:147], v[222:225], v[96:99]
	v_mfma_f32_16x16x32_bf16 v[88:91], v[136:139], v[230:233], v[88:91]
	v_mfma_f32_16x16x32_bf16 v[80:83], v[144:147], v[230:233], v[80:83]
	v_mfma_f32_16x16x32_bf16 v[128:131], v[140:143], v[194:197], v[128:131]
	v_mfma_f32_16x16x32_bf16 v[124:127], v[148:151], v[194:197], v[124:127]
	v_mfma_f32_16x16x32_bf16 v[120:123], v[140:143], v[218:221], v[120:123]
	v_mfma_f32_16x16x32_bf16 v[112:115], v[148:151], v[218:221], v[112:115]
	v_mfma_f32_16x16x32_bf16 v[104:107], v[140:143], v[226:229], v[104:107]
	v_mfma_f32_16x16x32_bf16 v[96:99], v[148:151], v[226:229], v[96:99]
	v_mfma_f32_16x16x32_bf16 v[88:91], v[140:143], v[234:237], v[88:91]
	v_mfma_f32_16x16x32_bf16 v[80:83], v[148:151], v[234:237], v[80:83]
	v_mfma_f32_16x16x32_bf16 v[116:119], v[152:155], v[190:193], v[116:119]
	v_mfma_f32_16x16x32_bf16 v[108:111], v[160:163], v[190:193], v[108:111]
	v_mfma_f32_16x16x32_bf16 v[100:103], v[152:155], v[214:217], v[100:103]
	v_mfma_f32_16x16x32_bf16 v[92:95], v[160:163], v[214:217], v[92:95]
	v_mfma_f32_16x16x32_bf16 v[84:87], v[152:155], v[222:225], v[84:87]
	v_mfma_f32_16x16x32_bf16 v[76:79], v[160:163], v[222:225], v[76:79]
	v_mfma_f32_16x16x32_bf16 v[72:75], v[152:155], v[230:233], v[72:75]
	v_mfma_f32_16x16x32_bf16 v[68:71], v[160:163], v[230:233], v[68:71]
	v_mfma_f32_16x16x32_bf16 v[116:119], v[156:159], v[194:197], v[116:119]
	v_mfma_f32_16x16x32_bf16 v[108:111], v[186:189], v[194:197], v[108:111]
	v_mfma_f32_16x16x32_bf16 v[100:103], v[156:159], v[218:221], v[100:103]
	v_mfma_f32_16x16x32_bf16 v[92:95], v[186:189], v[218:221], v[92:95]
	v_mfma_f32_16x16x32_bf16 v[84:87], v[156:159], v[226:229], v[84:87]
	v_mfma_f32_16x16x32_bf16 v[76:79], v[186:189], v[226:229], v[76:79]
	v_mfma_f32_16x16x32_bf16 v[72:75], v[156:159], v[234:237], v[72:75]
	v_mfma_f32_16x16x32_bf16 v[68:71], v[186:189], v[234:237], v[68:71]
	s_barrier
	s_add_i32 s2, s18, s96
	v_lshl_add_u64 v[198:199], v[198:199], 0, s[38:39]
	s_mov_b32 m0, s2
	s_nop 0
	global_load_lds_dwordx4 v[198:199], off
	s_add_i32 m0, s2, 0x2000
	s_add_u32 s2, s68, 0x80080
	v_lshl_add_u64 v[198:199], v[238:239], 0, s[38:39]
	s_addc_u32 s3, s69, 0
	s_add_i32 s18, s19, s96
	global_load_lds_dwordx4 v[198:199], off
	v_lshl_add_u64 v[198:199], s[2:3], 0, v[166:167]
	s_mov_b32 m0, s18
	s_nop 0
	global_load_lds_dwordx4 v[198:199], off
	v_lshl_add_u64 v[198:199], s[2:3], 0, v[170:171]
	s_add_i32 m0, s18, 0x2000
	s_nop 0
	global_load_lds_dwordx4 v[198:199], off
	v_lshl_add_u64 v[198:199], v[240:241], 0, s[38:39]
	s_mov_b32 m0, s56
	s_nop 0
	global_load_lds_dwordx4 v[198:199], off
	v_lshl_add_u64 v[198:199], v[244:245], 0, s[38:39]
	s_mov_b32 m0, s57
	s_nop 0
	global_load_lds_dwordx4 v[198:199], off
	ds_read_b128 v[190:193], v213 offset:49152
	ds_read_b128 v[194:197], v213 offset:50176
	ds_read_b128 v[214:217], v213 offset:51200
	ds_read_b128 v[218:221], v213 offset:52224
	ds_read_b128 v[222:225], v213 offset:53248
	ds_read_b128 v[226:229], v213 offset:54272
	ds_read_b128 v[230:233], v213 offset:55296
	ds_read_b128 v[234:237], v213 offset:56320
	s_waitcnt vmcnt(8)
	s_waitcnt lgkmcnt(0)
	s_barrier
	s_waitcnt lgkmcnt(0)
	v_mfma_f32_16x16x32_bf16 v[64:67], v[136:139], v[190:193], v[64:67]
	v_mfma_f32_16x16x32_bf16 v[60:63], v[144:147], v[190:193], v[60:63]
	v_mfma_f32_16x16x32_bf16 v[52:55], v[136:139], v[214:217], v[52:55]
	v_mfma_f32_16x16x32_bf16 v[44:47], v[144:147], v[214:217], v[44:47]
	v_mfma_f32_16x16x32_bf16 v[36:39], v[136:139], v[222:225], v[36:39]
	v_mfma_f32_16x16x32_bf16 v[28:31], v[144:147], v[222:225], v[28:31]
	v_mfma_f32_16x16x32_bf16 v[20:23], v[136:139], v[230:233], v[20:23]
	v_mfma_f32_16x16x32_bf16 v[12:15], v[144:147], v[230:233], v[12:15]
	v_mfma_f32_16x16x32_bf16 v[64:67], v[140:143], v[194:197], v[64:67]
	v_mfma_f32_16x16x32_bf16 v[60:63], v[148:151], v[194:197], v[60:63]
	v_mfma_f32_16x16x32_bf16 v[52:55], v[140:143], v[218:221], v[52:55]
	v_mfma_f32_16x16x32_bf16 v[44:47], v[148:151], v[218:221], v[44:47]
	v_mfma_f32_16x16x32_bf16 v[36:39], v[140:143], v[226:229], v[36:39]
	v_mfma_f32_16x16x32_bf16 v[28:31], v[148:151], v[226:229], v[28:31]
	v_mfma_f32_16x16x32_bf16 v[20:23], v[140:143], v[234:237], v[20:23]
	v_mfma_f32_16x16x32_bf16 v[12:15], v[148:151], v[234:237], v[12:15]
	v_mfma_f32_16x16x32_bf16 v[56:59], v[152:155], v[190:193], v[56:59]
	v_mfma_f32_16x16x32_bf16 v[48:51], v[160:163], v[190:193], v[48:51]
	v_mfma_f32_16x16x32_bf16 v[40:43], v[152:155], v[214:217], v[40:43]
	v_mfma_f32_16x16x32_bf16 v[32:35], v[160:163], v[214:217], v[32:35]
	v_mfma_f32_16x16x32_bf16 v[24:27], v[152:155], v[222:225], v[24:27]
	v_mfma_f32_16x16x32_bf16 v[16:19], v[160:163], v[222:225], v[16:19]
	v_mfma_f32_16x16x32_bf16 v[8:11], v[152:155], v[230:233], v[8:11]
	v_mfma_f32_16x16x32_bf16 v[4:7], v[160:163], v[230:233], v[4:7]
	v_mfma_f32_16x16x32_bf16 v[56:59], v[156:159], v[194:197], v[56:59]
	v_mfma_f32_16x16x32_bf16 v[48:51], v[186:189], v[194:197], v[48:51]
	v_mfma_f32_16x16x32_bf16 v[40:43], v[156:159], v[218:221], v[40:43]
	v_mfma_f32_16x16x32_bf16 v[32:35], v[186:189], v[218:221], v[32:35]
	v_mfma_f32_16x16x32_bf16 v[24:27], v[156:159], v[226:229], v[24:27]
	v_mfma_f32_16x16x32_bf16 v[16:19], v[186:189], v[226:229], v[16:19]
	v_mfma_f32_16x16x32_bf16 v[8:11], v[156:159], v[234:237], v[8:11]
	v_mfma_f32_16x16x32_bf16 v[4:7], v[186:189], v[234:237], v[4:7]
	s_barrier
	s_add_i32 s40, s40, 2
	s_cmp_gt_u32 s40, 29
	s_mov_b64 s[18:19], s[66:67]
	s_cbranch_scc0 .LBB0_120
	v_readlane_b32 s2, v252, 27
	v_readlane_b32 s3, v252, 28
	s_and_b64 vcc, exec, s[2:3]
	s_cbranch_vccz .LBB0_123
	s_barrier

.LBB0_346:
	s_add_u32 s34, s51, s28
	s_addc_u32 s35, s52, s29
	s_add_u32 s30, s28, 0x100
	s_addc_u32 s31, s29, 0
	s_cmp_eq_u32 s53, 28
	s_cselect_b64 s[36:37], -1, 0
	s_and_b64 s[2:3], s[36:37], exec
	s_cselect_b32 s35, s15, s35
	s_cselect_b32 s34, s17, s34
	s_cselect_b32 s54, 0, s30
	v_lshl_add_u64 v[220:221], v[140:141], 0, s[28:29]
	s_add_i32 m0, s21, 0xc000
	s_nop 0
	global_load_lds_dwordx4 v[220:221], off
	v_lshl_add_u64 v[220:221], v[142:143], 0, s[28:29]
	s_add_i32 m0, s21, 0xe000
	s_nop 0
	global_load_lds_dwordx4 v[220:221], off
	ds_read_b128 v[148:151], v1
	ds_read_b128 v[152:155], v1 offset:1024
	ds_read_b128 v[156:159], v1 offset:2048
	ds_read_b128 v[160:163], v1 offset:3072
	ds_read_b128 v[172:175], v145
	ds_read_b128 v[176:179], v145 offset:1024
	ds_read_b128 v[180:183], v145 offset:2048
	ds_read_b128 v[184:187], v145 offset:3072
	ds_read_b128 v[188:191], v146
	ds_read_b128 v[192:195], v146 offset:1024
	ds_read_b128 v[196:199], v146 offset:2048
	ds_read_b128 v[200:203], v146 offset:3072
	ds_read_b128 v[204:207], v146 offset:4096
	ds_read_b128 v[208:211], v146 offset:5120
	ds_read_b128 v[212:215], v146 offset:6144
	ds_read_b128 v[216:219], v146 offset:7168
	s_waitcnt vmcnt(8)
	s_waitcnt lgkmcnt(0)
	s_barrier
	s_waitcnt lgkmcnt(0)
	v_mfma_f32_16x16x32_bf16 v[126:129], v[188:191], v[148:151], v[126:129]
	v_mfma_f32_16x16x32_bf16 v[114:117], v[188:191], v[156:159], v[114:117]
	v_mfma_f32_16x16x32_bf16 v[122:125], v[196:199], v[148:151], v[122:125]
	v_mfma_f32_16x16x32_bf16 v[106:109], v[196:199], v[156:159], v[106:109]
	v_mfma_f32_16x16x32_bf16 v[118:121], v[204:207], v[148:151], v[118:121]
	v_mfma_f32_16x16x32_bf16 v[102:105], v[204:207], v[156:159], v[102:105]
	v_mfma_f32_16x16x32_bf16 v[110:113], v[212:215], v[148:151], v[110:113]
	v_mfma_f32_16x16x32_bf16 v[98:101], v[212:215], v[156:159], v[98:101]
	v_mfma_f32_16x16x32_bf16 v[126:129], v[192:195], v[152:155], v[126:129]
	v_mfma_f32_16x16x32_bf16 v[114:117], v[192:195], v[160:163], v[114:117]
	v_mfma_f32_16x16x32_bf16 v[122:125], v[200:203], v[152:155], v[122:125]
	v_mfma_f32_16x16x32_bf16 v[106:109], v[200:203], v[160:163], v[106:109]
	v_mfma_f32_16x16x32_bf16 v[118:121], v[208:211], v[152:155], v[118:121]
	v_mfma_f32_16x16x32_bf16 v[102:105], v[208:211], v[160:163], v[102:105]
	v_mfma_f32_16x16x32_bf16 v[110:113], v[216:219], v[152:155], v[110:113]
	v_mfma_f32_16x16x32_bf16 v[98:101], v[216:219], v[160:163], v[98:101]
	v_mfma_f32_16x16x32_bf16 v[94:97], v[188:191], v[172:175], v[94:97]
	v_mfma_f32_16x16x32_bf16 v[82:85], v[188:191], v[180:183], v[82:85]
	v_mfma_f32_16x16x32_bf16 v[90:93], v[196:199], v[172:175], v[90:93]
	v_mfma_f32_16x16x32_bf16 v[74:77], v[196:199], v[180:183], v[74:77]
	v_mfma_f32_16x16x32_bf16 v[86:89], v[204:207], v[172:175], v[86:89]
	v_mfma_f32_16x16x32_bf16 v[70:73], v[204:207], v[180:183], v[70:73]
	v_mfma_f32_16x16x32_bf16 v[78:81], v[212:215], v[172:175], v[78:81]
	v_mfma_f32_16x16x32_bf16 v[66:69], v[212:215], v[180:183], v[66:69]
	v_mfma_f32_16x16x32_bf16 v[94:97], v[192:195], v[176:179], v[94:97]
	v_mfma_f32_16x16x32_bf16 v[82:85], v[192:195], v[184:187], v[82:85]
	v_mfma_f32_16x16x32_bf16 v[90:93], v[200:203], v[176:179], v[90:93]
	v_mfma_f32_16x16x32_bf16 v[74:77], v[200:203], v[184:187], v[74:77]
	v_mfma_f32_16x16x32_bf16 v[86:89], v[208:211], v[176:179], v[86:89]
	v_mfma_f32_16x16x32_bf16 v[70:73], v[208:211], v[184:187], v[70:73]
	v_mfma_f32_16x16x32_bf16 v[78:81], v[216:219], v[176:179], v[78:81]
	v_mfma_f32_16x16x32_bf16 v[66:69], v[216:219], v[184:187], v[66:69]
	s_barrier
	s_add_i32 s2, s49, s20
	v_lshl_add_u64 v[220:221], s[34:35], 0, v[164:165]
	s_mov_b32 m0, s2
	s_nop 0
	global_load_lds_dwordx4 v[220:221], off
	s_add_i32 m0, s2, 0x2000
	s_add_u32 s2, s34, 0x80000
	v_lshl_add_u64 v[222:223], s[34:35], 0, v[168:169]
	s_addc_u32 s3, s35, 0
	s_add_i32 s28, s50, s20
	global_load_lds_dwordx4 v[222:223], off
	v_lshl_add_u64 v[224:225], s[2:3], 0, v[164:165]
	s_mov_b32 m0, s28
	s_nop 0
	global_load_lds_dwordx4 v[224:225], off
	v_lshl_add_u64 v[224:225], s[2:3], 0, v[168:169]
	s_add_i32 m0, s28, 0x2000
	s_and_b64 s[2:3], s[6:7], s[36:37]
	s_and_b64 s[2:3], s[2:3], exec
	s_cselect_b32 s2, s18, s26
	s_cselect_b32 s3, s19, s27
	s_add_u32 s2, s2, s54
	s_addc_u32 s3, s3, 0
	global_load_lds_dwordx4 v[224:225], off
	v_lshl_add_u64 v[224:225], s[2:3], 0, v[166:167]
	s_mov_b32 m0, s21
	v_lshl_add_u64 v[226:227], s[2:3], 0, v[170:171]
	global_load_lds_dwordx4 v[224:225], off
	s_mov_b32 m0, s33
	s_nop 0
	global_load_lds_dwordx4 v[226:227], off
	ds_read_b128 v[188:191], v146 offset:16384
	ds_read_b128 v[192:195], v146 offset:17408
	ds_read_b128 v[196:199], v146 offset:18432
	ds_read_b128 v[200:203], v146 offset:19456
	ds_read_b128 v[204:207], v146 offset:20480
	ds_read_b128 v[208:211], v146 offset:21504
	ds_read_b128 v[212:215], v146 offset:22528
	ds_read_b128 v[216:219], v146 offset:23552
	s_waitcnt vmcnt(8)
	s_waitcnt lgkmcnt(0)
	s_barrier
	s_waitcnt lgkmcnt(0)
	v_mfma_f32_16x16x32_bf16 v[62:65], v[188:191], v[148:151], v[62:65]
	v_mfma_f32_16x16x32_bf16 v[50:53], v[188:191], v[156:159], v[50:53]
	v_mfma_f32_16x16x32_bf16 v[58:61], v[196:199], v[148:151], v[58:61]
	v_mfma_f32_16x16x32_bf16 v[42:45], v[196:199], v[156:159], v[42:45]
	v_mfma_f32_16x16x32_bf16 v[54:57], v[204:207], v[148:151], v[54:57]
	v_mfma_f32_16x16x32_bf16 v[38:41], v[204:207], v[156:159], v[38:41]
	v_mfma_f32_16x16x32_bf16 v[46:49], v[212:215], v[148:151], v[46:49]
	v_mfma_f32_16x16x32_bf16 v[34:37], v[212:215], v[156:159], v[34:37]
	v_mfma_f32_16x16x32_bf16 v[62:65], v[192:195], v[152:155], v[62:65]
	v_mfma_f32_16x16x32_bf16 v[50:53], v[192:195], v[160:163], v[50:53]
	v_mfma_f32_16x16x32_bf16 v[58:61], v[200:203], v[152:155], v[58:61]
	v_mfma_f32_16x16x32_bf16 v[42:45], v[200:203], v[160:163], v[42:45]
	v_mfma_f32_16x16x32_bf16 v[54:57], v[208:211], v[152:155], v[54:57]
	v_mfma_f32_16x16x32_bf16 v[38:41], v[208:211], v[160:163], v[38:41]
	v_mfma_f32_16x16x32_bf16 v[46:49], v[216:219], v[152:155], v[46:49]
	v_mfma_f32_16x16x32_bf16 v[34:37], v[216:219], v[160:163], v[34:37]
	v_mfma_f32_16x16x32_bf16 v[30:33], v[188:191], v[172:175], v[30:33]
	v_mfma_f32_16x16x32_bf16 v[18:21], v[188:191], v[180:183], v[18:21]
	v_mfma_f32_16x16x32_bf16 v[26:29], v[196:199], v[172:175], v[26:29]
	v_mfma_f32_16x16x32_bf16 v[10:13], v[196:199], v[180:183], v[10:13]
	v_mfma_f32_16x16x32_bf16 v[22:25], v[204:207], v[172:175], v[22:25]
	v_mfma_f32_16x16x32_bf16 v[6:9], v[204:207], v[180:183], v[6:9]
	v_mfma_f32_16x16x32_bf16 v[14:17], v[212:215], v[172:175], v[14:17]
	v_mfma_f32_16x16x32_bf16 v[2:5], v[212:215], v[180:183], v[2:5]
	v_mfma_f32_16x16x32_bf16 v[30:33], v[192:195], v[176:179], v[30:33]
	v_mfma_f32_16x16x32_bf16 v[18:21], v[192:195], v[184:187], v[18:21]
	v_mfma_f32_16x16x32_bf16 v[26:29], v[200:203], v[176:179], v[26:29]
	v_mfma_f32_16x16x32_bf16 v[10:13], v[200:203], v[184:187], v[10:13]
	v_mfma_f32_16x16x32_bf16 v[22:25], v[208:211], v[176:179], v[22:25]
	v_mfma_f32_16x16x32_bf16 v[6:9], v[208:211], v[184:187], v[6:9]
	v_mfma_f32_16x16x32_bf16 v[14:17], v[216:219], v[176:179], v[14:17]
	v_mfma_f32_16x16x32_bf16 v[2:5], v[216:219], v[184:187], v[2:5]
	s_barrier
	s_add_u32 s2, s2, 0x80000
	s_addc_u32 s3, s3, 0
	s_mov_b32 m0, s38
	v_lshl_add_u64 v[228:229], s[2:3], 0, v[166:167]
	global_load_lds_dwordx4 v[228:229], off
	v_lshl_add_u64 v[228:229], s[2:3], 0, v[170:171]
	s_mov_b32 m0, s39
	s_nop 0
	global_load_lds_dwordx4 v[228:229], off
	s_add_i32 s28, 0, 0x18000
	v_add_u32_e32 v147, s28, v144
	s_add_i32 s29, 0, 0x1c000
	ds_read_b128 v[148:151], v147
	ds_read_b128 v[152:155], v147 offset:1024
	ds_read_b128 v[156:159], v147 offset:2048
	ds_read_b128 v[160:163], v147 offset:3072
	v_add_u32_e32 v147, s29, v144
	ds_read_b128 v[172:175], v147
	ds_read_b128 v[176:179], v147 offset:1024
	ds_read_b128 v[180:183], v147 offset:2048
	ds_read_b128 v[184:187], v147 offset:3072
	ds_read_b128 v[188:191], v146 offset:32768
	ds_read_b128 v[192:195], v146 offset:33792
	ds_read_b128 v[196:199], v146 offset:34816
	ds_read_b128 v[200:203], v146 offset:35840
	ds_read_b128 v[204:207], v146 offset:36864
	ds_read_b128 v[208:211], v146 offset:37888
	ds_read_b128 v[212:215], v146 offset:38912
	ds_read_b128 v[216:219], v146 offset:39936
	s_waitcnt vmcnt(8)
	s_waitcnt lgkmcnt(0)
	s_barrier
	s_waitcnt lgkmcnt(0)
	v_mfma_f32_16x16x32_bf16 v[126:129], v[188:191], v[148:151], v[126:129]
	v_mfma_f32_16x16x32_bf16 v[114:117], v[188:191], v[156:159], v[114:117]
	v_mfma_f32_16x16x32_bf16 v[122:125], v[196:199], v[148:151], v[122:125]
	v_mfma_f32_16x16x32_bf16 v[106:109], v[196:199], v[156:159], v[106:109]
	v_mfma_f32_16x16x32_bf16 v[118:121], v[204:207], v[148:151], v[118:121]
	v_mfma_f32_16x16x32_bf16 v[102:105], v[204:207], v[156:159], v[102:105]
	v_mfma_f32_16x16x32_bf16 v[110:113], v[212:215], v[148:151], v[110:113]
	v_mfma_f32_16x16x32_bf16 v[98:101], v[212:215], v[156:159], v[98:101]
	v_mfma_f32_16x16x32_bf16 v[126:129], v[192:195], v[152:155], v[126:129]
	v_mfma_f32_16x16x32_bf16 v[114:117], v[192:195], v[160:163], v[114:117]
	v_mfma_f32_16x16x32_bf16 v[122:125], v[200:203], v[152:155], v[122:125]
	v_mfma_f32_16x16x32_bf16 v[106:109], v[200:203], v[160:163], v[106:109]
	v_mfma_f32_16x16x32_bf16 v[118:121], v[208:211], v[152:155], v[118:121]
	v_mfma_f32_16x16x32_bf16 v[102:105], v[208:211], v[160:163], v[102:105]
	v_mfma_f32_16x16x32_bf16 v[110:113], v[216:219], v[152:155], v[110:113]
	v_mfma_f32_16x16x32_bf16 v[98:101], v[216:219], v[160:163], v[98:101]
	v_mfma_f32_16x16x32_bf16 v[94:97], v[188:191], v[172:175], v[94:97]
	v_mfma_f32_16x16x32_bf16 v[82:85], v[188:191], v[180:183], v[82:85]
	v_mfma_f32_16x16x32_bf16 v[90:93], v[196:199], v[172:175], v[90:93]
	v_mfma_f32_16x16x32_bf16 v[74:77], v[196:199], v[180:183], v[74:77]
	v_mfma_f32_16x16x32_bf16 v[86:89], v[204:207], v[172:175], v[86:89]
	v_mfma_f32_16x16x32_bf16 v[70:73], v[204:207], v[180:183], v[70:73]
	v_mfma_f32_16x16x32_bf16 v[78:81], v[212:215], v[172:175], v[78:81]
	v_mfma_f32_16x16x32_bf16 v[66:69], v[212:215], v[180:183], v[66:69]
	v_mfma_f32_16x16x32_bf16 v[94:97], v[192:195], v[176:179], v[94:97]
	v_mfma_f32_16x16x32_bf16 v[82:85], v[192:195], v[184:187], v[82:85]
	v_mfma_f32_16x16x32_bf16 v[90:93], v[200:203], v[176:179], v[90:93]
	v_mfma_f32_16x16x32_bf16 v[74:77], v[200:203], v[184:187], v[74:77]
	v_mfma_f32_16x16x32_bf16 v[86:89], v[208:211], v[176:179], v[86:89]
	v_mfma_f32_16x16x32_bf16 v[70:73], v[208:211], v[184:187], v[70:73]
	v_mfma_f32_16x16x32_bf16 v[78:81], v[216:219], v[176:179], v[78:81]
	v_mfma_f32_16x16x32_bf16 v[66:69], v[216:219], v[184:187], v[66:69]
	s_barrier
	s_add_i32 s2, s28, s20
	v_lshl_add_u64 v[220:221], v[220:221], 0, s[10:11]
	s_mov_b32 m0, s2
	s_nop 0
	global_load_lds_dwordx4 v[220:221], off
	s_add_i32 m0, s2, 0x2000
	s_add_u32 s2, s34, 0x80080
	v_lshl_add_u64 v[220:221], v[222:223], 0, s[10:11]
	s_addc_u32 s3, s35, 0
	s_add_i32 s28, s29, s20
	global_load_lds_dwordx4 v[220:221], off
	v_lshl_add_u64 v[220:221], s[2:3], 0, v[164:165]
	s_mov_b32 m0, s28
	s_nop 0
	global_load_lds_dwordx4 v[220:221], off
	v_lshl_add_u64 v[220:221], s[2:3], 0, v[168:169]
	s_add_i32 m0, s28, 0x2000
	s_nop 0
	global_load_lds_dwordx4 v[220:221], off
	v_lshl_add_u64 v[220:221], v[224:225], 0, s[10:11]
	s_mov_b32 m0, s43
	s_nop 0
	global_load_lds_dwordx4 v[220:221], off
	v_lshl_add_u64 v[220:221], v[226:227], 0, s[10:11]
	s_mov_b32 m0, s48
	s_nop 0
	global_load_lds_dwordx4 v[220:221], off
	ds_read_b128 v[188:191], v146 offset:49152
	ds_read_b128 v[192:195], v146 offset:50176
	ds_read_b128 v[196:199], v146 offset:51200
	ds_read_b128 v[200:203], v146 offset:52224
	ds_read_b128 v[204:207], v146 offset:53248
	ds_read_b128 v[208:211], v146 offset:54272
	ds_read_b128 v[212:215], v146 offset:55296
	ds_read_b128 v[216:219], v146 offset:56320
	s_waitcnt vmcnt(8)
	s_waitcnt lgkmcnt(0)
	s_barrier
	s_waitcnt lgkmcnt(0)
	v_mfma_f32_16x16x32_bf16 v[62:65], v[188:191], v[148:151], v[62:65]
	v_mfma_f32_16x16x32_bf16 v[50:53], v[188:191], v[156:159], v[50:53]
	v_mfma_f32_16x16x32_bf16 v[58:61], v[196:199], v[148:151], v[58:61]
	v_mfma_f32_16x16x32_bf16 v[42:45], v[196:199], v[156:159], v[42:45]
	v_mfma_f32_16x16x32_bf16 v[54:57], v[204:207], v[148:151], v[54:57]
	v_mfma_f32_16x16x32_bf16 v[38:41], v[204:207], v[156:159], v[38:41]
	v_mfma_f32_16x16x32_bf16 v[46:49], v[212:215], v[148:151], v[46:49]
	v_mfma_f32_16x16x32_bf16 v[34:37], v[212:215], v[156:159], v[34:37]
	v_mfma_f32_16x16x32_bf16 v[62:65], v[192:195], v[152:155], v[62:65]
	v_mfma_f32_16x16x32_bf16 v[50:53], v[192:195], v[160:163], v[50:53]
	v_mfma_f32_16x16x32_bf16 v[58:61], v[200:203], v[152:155], v[58:61]
	v_mfma_f32_16x16x32_bf16 v[42:45], v[200:203], v[160:163], v[42:45]
	v_mfma_f32_16x16x32_bf16 v[54:57], v[208:211], v[152:155], v[54:57]
	v_mfma_f32_16x16x32_bf16 v[38:41], v[208:211], v[160:163], v[38:41]
	v_mfma_f32_16x16x32_bf16 v[46:49], v[216:219], v[152:155], v[46:49]
	v_mfma_f32_16x16x32_bf16 v[34:37], v[216:219], v[160:163], v[34:37]
	v_mfma_f32_16x16x32_bf16 v[30:33], v[188:191], v[172:175], v[30:33]
	v_mfma_f32_16x16x32_bf16 v[18:21], v[188:191], v[180:183], v[18:21]
	v_mfma_f32_16x16x32_bf16 v[26:29], v[196:199], v[172:175], v[26:29]
	v_mfma_f32_16x16x32_bf16 v[10:13], v[196:199], v[180:183], v[10:13]
	v_mfma_f32_16x16x32_bf16 v[22:25], v[204:207], v[172:175], v[22:25]
	v_mfma_f32_16x16x32_bf16 v[6:9], v[204:207], v[180:183], v[6:9]
	v_mfma_f32_16x16x32_bf16 v[14:17], v[212:215], v[172:175], v[14:17]
	v_mfma_f32_16x16x32_bf16 v[2:5], v[212:215], v[180:183], v[2:5]
	v_mfma_f32_16x16x32_bf16 v[30:33], v[192:195], v[176:179], v[30:33]
	v_mfma_f32_16x16x32_bf16 v[18:21], v[192:195], v[184:187], v[18:21]
	v_mfma_f32_16x16x32_bf16 v[26:29], v[200:203], v[176:179], v[26:29]
	v_mfma_f32_16x16x32_bf16 v[10:13], v[200:203], v[184:187], v[10:13]
	v_mfma_f32_16x16x32_bf16 v[22:25], v[208:211], v[176:179], v[22:25]
	v_mfma_f32_16x16x32_bf16 v[6:9], v[208:211], v[184:187], v[6:9]
	v_mfma_f32_16x16x32_bf16 v[14:17], v[216:219], v[176:179], v[14:17]
	v_mfma_f32_16x16x32_bf16 v[2:5], v[216:219], v[184:187], v[2:5]
	s_barrier
	s_add_i32 s53, s53, 2
	s_cmp_gt_u32 s53, 29
	s_mov_b64 s[28:29], s[30:31]
	s_cbranch_scc0 .LBB0_346
	s_and_b64 vcc, exec, s[12:13]
	s_cbranch_vccz .LBB0_349
	s_barrier

.LBB0_712:
	s_mov_b64 s[72:73], s[56:57]
	s_add_u32 s2, s69, s72
	s_addc_u32 s74, s70, s73
	s_add_u32 s56, s72, 0x100
	s_addc_u32 s57, s73, 0
	s_cmpk_eq_i32 s72, 0xf00
	s_cselect_b64 s[58:59], -1, 0
	s_and_b64 s[60:61], s[58:59], exec
	s_cselect_b32 s61, s35, s74
	s_cselect_b32 s60, s68, s2
	s_cselect_b32 s2, 0, s56
	v_lshl_add_u64 v[4:5], v[136:137], 0, s[72:73]
	s_add_i32 m0, s42, 0xc000
	s_nop 0
	global_load_lds_dwordx4 v[4:5], off
	v_lshl_add_u64 v[4:5], v[134:135], 0, s[72:73]
	s_add_i32 m0, s42, 0xe000
	s_nop 0
	global_load_lds_dwordx4 v[4:5], off
	ds_read_b128 v[140:143], v205
	ds_read_b128 v[144:147], v205 offset:1024
	ds_read_b128 v[148:151], v205 offset:2048
	ds_read_b128 v[152:155], v205 offset:3072
	ds_read_b128 v[182:185], v207
	ds_read_b128 v[186:189], v207 offset:1024
	ds_read_b128 v[196:199], v207 offset:2048
	ds_read_b128 v[212:215], v207 offset:3072
	ds_read_b128 v[216:219], v210
	ds_read_b128 v[220:223], v210 offset:1024
	ds_read_b128 v[224:227], v210 offset:2048
	ds_read_b128 v[228:231], v210 offset:3072
	ds_read_b128 v[232:235], v210 offset:4096
	ds_read_b128 v[236:239], v210 offset:5120
	ds_read_b128 v[244:247], v210 offset:6144
	ds_read_b128 v[248:251], v210 offset:7168
	s_waitcnt vmcnt(8)
	s_waitcnt lgkmcnt(0)
	s_barrier
	s_waitcnt lgkmcnt(0)
	v_mfma_f32_16x16x32_bf16 v[130:133], v[140:143], v[216:219], v[130:133]
	v_mfma_f32_16x16x32_bf16 v[126:129], v[148:151], v[216:219], v[126:129]
	v_mfma_f32_16x16x32_bf16 v[114:117], v[140:143], v[224:227], v[114:117]
	v_mfma_f32_16x16x32_bf16 v[110:113], v[148:151], v[224:227], v[110:113]
	v_mfma_f32_16x16x32_bf16 v[98:101], v[140:143], v[232:235], v[98:101]
	v_mfma_f32_16x16x32_bf16 v[94:97], v[148:151], v[232:235], v[94:97]
	v_mfma_f32_16x16x32_bf16 v[82:85], v[140:143], v[244:247], v[82:85]
	v_mfma_f32_16x16x32_bf16 v[78:81], v[148:151], v[244:247], v[78:81]
	v_mfma_f32_16x16x32_bf16 v[130:133], v[144:147], v[220:223], v[130:133]
	v_mfma_f32_16x16x32_bf16 v[126:129], v[152:155], v[220:223], v[126:129]
	v_mfma_f32_16x16x32_bf16 v[114:117], v[144:147], v[228:231], v[114:117]
	v_mfma_f32_16x16x32_bf16 v[110:113], v[152:155], v[228:231], v[110:113]
	v_mfma_f32_16x16x32_bf16 v[98:101], v[144:147], v[236:239], v[98:101]
	v_mfma_f32_16x16x32_bf16 v[94:97], v[152:155], v[236:239], v[94:97]
	v_mfma_f32_16x16x32_bf16 v[82:85], v[144:147], v[248:251], v[82:85]
	v_mfma_f32_16x16x32_bf16 v[78:81], v[152:155], v[248:251], v[78:81]
	v_mfma_f32_16x16x32_bf16 v[122:125], v[182:185], v[216:219], v[122:125]
	v_mfma_f32_16x16x32_bf16 v[118:121], v[196:199], v[216:219], v[118:121]
	v_mfma_f32_16x16x32_bf16 v[106:109], v[182:185], v[224:227], v[106:109]
	v_mfma_f32_16x16x32_bf16 v[102:105], v[196:199], v[224:227], v[102:105]
	v_mfma_f32_16x16x32_bf16 v[90:93], v[182:185], v[232:235], v[90:93]
	v_mfma_f32_16x16x32_bf16 v[86:89], v[196:199], v[232:235], v[86:89]
	v_mfma_f32_16x16x32_bf16 v[74:77], v[182:185], v[244:247], v[74:77]
	v_mfma_f32_16x16x32_bf16 v[70:73], v[196:199], v[244:247], v[70:73]
	v_mfma_f32_16x16x32_bf16 v[122:125], v[186:189], v[220:223], v[122:125]
	v_mfma_f32_16x16x32_bf16 v[118:121], v[212:215], v[220:223], v[118:121]
	v_mfma_f32_16x16x32_bf16 v[106:109], v[186:189], v[228:231], v[106:109]
	v_mfma_f32_16x16x32_bf16 v[102:105], v[212:215], v[228:231], v[102:105]
	v_mfma_f32_16x16x32_bf16 v[90:93], v[186:189], v[236:239], v[90:93]
	v_mfma_f32_16x16x32_bf16 v[86:89], v[212:215], v[236:239], v[86:89]
	v_mfma_f32_16x16x32_bf16 v[74:77], v[186:189], v[248:251], v[74:77]
	v_mfma_f32_16x16x32_bf16 v[70:73], v[212:215], v[248:251], v[70:73]
	s_barrier
	s_add_i32 s72, s63, s15
	v_lshl_add_u64 v[156:157], s[60:61], 0, v[160:161]
	s_mov_b32 m0, s72
	s_nop 0
	global_load_lds_dwordx4 v[156:157], off
	s_add_i32 m0, s72, 0x2000
	s_add_u32 s72, s60, 0x80000
	v_lshl_add_u64 v[178:179], s[60:61], 0, v[164:165]
	s_addc_u32 s73, s61, 0
	s_add_i32 s74, s64, s15
	global_load_lds_dwordx4 v[178:179], off
	v_lshl_add_u64 v[4:5], s[72:73], 0, v[160:161]
	s_mov_b32 m0, s74
	s_nop 0
	global_load_lds_dwordx4 v[4:5], off
	v_lshl_add_u64 v[4:5], s[72:73], 0, v[164:165]
	s_add_i32 m0, s74, 0x2000
	s_and_b64 s[72:73], s[10:11], s[58:59]
	s_and_b64 s[72:73], s[72:73], exec
	s_cselect_b32 s72, s38, s54
	s_cselect_b32 s73, s39, s55
	s_add_u32 s72, s72, s2
	s_addc_u32 s73, s73, 0
	global_load_lds_dwordx4 v[4:5], off
	v_lshl_add_u64 v[192:193], s[72:73], 0, v[158:159]
	s_mov_b32 m0, s42
	v_lshl_add_u64 v[202:203], s[72:73], 0, v[162:163]
	global_load_lds_dwordx4 v[192:193], off
	s_mov_b32 m0, s43
	s_nop 0
	global_load_lds_dwordx4 v[202:203], off
	ds_read_b128 v[216:219], v210 offset:16384
	ds_read_b128 v[220:223], v210 offset:17408
	ds_read_b128 v[224:227], v210 offset:18432
	ds_read_b128 v[228:231], v210 offset:19456
	ds_read_b128 v[232:235], v210 offset:20480
	ds_read_b128 v[236:239], v210 offset:21504
	ds_read_b128 v[244:247], v210 offset:22528
	ds_read_b128 v[248:251], v210 offset:23552
	s_waitcnt vmcnt(8)
	s_waitcnt lgkmcnt(0)
	s_barrier
	s_waitcnt lgkmcnt(0)
	v_mfma_f32_16x16x32_bf16 v[66:69], v[140:143], v[216:219], v[66:69]
	v_mfma_f32_16x16x32_bf16 v[62:65], v[148:151], v[216:219], v[62:65]
	v_mfma_f32_16x16x32_bf16 v[50:53], v[140:143], v[224:227], v[50:53]
	v_mfma_f32_16x16x32_bf16 v[46:49], v[148:151], v[224:227], v[46:49]
	v_mfma_f32_16x16x32_bf16 v[34:37], v[140:143], v[232:235], v[34:37]
	v_mfma_f32_16x16x32_bf16 v[30:33], v[148:151], v[232:235], v[30:33]
	v_mfma_f32_16x16x32_bf16 v[18:21], v[140:143], v[244:247], v[18:21]
	v_mfma_f32_16x16x32_bf16 v[14:17], v[148:151], v[244:247], v[14:17]
	v_mfma_f32_16x16x32_bf16 v[66:69], v[144:147], v[220:223], v[66:69]
	v_mfma_f32_16x16x32_bf16 v[62:65], v[152:155], v[220:223], v[62:65]
	v_mfma_f32_16x16x32_bf16 v[50:53], v[144:147], v[228:231], v[50:53]
	v_mfma_f32_16x16x32_bf16 v[46:49], v[152:155], v[228:231], v[46:49]
	v_mfma_f32_16x16x32_bf16 v[34:37], v[144:147], v[236:239], v[34:37]
	v_mfma_f32_16x16x32_bf16 v[30:33], v[152:155], v[236:239], v[30:33]
	v_mfma_f32_16x16x32_bf16 v[18:21], v[144:147], v[248:251], v[18:21]
	v_mfma_f32_16x16x32_bf16 v[14:17], v[152:155], v[248:251], v[14:17]
	v_mfma_f32_16x16x32_bf16 v[58:61], v[182:185], v[216:219], v[58:61]
	v_mfma_f32_16x16x32_bf16 v[54:57], v[196:199], v[216:219], v[54:57]
	v_mfma_f32_16x16x32_bf16 v[42:45], v[182:185], v[224:227], v[42:45]
	v_mfma_f32_16x16x32_bf16 v[38:41], v[196:199], v[224:227], v[38:41]
	v_mfma_f32_16x16x32_bf16 v[26:29], v[182:185], v[232:235], v[26:29]
	v_mfma_f32_16x16x32_bf16 v[22:25], v[196:199], v[232:235], v[22:25]
	v_mfma_f32_16x16x32_bf16 v[10:13], v[182:185], v[244:247], v[10:13]
	v_mfma_f32_16x16x32_bf16 v[4:7], v[196:199], v[244:247], v[6:9]
	v_mfma_f32_16x16x32_bf16 v[58:61], v[186:189], v[220:223], v[58:61]
	v_mfma_f32_16x16x32_bf16 v[54:57], v[212:215], v[220:223], v[54:57]
	v_mfma_f32_16x16x32_bf16 v[42:45], v[186:189], v[228:231], v[42:45]
	v_mfma_f32_16x16x32_bf16 v[38:41], v[212:215], v[228:231], v[38:41]
	v_mfma_f32_16x16x32_bf16 v[26:29], v[186:189], v[236:239], v[26:29]
	v_mfma_f32_16x16x32_bf16 v[22:25], v[212:215], v[236:239], v[22:25]
	v_mfma_f32_16x16x32_bf16 v[10:13], v[186:189], v[248:251], v[10:13]
	v_mfma_f32_16x16x32_bf16 v[4:7], v[212:215], v[248:251], v[4:7]
	s_barrier
	s_add_u32 s72, s72, 0x80000
	s_addc_u32 s73, s73, 0
	s_mov_b32 m0, s48
	v_lshl_add_u64 v[8:9], s[72:73], 0, v[158:159]
	global_load_lds_dwordx4 v[8:9], off
	v_lshl_add_u64 v[8:9], s[72:73], 0, v[162:163]
	s_mov_b32 m0, s49
	s_nop 0
	global_load_lds_dwordx4 v[8:9], off
	s_add_i32 s2, 0, 0x18000
	v_add_u32_e32 v3, s2, v177
	s_add_i32 s74, 0, 0x1c000
	ds_read_b128 v[140:143], v3
	ds_read_b128 v[144:147], v3 offset:1024
	ds_read_b128 v[148:151], v3 offset:2048
	ds_read_b128 v[152:155], v3 offset:3072
	v_add_u32_e32 v3, s74, v177
	ds_read_b128 v[182:185], v3
	ds_read_b128 v[186:189], v3 offset:1024
	ds_read_b128 v[196:199], v3 offset:2048
	ds_read_b128 v[212:215], v3 offset:3072
	ds_read_b128 v[216:219], v210 offset:32768
	ds_read_b128 v[220:223], v210 offset:33792
	ds_read_b128 v[224:227], v210 offset:34816
	ds_read_b128 v[228:231], v210 offset:35840
	ds_read_b128 v[232:235], v210 offset:36864
	ds_read_b128 v[236:239], v210 offset:37888
	ds_read_b128 v[244:247], v210 offset:38912
	ds_read_b128 v[248:251], v210 offset:39936
	s_waitcnt vmcnt(8)
	s_waitcnt lgkmcnt(0)
	s_barrier
	s_waitcnt lgkmcnt(0)
	v_mfma_f32_16x16x32_bf16 v[130:133], v[140:143], v[216:219], v[130:133]
	v_mfma_f32_16x16x32_bf16 v[126:129], v[148:151], v[216:219], v[126:129]
	v_mfma_f32_16x16x32_bf16 v[114:117], v[140:143], v[224:227], v[114:117]
	v_mfma_f32_16x16x32_bf16 v[110:113], v[148:151], v[224:227], v[110:113]
	v_mfma_f32_16x16x32_bf16 v[98:101], v[140:143], v[232:235], v[98:101]
	v_mfma_f32_16x16x32_bf16 v[94:97], v[148:151], v[232:235], v[94:97]
	v_mfma_f32_16x16x32_bf16 v[82:85], v[140:143], v[244:247], v[82:85]
	v_mfma_f32_16x16x32_bf16 v[78:81], v[148:151], v[244:247], v[78:81]
	v_mfma_f32_16x16x32_bf16 v[130:133], v[144:147], v[220:223], v[130:133]
	v_mfma_f32_16x16x32_bf16 v[126:129], v[152:155], v[220:223], v[126:129]
	v_mfma_f32_16x16x32_bf16 v[114:117], v[144:147], v[228:231], v[114:117]
	v_mfma_f32_16x16x32_bf16 v[110:113], v[152:155], v[228:231], v[110:113]
	v_mfma_f32_16x16x32_bf16 v[98:101], v[144:147], v[236:239], v[98:101]
	v_mfma_f32_16x16x32_bf16 v[94:97], v[152:155], v[236:239], v[94:97]
	v_mfma_f32_16x16x32_bf16 v[82:85], v[144:147], v[248:251], v[82:85]
	v_mfma_f32_16x16x32_bf16 v[78:81], v[152:155], v[248:251], v[78:81]
	v_mfma_f32_16x16x32_bf16 v[122:125], v[182:185], v[216:219], v[122:125]
	v_mfma_f32_16x16x32_bf16 v[118:121], v[196:199], v[216:219], v[118:121]
	v_mfma_f32_16x16x32_bf16 v[106:109], v[182:185], v[224:227], v[106:109]
	v_mfma_f32_16x16x32_bf16 v[102:105], v[196:199], v[224:227], v[102:105]
	v_mfma_f32_16x16x32_bf16 v[90:93], v[182:185], v[232:235], v[90:93]
	v_mfma_f32_16x16x32_bf16 v[86:89], v[196:199], v[232:235], v[86:89]
	v_mfma_f32_16x16x32_bf16 v[74:77], v[182:185], v[244:247], v[74:77]
	v_mfma_f32_16x16x32_bf16 v[70:73], v[196:199], v[244:247], v[70:73]
	v_mfma_f32_16x16x32_bf16 v[122:125], v[186:189], v[220:223], v[122:125]
	v_mfma_f32_16x16x32_bf16 v[118:121], v[212:215], v[220:223], v[118:121]
	v_mfma_f32_16x16x32_bf16 v[106:109], v[186:189], v[228:231], v[106:109]
	v_mfma_f32_16x16x32_bf16 v[102:105], v[212:215], v[228:231], v[102:105]
	v_mfma_f32_16x16x32_bf16 v[90:93], v[186:189], v[236:239], v[90:93]
	v_mfma_f32_16x16x32_bf16 v[86:89], v[212:215], v[236:239], v[86:89]
	v_mfma_f32_16x16x32_bf16 v[74:77], v[186:189], v[248:251], v[74:77]
	v_mfma_f32_16x16x32_bf16 v[70:73], v[212:215], v[248:251], v[70:73]
	s_barrier
	s_add_i32 s2, s2, s15
	v_lshl_add_u64 v[8:9], v[156:157], 0, s[28:29]
	s_mov_b32 m0, s2
	s_nop 0
	global_load_lds_dwordx4 v[8:9], off
	s_add_i32 m0, s2, 0x2000
	s_add_u32 s60, s60, 0x80080
	v_lshl_add_u64 v[8:9], v[178:179], 0, s[28:29]
	s_addc_u32 s61, s61, 0
	s_add_i32 s2, s74, s15
	global_load_lds_dwordx4 v[8:9], off
	v_lshl_add_u64 v[8:9], s[60:61], 0, v[160:161]
	s_mov_b32 m0, s2
	s_nop 0
	global_load_lds_dwordx4 v[8:9], off
	v_lshl_add_u64 v[8:9], s[60:61], 0, v[164:165]
	s_add_i32 m0, s2, 0x2000
	s_nop 0
	global_load_lds_dwordx4 v[8:9], off
	v_lshl_add_u64 v[8:9], v[192:193], 0, s[28:29]
	s_mov_b32 m0, s51
	s_nop 0
	global_load_lds_dwordx4 v[8:9], off
	v_lshl_add_u64 v[8:9], v[202:203], 0, s[28:29]
	s_mov_b32 m0, s52
	s_nop 0
	global_load_lds_dwordx4 v[8:9], off
	ds_read_b128 v[216:219], v210 offset:49152
	ds_read_b128 v[220:223], v210 offset:50176
	ds_read_b128 v[224:227], v210 offset:51200
	ds_read_b128 v[228:231], v210 offset:52224
	ds_read_b128 v[232:235], v210 offset:53248
	ds_read_b128 v[236:239], v210 offset:54272
	ds_read_b128 v[244:247], v210 offset:55296
	ds_read_b128 v[248:251], v210 offset:56320
	s_waitcnt vmcnt(8)
	s_waitcnt lgkmcnt(0)
	s_barrier
	s_waitcnt lgkmcnt(0)
	v_mfma_f32_16x16x32_bf16 v[66:69], v[140:143], v[216:219], v[66:69]
	v_mfma_f32_16x16x32_bf16 v[62:65], v[148:151], v[216:219], v[62:65]
	v_mfma_f32_16x16x32_bf16 v[50:53], v[140:143], v[224:227], v[50:53]
	v_mfma_f32_16x16x32_bf16 v[46:49], v[148:151], v[224:227], v[46:49]
	v_mfma_f32_16x16x32_bf16 v[34:37], v[140:143], v[232:235], v[34:37]
	v_mfma_f32_16x16x32_bf16 v[30:33], v[148:151], v[232:235], v[30:33]
	v_mfma_f32_16x16x32_bf16 v[18:21], v[140:143], v[244:247], v[18:21]
	v_mfma_f32_16x16x32_bf16 v[14:17], v[148:151], v[244:247], v[14:17]
	v_mfma_f32_16x16x32_bf16 v[66:69], v[144:147], v[220:223], v[66:69]
	v_mfma_f32_16x16x32_bf16 v[62:65], v[152:155], v[220:223], v[62:65]
	v_mfma_f32_16x16x32_bf16 v[50:53], v[144:147], v[228:231], v[50:53]
	v_mfma_f32_16x16x32_bf16 v[46:49], v[152:155], v[228:231], v[46:49]
	v_mfma_f32_16x16x32_bf16 v[34:37], v[144:147], v[236:239], v[34:37]
	v_mfma_f32_16x16x32_bf16 v[30:33], v[152:155], v[236:239], v[30:33]
	v_mfma_f32_16x16x32_bf16 v[18:21], v[144:147], v[248:251], v[18:21]
	v_mfma_f32_16x16x32_bf16 v[14:17], v[152:155], v[248:251], v[14:17]
	v_mfma_f32_16x16x32_bf16 v[58:61], v[182:185], v[216:219], v[58:61]
	v_mfma_f32_16x16x32_bf16 v[54:57], v[196:199], v[216:219], v[54:57]
	v_mfma_f32_16x16x32_bf16 v[42:45], v[182:185], v[224:227], v[42:45]
	v_mfma_f32_16x16x32_bf16 v[38:41], v[196:199], v[224:227], v[38:41]
	v_mfma_f32_16x16x32_bf16 v[26:29], v[182:185], v[232:235], v[26:29]
	v_mfma_f32_16x16x32_bf16 v[22:25], v[196:199], v[232:235], v[22:25]
	v_mfma_f32_16x16x32_bf16 v[8:11], v[182:185], v[244:247], v[10:13]
	v_mfma_f32_16x16x32_bf16 v[4:7], v[196:199], v[244:247], v[4:7]
	v_mfma_f32_16x16x32_bf16 v[58:61], v[186:189], v[220:223], v[58:61]
	v_mfma_f32_16x16x32_bf16 v[54:57], v[212:215], v[220:223], v[54:57]
	v_mfma_f32_16x16x32_bf16 v[42:45], v[186:189], v[228:231], v[42:45]
	v_mfma_f32_16x16x32_bf16 v[38:41], v[212:215], v[228:231], v[38:41]
	v_mfma_f32_16x16x32_bf16 v[26:29], v[186:189], v[236:239], v[26:29]
	v_mfma_f32_16x16x32_bf16 v[22:25], v[212:215], v[236:239], v[22:25]
	v_mfma_f32_16x16x32_bf16 v[10:13], v[186:189], v[248:251], v[8:11]
	v_mfma_f32_16x16x32_bf16 v[6:9], v[212:215], v[248:251], v[4:7]
	s_barrier
	s_add_i32 s2, s71, 4
	s_and_b32 s2, s2, 6
	s_cmp_lg_u32 s2, 0
	s_cselect_b64 s[60:61], -1, 0
	s_or_b64 s[58:59], s[58:59], s[60:61]
	s_and_b64 vcc, exec, s[58:59]
	s_cbranch_vccnz .LBB0_711
	ds_read2st64_b32 v[4:5], v138 offset1:1
	ds_read2st64_b32 v[140:141], v138 offset0:2 offset1:3
	ds_read2st64_b32 v[142:143], v138 offset0:8 offset1:9
	ds_read2st64_b32 v[144:145], v138 offset0:10 offset1:11
	s_waitcnt lgkmcnt(0)
	v_pk_mul_f32 v[132:133], v[132:133], v[4:5] op_sel_hi:[1,0]
	v_pk_mul_f32 v[130:131], v[130:131], v[4:5] op_sel_hi:[1,0]
	v_pk_mul_f32 v[128:129], v[128:129], v[4:5] op_sel_hi:[1,0]
	v_pk_mul_f32 v[126:127], v[126:127], v[4:5] op_sel_hi:[1,0]
	v_pk_mul_f32 v[124:125], v[124:125], v[4:5] op_sel_hi:[1,0]
	v_pk_mul_f32 v[122:123], v[122:123], v[4:5] op_sel_hi:[1,0]
	v_pk_mul_f32 v[120:121], v[120:121], v[4:5] op_sel_hi:[1,0]
	v_pk_mul_f32 v[118:119], v[118:119], v[4:5] op_sel_hi:[1,0]
	v_mov_b32_e32 v4, v5
	v_pk_mul_f32 v[116:117], v[116:117], v[4:5] op_sel_hi:[1,0]
	v_pk_mul_f32 v[114:115], v[114:115], v[4:5] op_sel_hi:[1,0]
	v_pk_mul_f32 v[112:113], v[112:113], v[4:5] op_sel_hi:[1,0]
	v_pk_mul_f32 v[110:111], v[110:111], v[4:5] op_sel_hi:[1,0]
	v_pk_mul_f32 v[108:109], v[108:109], v[4:5] op_sel_hi:[1,0]
	v_pk_mul_f32 v[106:107], v[106:107], v[4:5] op_sel_hi:[1,0]
	v_pk_mul_f32 v[104:105], v[104:105], v[4:5] op_sel_hi:[1,0]
	v_pk_mul_f32 v[102:103], v[102:103], v[4:5] op_sel_hi:[1,0]
	v_mov_b32_e32 v4, v141
	v_pk_mul_f32 v[84:85], v[84:85], v[4:5] op_sel_hi:[1,0]
	v_pk_mul_f32 v[82:83], v[82:83], v[4:5] op_sel_hi:[1,0]
	v_pk_mul_f32 v[80:81], v[80:81], v[4:5] op_sel_hi:[1,0]
	v_pk_mul_f32 v[78:79], v[78:79], v[4:5] op_sel_hi:[1,0]
	v_pk_mul_f32 v[76:77], v[76:77], v[4:5] op_sel_hi:[1,0]
	v_pk_mul_f32 v[74:75], v[74:75], v[4:5] op_sel_hi:[1,0]
	v_pk_mul_f32 v[72:73], v[72:73], v[4:5] op_sel_hi:[1,0]
	v_pk_mul_f32 v[70:71], v[70:71], v[4:5] op_sel_hi:[1,0]
	v_mov_b32_e32 v4, v143
	v_pk_mul_f32 v[52:53], v[52:53], v[4:5] op_sel_hi:[1,0]
	v_pk_mul_f32 v[50:51], v[50:51], v[4:5] op_sel_hi:[1,0]
	v_pk_mul_f32 v[48:49], v[48:49], v[4:5] op_sel_hi:[1,0]
	v_pk_mul_f32 v[46:47], v[46:47], v[4:5] op_sel_hi:[1,0]
	v_pk_mul_f32 v[44:45], v[44:45], v[4:5] op_sel_hi:[1,0]
	v_pk_mul_f32 v[42:43], v[42:43], v[4:5] op_sel_hi:[1,0]
	v_pk_mul_f32 v[40:41], v[40:41], v[4:5] op_sel_hi:[1,0]
	v_pk_mul_f32 v[38:39], v[38:39], v[4:5] op_sel_hi:[1,0]
	v_mov_b32_e32 v4, v145
	v_pk_mul_f32 v[100:101], v[100:101], v[140:141] op_sel_hi:[1,0]
	v_pk_mul_f32 v[98:99], v[98:99], v[140:141] op_sel_hi:[1,0]
	v_pk_mul_f32 v[96:97], v[96:97], v[140:141] op_sel_hi:[1,0]
	v_pk_mul_f32 v[94:95], v[94:95], v[140:141] op_sel_hi:[1,0]
	v_pk_mul_f32 v[92:93], v[92:93], v[140:141] op_sel_hi:[1,0]
	v_pk_mul_f32 v[90:91], v[90:91], v[140:141] op_sel_hi:[1,0]
	v_pk_mul_f32 v[88:89], v[88:89], v[140:141] op_sel_hi:[1,0]
	v_pk_mul_f32 v[86:87], v[86:87], v[140:141] op_sel_hi:[1,0]
	v_pk_mul_f32 v[68:69], v[68:69], v[142:143] op_sel_hi:[1,0]
	v_pk_mul_f32 v[66:67], v[66:67], v[142:143] op_sel_hi:[1,0]
	v_pk_mul_f32 v[64:65], v[64:65], v[142:143] op_sel_hi:[1,0]
	v_pk_mul_f32 v[62:63], v[62:63], v[142:143] op_sel_hi:[1,0]
	v_pk_mul_f32 v[60:61], v[60:61], v[142:143] op_sel_hi:[1,0]
	v_pk_mul_f32 v[58:59], v[58:59], v[142:143] op_sel_hi:[1,0]
	v_pk_mul_f32 v[56:57], v[56:57], v[142:143] op_sel_hi:[1,0]
	v_pk_mul_f32 v[54:55], v[54:55], v[142:143] op_sel_hi:[1,0]
	v_pk_mul_f32 v[36:37], v[36:37], v[144:145] op_sel_hi:[1,0]
	v_pk_mul_f32 v[34:35], v[34:35], v[144:145] op_sel_hi:[1,0]
	v_pk_mul_f32 v[32:33], v[32:33], v[144:145] op_sel_hi:[1,0]
	v_pk_mul_f32 v[30:31], v[30:31], v[144:145] op_sel_hi:[1,0]
	v_pk_mul_f32 v[28:29], v[28:29], v[144:145] op_sel_hi:[1,0]
	v_pk_mul_f32 v[26:27], v[26:27], v[144:145] op_sel_hi:[1,0]
	v_pk_mul_f32 v[24:25], v[24:25], v[144:145] op_sel_hi:[1,0]
	v_pk_mul_f32 v[22:23], v[22:23], v[144:145] op_sel_hi:[1,0]
	v_pk_mul_f32 v[20:21], v[20:21], v[4:5] op_sel_hi:[1,0]
	v_pk_mul_f32 v[18:19], v[18:19], v[4:5] op_sel_hi:[1,0]
	v_pk_mul_f32 v[16:17], v[16:17], v[4:5] op_sel_hi:[1,0]
	v_pk_mul_f32 v[14:15], v[14:15], v[4:5] op_sel_hi:[1,0]
	v_pk_mul_f32 v[12:13], v[12:13], v[4:5] op_sel_hi:[1,0]
	v_pk_mul_f32 v[10:11], v[10:11], v[4:5] op_sel_hi:[1,0]
	v_pk_mul_f32 v[8:9], v[8:9], v[4:5] op_sel_hi:[1,0]
	v_pk_mul_f32 v[6:7], v[6:7], v[4:5] op_sel_hi:[1,0]
	s_branch .LBB0_711

.LBB0_812:
	s_mov_b64 s[56:57], s[38:39]
	s_add_u32 s74, s71, s56
	s_addc_u32 s75, s72, s57
	s_add_u32 s38, s56, 0x100
	s_addc_u32 s39, s57, 0
	s_cmp_eq_u32 s73, 12
	s_cselect_b64 s[40:41], -1, 0
	s_and_b64 s[54:55], s[40:41], exec
	s_cselect_b32 s75, s27, s75
	s_cselect_b32 s74, s29, s74
	s_cselect_b32 s54, 0, s38
	s_add_i32 s81, s68, s43
	s_add_i32 m0, s48, 0xc000
	s_add_i32 s80, s48, 0xe000
	s_add_i32 s82, s81, 0x2000
	s_add_u32 s76, s74, 0x80000
	s_addc_u32 s77, s75, 0
	s_and_b64 s[40:41], s[6:7], s[40:41]
	s_and_b64 s[40:41], s[40:41], exec
	s_cselect_b32 s41, s30, s14
	s_cselect_b32 s40, s31, s15
	s_add_u32 s78, s41, s54
	ds_read_b128 v[66:69], v135
	ds_read_b128 v[70:73], v135 offset:1024
	ds_read_b128 v[74:77], v135 offset:2048
	ds_read_b128 v[78:81], v135 offset:3072
	s_addc_u32 s79, s40, 0
	s_add_i32 s83, 0, 0x18000
	s_add_u32 s54, s78, 0x80000
	s_addc_u32 s55, s79, 0
	s_add_i32 s84, s83, s43
	s_add_i32 s85, s84, 0x2000
	s_add_u32 s40, s74, 0x80080
	s_addc_u32 s41, s75, 0
	s_cmp_lg_u32 s73, 12
	v_lshl_add_u64 v[138:139], v[128:129], 0, s[56:57]
	ds_read_b128 v[82:85], v136
	ds_read_b128 v[86:89], v136 offset:1024
	ds_read_b128 v[90:93], v136 offset:2048
	ds_read_b128 v[94:97], v136 offset:3072
	ds_read_b128 v[98:101], v136 offset:4096
	ds_read_b128 v[102:105], v136 offset:5120
	ds_read_b128 v[106:109], v136 offset:6144
	ds_read_b128 v[110:113], v136 offset:7168
	global_load_lds_dwordx4 v[138:139], off
	v_lshl_add_u64 v[138:139], v[130:131], 0, s[56:57]
	s_mov_b32 m0, s80
	s_nop 0
	global_load_lds_dwordx4 v[138:139], off
	s_waitcnt vmcnt(8)
	s_waitcnt lgkmcnt(0)
	s_barrier
	s_waitcnt lgkmcnt(0)
	v_mfma_f32_16x16x32_bf16 v[62:65], v[66:69], v[82:85], v[62:65]
	v_mfma_f32_16x16x32_bf16 v[54:57], v[74:77], v[82:85], v[54:57]
	v_mfma_f32_16x16x32_bf16 v[46:49], v[66:69], v[90:93], v[46:49]
	v_mfma_f32_16x16x32_bf16 v[42:45], v[74:77], v[90:93], v[42:45]
	v_mfma_f32_16x16x32_bf16 v[38:41], v[66:69], v[98:101], v[38:41]
	v_mfma_f32_16x16x32_bf16 v[30:33], v[74:77], v[98:101], v[30:33]
	v_mfma_f32_16x16x32_bf16 v[22:25], v[66:69], v[106:109], v[22:25]
	v_mfma_f32_16x16x32_bf16 v[18:21], v[74:77], v[106:109], v[18:21]
	v_mfma_f32_16x16x32_bf16 v[62:65], v[70:73], v[86:89], v[62:65]
	v_mfma_f32_16x16x32_bf16 v[54:57], v[78:81], v[86:89], v[54:57]
	v_mfma_f32_16x16x32_bf16 v[46:49], v[70:73], v[94:97], v[46:49]
	v_mfma_f32_16x16x32_bf16 v[42:45], v[78:81], v[94:97], v[42:45]
	v_mfma_f32_16x16x32_bf16 v[38:41], v[70:73], v[102:105], v[38:41]
	v_mfma_f32_16x16x32_bf16 v[30:33], v[78:81], v[102:105], v[30:33]
	v_mfma_f32_16x16x32_bf16 v[22:25], v[70:73], v[110:113], v[22:25]
	v_mfma_f32_16x16x32_bf16 v[18:21], v[78:81], v[110:113], v[18:21]
	s_barrier
	s_mov_b32 m0, s81
	v_lshl_add_u64 v[138:139], s[74:75], 0, v[114:115]
	global_load_lds_dwordx4 v[138:139], off
	v_lshl_add_u64 v[140:141], s[74:75], 0, v[116:117]
	s_mov_b32 m0, s82
	v_lshl_add_u64 v[142:143], s[76:77], 0, v[114:115]
	global_load_lds_dwordx4 v[140:141], off
	s_mov_b32 m0, s49
	v_lshl_add_u64 v[144:145], s[78:79], 0, v[116:117]
	global_load_lds_dwordx4 v[142:143], off
	v_lshl_add_u64 v[142:143], s[76:77], 0, v[116:117]
	s_mov_b32 m0, s50
	s_nop 0
	global_load_lds_dwordx4 v[142:143], off
	v_lshl_add_u64 v[142:143], s[78:79], 0, v[114:115]
	s_mov_b32 m0, s48
	s_nop 0
	global_load_lds_dwordx4 v[142:143], off
	s_mov_b32 m0, s51
	s_nop 0
	global_load_lds_dwordx4 v[144:145], off
	ds_read_b128 v[82:85], v136 offset:16384
	ds_read_b128 v[86:89], v136 offset:17408
	ds_read_b128 v[90:93], v136 offset:18432
	ds_read_b128 v[94:97], v136 offset:19456
	ds_read_b128 v[98:101], v136 offset:20480
	ds_read_b128 v[102:105], v136 offset:21504
	ds_read_b128 v[106:109], v136 offset:22528
	ds_read_b128 v[110:113], v136 offset:23552
	s_waitcnt vmcnt(8)
	s_waitcnt lgkmcnt(0)
	s_barrier
	s_waitcnt lgkmcnt(0)
	v_mfma_f32_16x16x32_bf16 v[58:61], v[66:69], v[82:85], v[58:61]
	v_mfma_f32_16x16x32_bf16 v[50:53], v[74:77], v[82:85], v[50:53]
	v_mfma_f32_16x16x32_bf16 v[34:37], v[66:69], v[90:93], v[34:37]
	v_mfma_f32_16x16x32_bf16 v[26:29], v[74:77], v[90:93], v[26:29]
	v_mfma_f32_16x16x32_bf16 v[14:17], v[66:69], v[98:101], v[14:17]
	v_mfma_f32_16x16x32_bf16 v[10:13], v[74:77], v[98:101], v[10:13]
	v_mfma_f32_16x16x32_bf16 v[6:9], v[66:69], v[106:109], v[6:9]
	v_mfma_f32_16x16x32_bf16 v[2:5], v[74:77], v[106:109], v[2:5]
	v_mfma_f32_16x16x32_bf16 v[58:61], v[70:73], v[86:89], v[58:61]
	v_mfma_f32_16x16x32_bf16 v[50:53], v[78:81], v[86:89], v[50:53]
	v_mfma_f32_16x16x32_bf16 v[34:37], v[70:73], v[94:97], v[34:37]
	v_mfma_f32_16x16x32_bf16 v[26:29], v[78:81], v[94:97], v[26:29]
	v_mfma_f32_16x16x32_bf16 v[14:17], v[70:73], v[102:105], v[14:17]
	v_mfma_f32_16x16x32_bf16 v[10:13], v[78:81], v[102:105], v[10:13]
	v_mfma_f32_16x16x32_bf16 v[6:9], v[70:73], v[110:113], v[6:9]
	v_mfma_f32_16x16x32_bf16 v[2:5], v[78:81], v[110:113], v[2:5]
	s_barrier
	s_mov_b32 m0, s52
	v_lshl_add_u64 v[146:147], s[54:55], 0, v[114:115]
	global_load_lds_dwordx4 v[146:147], off
	v_lshl_add_u64 v[146:147], s[54:55], 0, v[116:117]
	s_mov_b32 m0, s53
	s_nop 0
	global_load_lds_dwordx4 v[146:147], off
	v_add_u32_e32 v78, s83, v133
	ds_read_b128 v[66:69], v78
	ds_read_b128 v[70:73], v78 offset:1024
	ds_read_b128 v[74:77], v78 offset:2048
	ds_read_b128 v[78:81], v78 offset:3072
	ds_read_b128 v[82:85], v136 offset:32768
	ds_read_b128 v[86:89], v136 offset:33792
	ds_read_b128 v[90:93], v136 offset:34816
	ds_read_b128 v[94:97], v136 offset:35840
	ds_read_b128 v[98:101], v136 offset:36864
	ds_read_b128 v[102:105], v136 offset:37888
	ds_read_b128 v[106:109], v136 offset:38912
	ds_read_b128 v[110:113], v136 offset:39936
	s_waitcnt vmcnt(8)
	s_waitcnt lgkmcnt(0)
	s_barrier
	s_waitcnt lgkmcnt(0)
	v_mfma_f32_16x16x32_bf16 v[62:65], v[66:69], v[82:85], v[62:65]
	v_mfma_f32_16x16x32_bf16 v[54:57], v[74:77], v[82:85], v[54:57]
	v_mfma_f32_16x16x32_bf16 v[46:49], v[66:69], v[90:93], v[46:49]
	v_mfma_f32_16x16x32_bf16 v[42:45], v[74:77], v[90:93], v[42:45]
	v_mfma_f32_16x16x32_bf16 v[38:41], v[66:69], v[98:101], v[38:41]
	v_mfma_f32_16x16x32_bf16 v[30:33], v[74:77], v[98:101], v[30:33]
	v_mfma_f32_16x16x32_bf16 v[22:25], v[66:69], v[106:109], v[22:25]
	v_mfma_f32_16x16x32_bf16 v[18:21], v[74:77], v[106:109], v[18:21]
	v_mfma_f32_16x16x32_bf16 v[62:65], v[70:73], v[86:89], v[62:65]
	v_mfma_f32_16x16x32_bf16 v[54:57], v[78:81], v[86:89], v[54:57]
	v_mfma_f32_16x16x32_bf16 v[46:49], v[70:73], v[94:97], v[46:49]
	v_mfma_f32_16x16x32_bf16 v[42:45], v[78:81], v[94:97], v[42:45]
	v_mfma_f32_16x16x32_bf16 v[38:41], v[70:73], v[102:105], v[38:41]
	v_mfma_f32_16x16x32_bf16 v[30:33], v[78:81], v[102:105], v[30:33]
	v_mfma_f32_16x16x32_bf16 v[22:25], v[70:73], v[110:113], v[22:25]
	v_mfma_f32_16x16x32_bf16 v[18:21], v[78:81], v[110:113], v[18:21]
	s_barrier
	s_mov_b32 m0, s84
	v_lshl_add_u64 v[138:139], v[138:139], 0, s[12:13]
	global_load_lds_dwordx4 v[138:139], off
	v_lshl_add_u64 v[138:139], v[140:141], 0, s[12:13]
	s_mov_b32 m0, s85
	s_nop 0
	global_load_lds_dwordx4 v[138:139], off
	v_lshl_add_u64 v[138:139], s[40:41], 0, v[114:115]
	s_mov_b32 m0, s65
	s_nop 0
	global_load_lds_dwordx4 v[138:139], off
	v_lshl_add_u64 v[138:139], s[40:41], 0, v[116:117]
	s_mov_b32 m0, s66
	s_nop 0
	global_load_lds_dwordx4 v[138:139], off
	v_lshl_add_u64 v[138:139], v[142:143], 0, s[12:13]
	s_mov_b32 m0, s63
	s_nop 0
	global_load_lds_dwordx4 v[138:139], off
	v_lshl_add_u64 v[138:139], v[144:145], 0, s[12:13]
	s_mov_b32 m0, s64
	s_nop 0
	global_load_lds_dwordx4 v[138:139], off
	ds_read_b128 v[106:109], v136 offset:49152
	ds_read_b128 v[110:113], v136 offset:50176
	ds_read_b128 v[98:101], v136 offset:51200
	ds_read_b128 v[102:105], v136 offset:52224
	ds_read_b128 v[90:93], v136 offset:53248
	ds_read_b128 v[94:97], v136 offset:54272
	ds_read_b128 v[82:85], v136 offset:55296
	ds_read_b128 v[86:89], v136 offset:56320
	s_waitcnt vmcnt(8)
	s_waitcnt lgkmcnt(0)
	s_barrier
	s_cbranch_scc1 .LBB0_811
	v_mov_b32_e32 v137, v1
	v_mov_b32_e32 v138, v132
	s_andn2_b64 vcc, exec, s[16:17]
	s_cbranch_vccnz .LBB0_810
	v_add_u32_e32 v140, s70, v137
	v_ashrrev_i32_e32 v141, 31, v140
	v_lshl_add_u32 v138, v138, 2, s62
	v_lshlrev_b64 v[140:141], 8, v[140:141]
	v_ashrrev_i32_e32 v139, 31, v138
	v_lshl_add_u64 v[140:141], s[36:37], 0, v[140:141]
	v_lshl_add_u64 v[138:139], v[138:139], 2, v[140:141]
	v_add_co_u32_e32 v142, vcc, 0x1000, v138
	global_store_dwordx4 v[138:139], v[62:65], off
	global_store_dwordx4 v[138:139], v[54:57], off offset:64
	v_addc_co_u32_e32 v143, vcc, 0, v139, vcc
	v_lshl_add_u64 v[140:141], v[138:139], 0, s[20:21]
	global_store_dwordx4 v[142:143], v[46:49], off
	global_store_dwordx4 v[140:141], v[42:45], off offset:64
	v_add_co_u32_e32 v142, vcc, 0x2000, v138
	v_lshl_add_u64 v[140:141], v[138:139], 0, s[22:23]
	s_nop 0
	v_addc_co_u32_e32 v143, vcc, 0, v139, vcc
	global_store_dwordx4 v[142:143], v[38:41], off
	global_store_dwordx4 v[140:141], v[30:33], off offset:64
	v_lshl_add_u64 v[140:141], v[138:139], 0, s[24:25]
	v_add_co_u32_e32 v138, vcc, 0x3000, v138
	s_nop 1
	v_addc_co_u32_e32 v139, vcc, 0, v139, vcc
	global_store_dwordx4 v[138:139], v[22:25], off
	global_store_dwordx4 v[140:141], v[18:21], off offset:64
	s_branch .LBB0_810

.Lmoe_ix_ready_0:
.LBB0_1005:
	s_add_u32 s40, s64, s10
	s_addc_u32 s41, s65, s11
	s_add_u32 s38, s10, 0x100
	s_addc_u32 s39, s11, 0
	s_cmpk_eq_i32 s10, 0xf00
	s_cselect_b64 vcc, -1, 0
	s_and_b64 s[2:3], vcc, exec
	s_cselect_b32 s41, s31, s41
	s_cselect_b32 s40, s37, s40
	s_cselect_b32 s67, 0, s38
	v_lshl_add_u64 v[226:227], v[146:147], 0, s[10:11]
	s_add_i32 m0, s49, 0xc000
	s_nop 0
	global_load_lds_dwordx4 v[226:227], off
	v_lshl_add_u64 v[226:227], v[144:145], 0, s[10:11]
	s_add_i32 m0, s49, 0xe000
	s_nop 0
	global_load_lds_dwordx4 v[226:227], off
	ds_read_b128 v[152:155], v158
	ds_read_b128 v[166:169], v158 offset:1024
	ds_read_b128 v[170:173], v158 offset:2048
	ds_read_b128 v[174:177], v158 offset:3072
	ds_read_b128 v[178:181], v159
	ds_read_b128 v[182:185], v159 offset:1024
	ds_read_b128 v[186:189], v159 offset:2048
	ds_read_b128 v[190:193], v159 offset:3072
	ds_read_b128 v[194:197], v160
	ds_read_b128 v[198:201], v160 offset:1024
	ds_read_b128 v[202:205], v160 offset:2048
	ds_read_b128 v[206:209], v160 offset:3072
	ds_read_b128 v[210:213], v160 offset:4096
	ds_read_b128 v[214:217], v160 offset:5120
	ds_read_b128 v[218:221], v160 offset:6144
	ds_read_b128 v[222:225], v160 offset:7168
	s_waitcnt vmcnt(8)
	s_waitcnt lgkmcnt(0)
	s_barrier
	s_waitcnt lgkmcnt(0)
	v_mfma_f32_16x16x32_bf16 v[126:129], v[152:155], v[194:197], v[126:129]
	v_mfma_f32_16x16x32_bf16 v[122:125], v[170:173], v[194:197], v[122:125]
	v_mfma_f32_16x16x32_bf16 v[110:113], v[152:155], v[202:205], v[110:113]
	v_mfma_f32_16x16x32_bf16 v[106:109], v[170:173], v[202:205], v[106:109]
	v_mfma_f32_16x16x32_bf16 v[94:97], v[152:155], v[210:213], v[94:97]
	v_mfma_f32_16x16x32_bf16 v[90:93], v[170:173], v[210:213], v[90:93]
	v_mfma_f32_16x16x32_bf16 v[78:81], v[152:155], v[218:221], v[78:81]
	v_mfma_f32_16x16x32_bf16 v[74:77], v[170:173], v[218:221], v[74:77]
	v_mfma_f32_16x16x32_bf16 v[126:129], v[166:169], v[198:201], v[126:129]
	v_mfma_f32_16x16x32_bf16 v[122:125], v[174:177], v[198:201], v[122:125]
	v_mfma_f32_16x16x32_bf16 v[110:113], v[166:169], v[206:209], v[110:113]
	v_mfma_f32_16x16x32_bf16 v[106:109], v[174:177], v[206:209], v[106:109]
	v_mfma_f32_16x16x32_bf16 v[94:97], v[166:169], v[214:217], v[94:97]
	v_mfma_f32_16x16x32_bf16 v[90:93], v[174:177], v[214:217], v[90:93]
	v_mfma_f32_16x16x32_bf16 v[78:81], v[166:169], v[222:225], v[78:81]
	v_mfma_f32_16x16x32_bf16 v[74:77], v[174:177], v[222:225], v[74:77]
	v_mfma_f32_16x16x32_bf16 v[118:121], v[178:181], v[194:197], v[118:121]
	v_mfma_f32_16x16x32_bf16 v[114:117], v[186:189], v[194:197], v[114:117]
	v_mfma_f32_16x16x32_bf16 v[102:105], v[178:181], v[202:205], v[102:105]
	v_mfma_f32_16x16x32_bf16 v[98:101], v[186:189], v[202:205], v[98:101]
	v_mfma_f32_16x16x32_bf16 v[86:89], v[178:181], v[210:213], v[86:89]
	v_mfma_f32_16x16x32_bf16 v[82:85], v[186:189], v[210:213], v[82:85]
	v_mfma_f32_16x16x32_bf16 v[70:73], v[178:181], v[218:221], v[70:73]
	v_mfma_f32_16x16x32_bf16 v[66:69], v[186:189], v[218:221], v[66:69]
	v_mfma_f32_16x16x32_bf16 v[118:121], v[182:185], v[198:201], v[118:121]
	v_mfma_f32_16x16x32_bf16 v[114:117], v[190:193], v[198:201], v[114:117]
	v_mfma_f32_16x16x32_bf16 v[102:105], v[182:185], v[206:209], v[102:105]
	v_mfma_f32_16x16x32_bf16 v[98:101], v[190:193], v[206:209], v[98:101]
	v_mfma_f32_16x16x32_bf16 v[86:89], v[182:185], v[214:217], v[86:89]
	v_mfma_f32_16x16x32_bf16 v[82:85], v[190:193], v[214:217], v[82:85]
	v_mfma_f32_16x16x32_bf16 v[70:73], v[182:185], v[222:225], v[70:73]
	v_mfma_f32_16x16x32_bf16 v[66:69], v[190:193], v[222:225], v[66:69]
	s_barrier
	s_add_i32 s2, s61, s48
	v_lshl_add_u64 v[226:227], s[40:41], 0, v[132:133]
	s_mov_b32 m0, s2
	s_nop 0
	global_load_lds_dwordx4 v[226:227], off
	s_add_i32 m0, s2, 0x2000
	s_add_u32 s2, s40, 0x80000
	v_lshl_add_u64 v[228:229], s[40:41], 0, v[134:135]
	s_addc_u32 s3, s41, 0
	s_add_i32 s10, s62, s48
	global_load_lds_dwordx4 v[228:229], off
	v_lshl_add_u64 v[230:231], s[2:3], 0, v[132:133]
	s_mov_b32 m0, s10
	v_cndmask_b32_e32 v130, v148, v164, vcc
	global_load_lds_dwordx4 v[230:231], off
	s_add_i32 m0, s10, 0x2000
	v_lshl_add_u64 v[230:231], s[2:3], 0, v[134:135]
	s_add_u32 s2, s16, s67
	global_load_lds_dwordx4 v[230:231], off
	s_addc_u32 s3, s17, 0
	s_mov_b32 m0, s49
	v_lshl_add_u64 v[230:231], s[2:3], 0, v[130:131]
	global_load_lds_dwordx4 v130, s[2:3]
	v_cndmask_b32_e32 v130, v140, v163, vcc
	s_mov_b32 m0, s50
	v_lshl_add_u64 v[232:233], s[2:3], 0, v[130:131]
	global_load_lds_dwordx4 v130, s[2:3]
	ds_read_b128 v[194:197], v160 offset:16384
	ds_read_b128 v[198:201], v160 offset:17408
	ds_read_b128 v[202:205], v160 offset:18432
	ds_read_b128 v[206:209], v160 offset:19456
	ds_read_b128 v[210:213], v160 offset:20480
	ds_read_b128 v[214:217], v160 offset:21504
	ds_read_b128 v[218:221], v160 offset:22528
	ds_read_b128 v[222:225], v160 offset:23552
	s_waitcnt vmcnt(8)
	s_waitcnt lgkmcnt(0)
	s_barrier
	s_waitcnt lgkmcnt(0)
	v_mfma_f32_16x16x32_bf16 v[62:65], v[152:155], v[194:197], v[62:65]
	v_mfma_f32_16x16x32_bf16 v[58:61], v[170:173], v[194:197], v[58:61]
	v_mfma_f32_16x16x32_bf16 v[46:49], v[152:155], v[202:205], v[46:49]
	v_mfma_f32_16x16x32_bf16 v[42:45], v[170:173], v[202:205], v[42:45]
	v_mfma_f32_16x16x32_bf16 v[30:33], v[152:155], v[210:213], v[30:33]
	v_mfma_f32_16x16x32_bf16 v[26:29], v[170:173], v[210:213], v[26:29]
	v_mfma_f32_16x16x32_bf16 v[14:17], v[152:155], v[218:221], v[14:17]
	v_mfma_f32_16x16x32_bf16 v[10:13], v[170:173], v[218:221], v[10:13]
	v_mfma_f32_16x16x32_bf16 v[62:65], v[166:169], v[198:201], v[62:65]
	v_mfma_f32_16x16x32_bf16 v[58:61], v[174:177], v[198:201], v[58:61]
	v_mfma_f32_16x16x32_bf16 v[46:49], v[166:169], v[206:209], v[46:49]
	v_mfma_f32_16x16x32_bf16 v[42:45], v[174:177], v[206:209], v[42:45]
	v_mfma_f32_16x16x32_bf16 v[30:33], v[166:169], v[214:217], v[30:33]
	v_mfma_f32_16x16x32_bf16 v[26:29], v[174:177], v[214:217], v[26:29]
	v_mfma_f32_16x16x32_bf16 v[14:17], v[166:169], v[222:225], v[14:17]
	v_mfma_f32_16x16x32_bf16 v[10:13], v[174:177], v[222:225], v[10:13]
	v_mfma_f32_16x16x32_bf16 v[54:57], v[178:181], v[194:197], v[54:57]
	v_mfma_f32_16x16x32_bf16 v[50:53], v[186:189], v[194:197], v[50:53]
	v_mfma_f32_16x16x32_bf16 v[38:41], v[178:181], v[202:205], v[38:41]
	v_mfma_f32_16x16x32_bf16 v[34:37], v[186:189], v[202:205], v[34:37]
	v_mfma_f32_16x16x32_bf16 v[22:25], v[178:181], v[210:213], v[22:25]
	v_mfma_f32_16x16x32_bf16 v[18:21], v[186:189], v[210:213], v[18:21]
	v_mfma_f32_16x16x32_bf16 v[6:9], v[178:181], v[218:221], v[6:9]
	v_mfma_f32_16x16x32_bf16 v[2:5], v[186:189], v[218:221], v[2:5]
	v_mfma_f32_16x16x32_bf16 v[54:57], v[182:185], v[198:201], v[54:57]
	v_mfma_f32_16x16x32_bf16 v[50:53], v[190:193], v[198:201], v[50:53]
	v_mfma_f32_16x16x32_bf16 v[38:41], v[182:185], v[206:209], v[38:41]
	v_mfma_f32_16x16x32_bf16 v[34:37], v[190:193], v[206:209], v[34:37]
	v_mfma_f32_16x16x32_bf16 v[22:25], v[182:185], v[214:217], v[22:25]
	v_mfma_f32_16x16x32_bf16 v[18:21], v[190:193], v[214:217], v[18:21]
	v_mfma_f32_16x16x32_bf16 v[6:9], v[182:185], v[222:225], v[6:9]
	v_mfma_f32_16x16x32_bf16 v[2:5], v[190:193], v[222:225], v[2:5]
	s_barrier
	s_add_i32 s10, 0, 0x18000
	v_add_u32_e32 v130, s10, v156
	s_add_i32 s11, 0, 0x1c000
	ds_read_b128 v[152:155], v130
	ds_read_b128 v[166:169], v130 offset:1024
	ds_read_b128 v[170:173], v130 offset:2048
	ds_read_b128 v[174:177], v130 offset:3072
	v_add_u32_e32 v130, s11, v156
	ds_read_b128 v[178:181], v130
	ds_read_b128 v[182:185], v130 offset:1024
	ds_read_b128 v[186:189], v130 offset:2048
	ds_read_b128 v[190:193], v130 offset:3072
	s_mov_b32 m0, s51
	v_cndmask_b32_e32 v130, v138, v161, vcc
	ds_read_b128 v[194:197], v160 offset:32768
	ds_read_b128 v[198:201], v160 offset:33792
	ds_read_b128 v[202:205], v160 offset:34816
	ds_read_b128 v[206:209], v160 offset:35840
	ds_read_b128 v[210:213], v160 offset:36864
	ds_read_b128 v[214:217], v160 offset:37888
	ds_read_b128 v[218:221], v160 offset:38912
	ds_read_b128 v[222:225], v160 offset:39936
	global_load_lds_dwordx4 v130, s[2:3]
	v_cndmask_b32_e32 v130, v142, v162, vcc
	s_mov_b32 m0, s52
	s_nop 0
	global_load_lds_dwordx4 v130, s[2:3]
	s_waitcnt vmcnt(8)
	s_waitcnt lgkmcnt(0)
	s_barrier
	s_waitcnt lgkmcnt(0)
	v_mfma_f32_16x16x32_bf16 v[126:129], v[152:155], v[194:197], v[126:129]
	v_mfma_f32_16x16x32_bf16 v[122:125], v[170:173], v[194:197], v[122:125]
	v_mfma_f32_16x16x32_bf16 v[110:113], v[152:155], v[202:205], v[110:113]
	v_mfma_f32_16x16x32_bf16 v[106:109], v[170:173], v[202:205], v[106:109]
	v_mfma_f32_16x16x32_bf16 v[94:97], v[152:155], v[210:213], v[94:97]
	v_mfma_f32_16x16x32_bf16 v[90:93], v[170:173], v[210:213], v[90:93]
	v_mfma_f32_16x16x32_bf16 v[78:81], v[152:155], v[218:221], v[78:81]
	v_mfma_f32_16x16x32_bf16 v[74:77], v[170:173], v[218:221], v[74:77]
	v_mfma_f32_16x16x32_bf16 v[126:129], v[166:169], v[198:201], v[126:129]
	v_mfma_f32_16x16x32_bf16 v[122:125], v[174:177], v[198:201], v[122:125]
	v_mfma_f32_16x16x32_bf16 v[110:113], v[166:169], v[206:209], v[110:113]
	v_mfma_f32_16x16x32_bf16 v[106:109], v[174:177], v[206:209], v[106:109]
	v_mfma_f32_16x16x32_bf16 v[94:97], v[166:169], v[214:217], v[94:97]
	v_mfma_f32_16x16x32_bf16 v[90:93], v[174:177], v[214:217], v[90:93]
	v_mfma_f32_16x16x32_bf16 v[78:81], v[166:169], v[222:225], v[78:81]
	v_mfma_f32_16x16x32_bf16 v[74:77], v[174:177], v[222:225], v[74:77]
	v_mfma_f32_16x16x32_bf16 v[118:121], v[178:181], v[194:197], v[118:121]
	v_mfma_f32_16x16x32_bf16 v[114:117], v[186:189], v[194:197], v[114:117]
	v_mfma_f32_16x16x32_bf16 v[102:105], v[178:181], v[202:205], v[102:105]
	v_mfma_f32_16x16x32_bf16 v[98:101], v[186:189], v[202:205], v[98:101]
	v_mfma_f32_16x16x32_bf16 v[86:89], v[178:181], v[210:213], v[86:89]
	v_mfma_f32_16x16x32_bf16 v[82:85], v[186:189], v[210:213], v[82:85]
	v_mfma_f32_16x16x32_bf16 v[70:73], v[178:181], v[218:221], v[70:73]
	v_mfma_f32_16x16x32_bf16 v[66:69], v[186:189], v[218:221], v[66:69]
	v_mfma_f32_16x16x32_bf16 v[118:121], v[182:185], v[198:201], v[118:121]
	v_mfma_f32_16x16x32_bf16 v[114:117], v[190:193], v[198:201], v[114:117]
	v_mfma_f32_16x16x32_bf16 v[102:105], v[182:185], v[206:209], v[102:105]
	v_mfma_f32_16x16x32_bf16 v[98:101], v[190:193], v[206:209], v[98:101]
	v_mfma_f32_16x16x32_bf16 v[86:89], v[182:185], v[214:217], v[86:89]
	v_mfma_f32_16x16x32_bf16 v[82:85], v[190:193], v[214:217], v[82:85]
	v_mfma_f32_16x16x32_bf16 v[70:73], v[182:185], v[222:225], v[70:73]
	v_mfma_f32_16x16x32_bf16 v[66:69], v[190:193], v[222:225], v[66:69]
	s_barrier
	s_add_i32 s2, s10, s48
	v_lshl_add_u64 v[226:227], v[226:227], 0, s[20:21]
	s_mov_b32 m0, s2
	s_nop 0
	global_load_lds_dwordx4 v[226:227], off
	s_add_i32 m0, s2, 0x2000
	s_add_u32 s2, s40, 0x80080
	v_lshl_add_u64 v[226:227], v[228:229], 0, s[20:21]
	s_addc_u32 s3, s41, 0
	s_add_i32 s10, s11, s48
	global_load_lds_dwordx4 v[226:227], off
	v_lshl_add_u64 v[226:227], s[2:3], 0, v[132:133]
	s_mov_b32 m0, s10
	s_nop 0
	global_load_lds_dwordx4 v[226:227], off
	v_lshl_add_u64 v[226:227], s[2:3], 0, v[134:135]
	s_add_i32 m0, s10, 0x2000
	s_nop 0
	global_load_lds_dwordx4 v[226:227], off
	v_lshl_add_u64 v[226:227], v[230:231], 0, s[20:21]
	s_mov_b32 m0, s58
	s_nop 0
	global_load_lds_dwordx4 v[226:227], off
	v_lshl_add_u64 v[226:227], v[232:233], 0, s[20:21]
	s_mov_b32 m0, s59
	s_nop 0
	global_load_lds_dwordx4 v[226:227], off
	ds_read_b128 v[194:197], v160 offset:49152
	ds_read_b128 v[198:201], v160 offset:50176
	ds_read_b128 v[202:205], v160 offset:51200
	ds_read_b128 v[206:209], v160 offset:52224
	ds_read_b128 v[210:213], v160 offset:53248
	ds_read_b128 v[214:217], v160 offset:54272
	ds_read_b128 v[218:221], v160 offset:55296
	ds_read_b128 v[222:225], v160 offset:56320
	s_waitcnt vmcnt(8)
	s_waitcnt lgkmcnt(0)
	s_barrier
	s_waitcnt lgkmcnt(0)
	v_mfma_f32_16x16x32_bf16 v[62:65], v[152:155], v[194:197], v[62:65]
	v_mfma_f32_16x16x32_bf16 v[58:61], v[170:173], v[194:197], v[58:61]
	v_mfma_f32_16x16x32_bf16 v[46:49], v[152:155], v[202:205], v[46:49]
	v_mfma_f32_16x16x32_bf16 v[42:45], v[170:173], v[202:205], v[42:45]
	v_mfma_f32_16x16x32_bf16 v[30:33], v[152:155], v[210:213], v[30:33]
	v_mfma_f32_16x16x32_bf16 v[26:29], v[170:173], v[210:213], v[26:29]
	v_mfma_f32_16x16x32_bf16 v[14:17], v[152:155], v[218:221], v[14:17]
	v_mfma_f32_16x16x32_bf16 v[10:13], v[170:173], v[218:221], v[10:13]
	v_mfma_f32_16x16x32_bf16 v[62:65], v[166:169], v[198:201], v[62:65]
	v_mfma_f32_16x16x32_bf16 v[58:61], v[174:177], v[198:201], v[58:61]
	v_mfma_f32_16x16x32_bf16 v[46:49], v[166:169], v[206:209], v[46:49]
	v_mfma_f32_16x16x32_bf16 v[42:45], v[174:177], v[206:209], v[42:45]
	v_mfma_f32_16x16x32_bf16 v[30:33], v[166:169], v[214:217], v[30:33]
	v_mfma_f32_16x16x32_bf16 v[26:29], v[174:177], v[214:217], v[26:29]
	v_mfma_f32_16x16x32_bf16 v[14:17], v[166:169], v[222:225], v[14:17]
	v_mfma_f32_16x16x32_bf16 v[10:13], v[174:177], v[222:225], v[10:13]
	v_mfma_f32_16x16x32_bf16 v[54:57], v[178:181], v[194:197], v[54:57]
	v_mfma_f32_16x16x32_bf16 v[50:53], v[186:189], v[194:197], v[50:53]
	v_mfma_f32_16x16x32_bf16 v[38:41], v[178:181], v[202:205], v[38:41]
	v_mfma_f32_16x16x32_bf16 v[34:37], v[186:189], v[202:205], v[34:37]
	v_mfma_f32_16x16x32_bf16 v[22:25], v[178:181], v[210:213], v[22:25]
	v_mfma_f32_16x16x32_bf16 v[18:21], v[186:189], v[210:213], v[18:21]
	v_mfma_f32_16x16x32_bf16 v[6:9], v[178:181], v[218:221], v[6:9]
	v_mfma_f32_16x16x32_bf16 v[2:5], v[186:189], v[218:221], v[2:5]
	v_mfma_f32_16x16x32_bf16 v[54:57], v[182:185], v[198:201], v[54:57]
	v_mfma_f32_16x16x32_bf16 v[50:53], v[190:193], v[198:201], v[50:53]
	v_mfma_f32_16x16x32_bf16 v[38:41], v[182:185], v[206:209], v[38:41]
	v_mfma_f32_16x16x32_bf16 v[34:37], v[190:193], v[206:209], v[34:37]
	v_mfma_f32_16x16x32_bf16 v[22:25], v[182:185], v[214:217], v[22:25]
	v_mfma_f32_16x16x32_bf16 v[18:21], v[190:193], v[214:217], v[18:21]
	v_mfma_f32_16x16x32_bf16 v[6:9], v[182:185], v[222:225], v[6:9]
	v_mfma_f32_16x16x32_bf16 v[2:5], v[190:193], v[222:225], v[2:5]
	s_barrier
	s_add_i32 s66, s66, 2
	s_cmp_gt_u32 s66, 29
	s_mov_b64 s[10:11], s[38:39]
	s_cbranch_scc0 .LBB0_1005
	s_and_b64 vcc, exec, s[24:25]
	s_cbranch_vccz .LBB0_1008
	s_barrier

.LBB0_1122:
	s_lshl_b32 s2, s87, 7
	v_add_u32_e32 v142, s80, v205
	v_add_u32_e32 v158, s81, v205
	s_add_u32 s64, s38, s2
	ds_read_b128 v[130:133], v142
	ds_read_b128 v[134:137], v142 offset:1024
	ds_read_b128 v[138:141], v142 offset:2048
	ds_read_b128 v[142:145], v142 offset:3072
	ds_read_b128 v[146:149], v158
	ds_read_b128 v[150:153], v158 offset:1024
	ds_read_b128 v[154:157], v158 offset:2048
	ds_read_b128 v[158:161], v158 offset:3072
	s_addc_u32 s65, s39, 0
	s_add_u32 s66, s64, 0x100
	s_addc_u32 s67, s65, 0
	s_and_b64 s[64:65], s[60:61], exec
	s_cselect_b32 s65, s35, s67
	s_cselect_b32 s64, s83, s66
	s_add_i32 s68, s2, 0x100
	s_and_b64 s[66:67], s[60:61], exec
	s_cselect_b32 s68, 0, s68
	s_add_u32 s2, s36, s2
	s_addc_u32 s67, s37, 0
	s_add_u32 s66, s2, 0x20080
	s_addc_u32 s67, s67, 0
	v_lshl_add_u64 v[210:211], s[66:67], 0, v[194:195]
	s_add_i32 m0, s50, 0xc000
	ds_read_b128 v[162:165], v209
	ds_read_b128 v[166:169], v209 offset:1024
	ds_read_b128 v[170:173], v209 offset:2048
	ds_read_b128 v[174:177], v209 offset:3072
	ds_read_b128 v[178:181], v209 offset:4096
	ds_read_b128 v[182:185], v209 offset:5120
	ds_read_b128 v[186:189], v209 offset:6144
	ds_read_b128 v[190:193], v209 offset:7168
	global_load_lds_dwordx4 v[210:211], off
	v_lshl_add_u64 v[210:211], s[66:67], 0, v[198:199]
	s_add_i32 m0, s50, 0xe000
	s_nop 0
	global_load_lds_dwordx4 v[210:211], off
	s_waitcnt vmcnt(8)
	s_waitcnt lgkmcnt(0)
	s_barrier
	s_waitcnt lgkmcnt(0)
	v_mfma_f32_16x16x32_bf16 v[86:89], v[130:133], v[162:165], v[86:89]
	v_mfma_f32_16x16x32_bf16 v[82:85], v[138:141], v[162:165], v[82:85]
	v_mfma_f32_16x16x32_bf16 v[78:81], v[130:133], v[170:173], v[78:81]
	v_mfma_f32_16x16x32_bf16 v[74:77], v[138:141], v[170:173], v[74:77]
	v_mfma_f32_16x16x32_bf16 v[70:73], v[130:133], v[178:181], v[70:73]
	v_mfma_f32_16x16x32_bf16 v[66:69], v[138:141], v[178:181], v[66:69]
	v_mfma_f32_16x16x32_bf16 v[62:65], v[130:133], v[186:189], v[62:65]
	v_mfma_f32_16x16x32_bf16 v[58:61], v[138:141], v[186:189], v[58:61]
	v_mfma_f32_16x16x32_bf16 v[86:89], v[134:137], v[166:169], v[86:89]
	v_mfma_f32_16x16x32_bf16 v[82:85], v[142:145], v[166:169], v[82:85]
	v_mfma_f32_16x16x32_bf16 v[78:81], v[134:137], v[174:177], v[78:81]
	v_mfma_f32_16x16x32_bf16 v[74:77], v[142:145], v[174:177], v[74:77]
	v_mfma_f32_16x16x32_bf16 v[70:73], v[134:137], v[182:185], v[70:73]
	v_mfma_f32_16x16x32_bf16 v[66:69], v[142:145], v[182:185], v[66:69]
	v_mfma_f32_16x16x32_bf16 v[62:65], v[134:137], v[190:193], v[62:65]
	v_mfma_f32_16x16x32_bf16 v[58:61], v[142:145], v[190:193], v[58:61]
	v_mfma_f32_16x16x32_bf16 v[54:57], v[146:149], v[162:165], v[54:57]
	v_mfma_f32_16x16x32_bf16 v[50:53], v[154:157], v[162:165], v[50:53]
	v_mfma_f32_16x16x32_bf16 v[46:49], v[146:149], v[170:173], v[46:49]
	v_mfma_f32_16x16x32_bf16 v[42:45], v[154:157], v[170:173], v[42:45]
	v_mfma_f32_16x16x32_bf16 v[34:37], v[146:149], v[178:181], v[34:37]
	v_mfma_f32_16x16x32_bf16 v[26:29], v[154:157], v[178:181], v[26:29]
	v_mfma_f32_16x16x32_bf16 v[18:21], v[146:149], v[186:189], v[18:21]
	v_mfma_f32_16x16x32_bf16 v[10:13], v[154:157], v[186:189], v[10:13]
	v_mfma_f32_16x16x32_bf16 v[54:57], v[150:153], v[166:169], v[54:57]
	v_mfma_f32_16x16x32_bf16 v[50:53], v[158:161], v[166:169], v[50:53]
	v_mfma_f32_16x16x32_bf16 v[46:49], v[150:153], v[174:177], v[46:49]
	v_mfma_f32_16x16x32_bf16 v[42:45], v[158:161], v[174:177], v[42:45]
	v_mfma_f32_16x16x32_bf16 v[34:37], v[150:153], v[182:185], v[34:37]
	v_mfma_f32_16x16x32_bf16 v[26:29], v[158:161], v[182:185], v[26:29]
	v_mfma_f32_16x16x32_bf16 v[18:21], v[150:153], v[190:193], v[18:21]
	v_mfma_f32_16x16x32_bf16 v[10:13], v[158:161], v[190:193], v[10:13]
	s_barrier
	s_add_i32 s2, s80, s49
	v_lshl_add_u64 v[210:211], s[64:65], 0, v[196:197]
	s_mov_b32 m0, s2
	s_nop 0
	global_load_lds_dwordx4 v[210:211], off
	s_add_i32 m0, s2, 0x2000
	s_add_u32 s66, s64, 0x20000
	v_lshl_add_u64 v[212:213], s[64:65], 0, v[200:201]
	s_addc_u32 s67, s65, 0
	s_add_i32 s2, s81, s49
	global_load_lds_dwordx4 v[212:213], off
	v_lshl_add_u64 v[214:215], s[66:67], 0, v[196:197]
	s_mov_b32 m0, s2
	s_nop 0
	global_load_lds_dwordx4 v[214:215], off
	s_add_i32 m0, s2, 0x2000
	s_add_u32 s62, s62, s68
	v_lshl_add_u64 v[214:215], s[66:67], 0, v[200:201]
	s_addc_u32 s63, s63, 0
	global_load_lds_dwordx4 v[214:215], off
	v_lshl_add_u64 v[214:215], s[62:63], 0, v[194:195]
	s_mov_b32 m0, s50
	v_lshl_add_u64 v[216:217], s[62:63], 0, v[198:199]
	global_load_lds_dwordx4 v[214:215], off
	s_mov_b32 m0, s51
	s_nop 0
	global_load_lds_dwordx4 v[216:217], off
	ds_read_b128 v[162:165], v209 offset:16384
	ds_read_b128 v[166:169], v209 offset:17408
	ds_read_b128 v[170:173], v209 offset:18432
	ds_read_b128 v[174:177], v209 offset:19456
	ds_read_b128 v[178:181], v209 offset:20480
	ds_read_b128 v[182:185], v209 offset:21504
	ds_read_b128 v[186:189], v209 offset:22528
	ds_read_b128 v[190:193], v209 offset:23552
	s_waitcnt vmcnt(8)
	s_waitcnt lgkmcnt(0)
	s_barrier
	s_waitcnt lgkmcnt(0)
	v_mfma_f32_16x16x32_bf16 v[126:129], v[130:133], v[162:165], v[126:129]
	v_mfma_f32_16x16x32_bf16 v[122:125], v[138:141], v[162:165], v[122:125]
	v_mfma_f32_16x16x32_bf16 v[110:113], v[130:133], v[170:173], v[110:113]
	v_mfma_f32_16x16x32_bf16 v[106:109], v[138:141], v[170:173], v[106:109]
	v_mfma_f32_16x16x32_bf16 v[94:97], v[130:133], v[178:181], v[94:97]
	v_mfma_f32_16x16x32_bf16 v[90:93], v[138:141], v[178:181], v[90:93]
	v_mfma_f32_16x16x32_bf16 v[22:25], v[130:133], v[186:189], v[22:25]
	v_mfma_f32_16x16x32_bf16 v[14:17], v[138:141], v[186:189], v[14:17]
	v_mfma_f32_16x16x32_bf16 v[126:129], v[134:137], v[166:169], v[126:129]
	v_mfma_f32_16x16x32_bf16 v[122:125], v[142:145], v[166:169], v[122:125]
	v_mfma_f32_16x16x32_bf16 v[110:113], v[134:137], v[174:177], v[110:113]
	v_mfma_f32_16x16x32_bf16 v[106:109], v[142:145], v[174:177], v[106:109]
	v_mfma_f32_16x16x32_bf16 v[94:97], v[134:137], v[182:185], v[94:97]
	v_mfma_f32_16x16x32_bf16 v[90:93], v[142:145], v[182:185], v[90:93]
	v_mfma_f32_16x16x32_bf16 v[22:25], v[134:137], v[190:193], v[22:25]
	v_mfma_f32_16x16x32_bf16 v[14:17], v[142:145], v[190:193], v[14:17]
	v_mfma_f32_16x16x32_bf16 v[118:121], v[146:149], v[162:165], v[118:121]
	v_mfma_f32_16x16x32_bf16 v[114:117], v[154:157], v[162:165], v[114:117]
	v_mfma_f32_16x16x32_bf16 v[102:105], v[146:149], v[170:173], v[102:105]
	v_mfma_f32_16x16x32_bf16 v[98:101], v[154:157], v[170:173], v[98:101]
	v_mfma_f32_16x16x32_bf16 v[38:41], v[146:149], v[178:181], v[38:41]
	v_mfma_f32_16x16x32_bf16 v[30:33], v[154:157], v[178:181], v[30:33]
	v_mfma_f32_16x16x32_bf16 v[6:9], v[146:149], v[186:189], v[6:9]
	v_mfma_f32_16x16x32_bf16 v[2:5], v[154:157], v[186:189], v[2:5]
	v_mfma_f32_16x16x32_bf16 v[118:121], v[150:153], v[166:169], v[118:121]
	v_mfma_f32_16x16x32_bf16 v[114:117], v[158:161], v[166:169], v[114:117]
	v_mfma_f32_16x16x32_bf16 v[102:105], v[150:153], v[174:177], v[102:105]
	v_mfma_f32_16x16x32_bf16 v[98:101], v[158:161], v[174:177], v[98:101]
	v_mfma_f32_16x16x32_bf16 v[38:41], v[150:153], v[182:185], v[38:41]
	v_mfma_f32_16x16x32_bf16 v[30:33], v[158:161], v[182:185], v[30:33]
	v_mfma_f32_16x16x32_bf16 v[6:9], v[150:153], v[190:193], v[6:9]
	v_mfma_f32_16x16x32_bf16 v[2:5], v[158:161], v[190:193], v[2:5]
	s_barrier
	s_add_u32 s62, s62, 0x20000
	s_addc_u32 s63, s63, 0
	s_mov_b32 m0, s52
	v_lshl_add_u64 v[218:219], s[62:63], 0, v[194:195]
	global_load_lds_dwordx4 v[218:219], off
	v_lshl_add_u64 v[218:219], s[62:63], 0, v[198:199]
	s_mov_b32 m0, s53
	s_nop 0
	global_load_lds_dwordx4 v[218:219], off
	s_add_i32 s2, 0, 0x18000
	s_add_i32 s66, 0, 0x1c000
	v_add_u32_e32 v130, s2, v205
	v_add_u32_e32 v142, s66, v205
	ds_read_b128 v[146:149], v130
	ds_read_b128 v[150:153], v130 offset:1024
	ds_read_b128 v[154:157], v130 offset:2048
	ds_read_b128 v[158:161], v130 offset:3072
	ds_read_b128 v[130:133], v142
	ds_read_b128 v[134:137], v142 offset:1024
	ds_read_b128 v[138:141], v142 offset:2048
	ds_read_b128 v[142:145], v142 offset:3072
	ds_read_b128 v[162:165], v209 offset:32768
	ds_read_b128 v[166:169], v209 offset:33792
	ds_read_b128 v[170:173], v209 offset:34816
	ds_read_b128 v[174:177], v209 offset:35840
	ds_read_b128 v[178:181], v209 offset:36864
	ds_read_b128 v[182:185], v209 offset:37888
	ds_read_b128 v[186:189], v209 offset:38912
	ds_read_b128 v[190:193], v209 offset:39936
	s_waitcnt vmcnt(8)
	s_waitcnt lgkmcnt(0)
	s_barrier
	s_waitcnt lgkmcnt(0)
	v_mfma_f32_16x16x32_bf16 v[86:89], v[146:149], v[162:165], v[86:89]
	v_mfma_f32_16x16x32_bf16 v[82:85], v[154:157], v[162:165], v[82:85]
	v_mfma_f32_16x16x32_bf16 v[78:81], v[146:149], v[170:173], v[78:81]
	v_mfma_f32_16x16x32_bf16 v[74:77], v[154:157], v[170:173], v[74:77]
	v_mfma_f32_16x16x32_bf16 v[70:73], v[146:149], v[178:181], v[70:73]
	v_mfma_f32_16x16x32_bf16 v[66:69], v[154:157], v[178:181], v[66:69]
	v_mfma_f32_16x16x32_bf16 v[62:65], v[146:149], v[186:189], v[62:65]
	v_mfma_f32_16x16x32_bf16 v[58:61], v[154:157], v[186:189], v[58:61]
	v_mfma_f32_16x16x32_bf16 v[86:89], v[150:153], v[166:169], v[86:89]
	v_mfma_f32_16x16x32_bf16 v[82:85], v[158:161], v[166:169], v[82:85]
	v_mfma_f32_16x16x32_bf16 v[78:81], v[150:153], v[174:177], v[78:81]
	v_mfma_f32_16x16x32_bf16 v[74:77], v[158:161], v[174:177], v[74:77]
	v_mfma_f32_16x16x32_bf16 v[70:73], v[150:153], v[182:185], v[70:73]
	v_mfma_f32_16x16x32_bf16 v[66:69], v[158:161], v[182:185], v[66:69]
	v_mfma_f32_16x16x32_bf16 v[62:65], v[150:153], v[190:193], v[62:65]
	v_mfma_f32_16x16x32_bf16 v[58:61], v[158:161], v[190:193], v[58:61]
	v_mfma_f32_16x16x32_bf16 v[54:57], v[130:133], v[162:165], v[54:57]
	v_mfma_f32_16x16x32_bf16 v[50:53], v[138:141], v[162:165], v[50:53]
	v_mfma_f32_16x16x32_bf16 v[46:49], v[130:133], v[170:173], v[46:49]
	v_mfma_f32_16x16x32_bf16 v[42:45], v[138:141], v[170:173], v[42:45]
	v_mfma_f32_16x16x32_bf16 v[34:37], v[130:133], v[178:181], v[34:37]
	v_mfma_f32_16x16x32_bf16 v[26:29], v[138:141], v[178:181], v[26:29]
	v_mfma_f32_16x16x32_bf16 v[18:21], v[130:133], v[186:189], v[18:21]
	v_mfma_f32_16x16x32_bf16 v[10:13], v[138:141], v[186:189], v[10:13]
	v_mfma_f32_16x16x32_bf16 v[54:57], v[134:137], v[166:169], v[54:57]
	v_mfma_f32_16x16x32_bf16 v[50:53], v[142:145], v[166:169], v[50:53]
	v_mfma_f32_16x16x32_bf16 v[46:49], v[134:137], v[174:177], v[46:49]
	v_mfma_f32_16x16x32_bf16 v[42:45], v[142:145], v[174:177], v[42:45]
	v_mfma_f32_16x16x32_bf16 v[34:37], v[134:137], v[182:185], v[34:37]
	v_mfma_f32_16x16x32_bf16 v[26:29], v[142:145], v[182:185], v[26:29]
	v_mfma_f32_16x16x32_bf16 v[18:21], v[134:137], v[190:193], v[18:21]
	v_mfma_f32_16x16x32_bf16 v[10:13], v[142:145], v[190:193], v[10:13]
	s_barrier
	s_add_i32 s2, s2, s49
	v_lshl_add_u64 v[210:211], v[210:211], 0, s[12:13]
	s_mov_b32 m0, s2
	s_nop 0
	global_load_lds_dwordx4 v[210:211], off
	s_add_i32 m0, s2, 0x2000
	s_add_u32 s62, s64, 0x20080
	v_lshl_add_u64 v[210:211], v[212:213], 0, s[12:13]
	s_addc_u32 s63, s65, 0
	s_add_i32 s2, s66, s49
	global_load_lds_dwordx4 v[210:211], off
	v_lshl_add_u64 v[210:211], s[62:63], 0, v[196:197]
	s_mov_b32 m0, s2
	s_andn2_b64 vcc, exec, s[60:61]
	global_load_lds_dwordx4 v[210:211], off
	v_lshl_add_u64 v[210:211], s[62:63], 0, v[200:201]
	s_add_i32 m0, s2, 0x2000
	s_nop 0
	global_load_lds_dwordx4 v[210:211], off
	v_lshl_add_u64 v[210:211], v[214:215], 0, s[12:13]
	s_mov_b32 m0, s73
	s_nop 0
	global_load_lds_dwordx4 v[210:211], off
	v_lshl_add_u64 v[210:211], v[216:217], 0, s[12:13]
	s_mov_b32 m0, s74
	s_nop 0
	global_load_lds_dwordx4 v[210:211], off
	ds_read_b128 v[186:189], v209 offset:49152
	ds_read_b128 v[190:193], v209 offset:50176
	ds_read_b128 v[178:181], v209 offset:51200
	ds_read_b128 v[182:185], v209 offset:52224
	ds_read_b128 v[170:173], v209 offset:53248
	ds_read_b128 v[174:177], v209 offset:54272
	ds_read_b128 v[162:165], v209 offset:55296
	ds_read_b128 v[166:169], v209 offset:56320
	s_waitcnt vmcnt(8)
	s_waitcnt lgkmcnt(0)
	s_barrier
	s_cbranch_vccnz .LBB0_1104
	v_pk_mul_f32 v[214:215], v[86:87], s[20:21] op_sel_hi:[1,0]
	v_pk_mul_f32 v[216:217], v[82:83], s[20:21] op_sel_hi:[1,0]
	v_mov_b32_e32 v218, 0
	v_mov_b32_e32 v219, 0
	v_cvt_pk_fp8_f32 v218, v214, v215
	v_cvt_pk_fp8_f32 v219, v216, v217
	v_pk_mul_f32 v[214:215], v[88:89], s[20:21] op_sel_hi:[1,0]
	v_pk_mul_f32 v[216:217], v[84:85], s[20:21] op_sel_hi:[1,0]
	v_cvt_pk_fp8_f32 v218, v214, v215 op_sel:[0,0,1]
	v_cvt_pk_fp8_f32 v219, v216, v217 op_sel:[0,0,1]
	v_pk_mul_f32 v[214:215], v[54:55], s[20:21] op_sel_hi:[1,0]
	v_pk_mul_f32 v[216:217], v[50:51], s[20:21] op_sel_hi:[1,0]
	v_mov_b32_e32 v220, 0
	v_mov_b32_e32 v221, 0
	v_mov_b32_e32 v210, v1
	v_mov_b32_e32 v211, v204
	v_cvt_pk_fp8_f32 v220, v214, v215
	v_cvt_pk_fp8_f32 v221, v216, v217
	v_pk_mul_f32 v[214:215], v[56:57], s[20:21] op_sel_hi:[1,0]
	v_add_u32_e32 v210, s85, v210
	v_lshl_add_u32 v212, v211, 3, s86
	v_ashrrev_i32_e32 v211, 31, v210
	v_pk_mul_f32 v[216:217], v[52:53], s[20:21] op_sel_hi:[1,0]
	v_lshlrev_b64 v[210:211], 11, v[210:211]
	v_cvt_pk_fp8_f32 v220, v214, v215 op_sel:[0,0,1]
	v_cvt_pk_fp8_f32 v221, v216, v217 op_sel:[0,0,1]
	v_ashrrev_i32_e32 v213, 31, v212
	v_lshl_add_u64 v[210:211], s[10:11], 0, v[210:211]
	v_lshl_add_u64 v[210:211], v[210:211], 0, v[212:213]
	global_store_dwordx2 v[210:211], v[218:219], off
	global_store_dwordx2 v[210:211], v[220:221], off offset:128
	v_pk_mul_f32 v[214:215], v[78:79], s[20:21] op_sel_hi:[1,0]
	v_pk_mul_f32 v[216:217], v[74:75], s[20:21] op_sel_hi:[1,0]
	v_mov_b32_e32 v218, 0
	v_mov_b32_e32 v219, 0
	v_cvt_pk_fp8_f32 v218, v214, v215
	v_cvt_pk_fp8_f32 v219, v216, v217
	v_pk_mul_f32 v[214:215], v[80:81], s[20:21] op_sel_hi:[1,0]
	v_pk_mul_f32 v[216:217], v[76:77], s[20:21] op_sel_hi:[1,0]
	v_cvt_pk_fp8_f32 v218, v214, v215 op_sel:[0,0,1]
	v_cvt_pk_fp8_f32 v219, v216, v217 op_sel:[0,0,1]
	v_pk_mul_f32 v[214:215], v[46:47], s[20:21] op_sel_hi:[1,0]
	v_pk_mul_f32 v[216:217], v[42:43], s[20:21] op_sel_hi:[1,0]
	v_mov_b32_e32 v220, 0
	v_mov_b32_e32 v221, 0
	v_cvt_pk_fp8_f32 v220, v214, v215
	v_cvt_pk_fp8_f32 v221, v216, v217
	v_pk_mul_f32 v[214:215], v[48:49], s[20:21] op_sel_hi:[1,0]
	v_pk_mul_f32 v[216:217], v[44:45], s[20:21] op_sel_hi:[1,0]
	v_cvt_pk_fp8_f32 v220, v214, v215 op_sel:[0,0,1]
	v_cvt_pk_fp8_f32 v221, v216, v217 op_sel:[0,0,1]
	s_mov_b32 s2, 0x8000
	v_add_co_u32_e32 v214, vcc, s2, v210
	s_mov_b64 s[60:61], 0x8000
	s_nop 0
	v_addc_co_u32_e32 v215, vcc, 0, v211, vcc
	v_lshl_add_u64 v[212:213], v[210:211], 0, s[60:61]
	global_store_dwordx2 v[214:215], v[218:219], off
	global_store_dwordx2 v[212:213], v[220:221], off offset:128
	v_pk_mul_f32 v[214:215], v[70:71], s[20:21] op_sel_hi:[1,0]
	v_pk_mul_f32 v[216:217], v[66:67], s[20:21] op_sel_hi:[1,0]
	v_mov_b32_e32 v218, 0
	v_mov_b32_e32 v219, 0
	v_cvt_pk_fp8_f32 v218, v214, v215
	v_cvt_pk_fp8_f32 v219, v216, v217
	v_pk_mul_f32 v[214:215], v[72:73], s[20:21] op_sel_hi:[1,0]
	v_pk_mul_f32 v[216:217], v[68:69], s[20:21] op_sel_hi:[1,0]
	v_cvt_pk_fp8_f32 v218, v214, v215 op_sel:[0,0,1]
	v_cvt_pk_fp8_f32 v219, v216, v217 op_sel:[0,0,1]
	v_pk_mul_f32 v[214:215], v[34:35], s[20:21] op_sel_hi:[1,0]
	v_pk_mul_f32 v[216:217], v[26:27], s[20:21] op_sel_hi:[1,0]
	v_mov_b32_e32 v220, 0
	v_mov_b32_e32 v221, 0
	v_cvt_pk_fp8_f32 v220, v214, v215
	v_cvt_pk_fp8_f32 v221, v216, v217
	v_pk_mul_f32 v[214:215], v[36:37], s[20:21] op_sel_hi:[1,0]
	v_pk_mul_f32 v[216:217], v[28:29], s[20:21] op_sel_hi:[1,0]
	v_cvt_pk_fp8_f32 v220, v214, v215 op_sel:[0,0,1]
	v_cvt_pk_fp8_f32 v221, v216, v217 op_sel:[0,0,1]
	s_mov_b32 s2, 0x10000
	v_add_co_u32_e32 v214, vcc, s2, v210
	v_lshl_add_u64 v[212:213], v[210:211], 0, s[24:25]
	s_nop 0
	v_addc_co_u32_e32 v215, vcc, 0, v211, vcc
	global_store_dwordx2 v[214:215], v[218:219], off
	global_store_dwordx2 v[212:213], v[220:221], off offset:128
	v_pk_mul_f32 v[214:215], v[62:63], s[20:21] op_sel_hi:[1,0]
	v_pk_mul_f32 v[216:217], v[58:59], s[20:21] op_sel_hi:[1,0]
	v_mov_b32_e32 v218, 0
	v_mov_b32_e32 v219, 0
	v_cvt_pk_fp8_f32 v218, v214, v215
	v_cvt_pk_fp8_f32 v219, v216, v217
	v_pk_mul_f32 v[214:215], v[64:65], s[20:21] op_sel_hi:[1,0]
	v_pk_mul_f32 v[216:217], v[60:61], s[20:21] op_sel_hi:[1,0]
	v_cvt_pk_fp8_f32 v218, v214, v215 op_sel:[0,0,1]
	v_cvt_pk_fp8_f32 v219, v216, v217 op_sel:[0,0,1]
	v_pk_mul_f32 v[214:215], v[18:19], s[20:21] op_sel_hi:[1,0]
	v_pk_mul_f32 v[216:217], v[10:11], s[20:21] op_sel_hi:[1,0]
	v_mov_b32_e32 v220, 0
	v_mov_b32_e32 v221, 0
	v_cvt_pk_fp8_f32 v220, v214, v215
	v_cvt_pk_fp8_f32 v221, v216, v217
	v_pk_mul_f32 v[214:215], v[20:21], s[20:21] op_sel_hi:[1,0]
	v_pk_mul_f32 v[216:217], v[12:13], s[20:21] op_sel_hi:[1,0]
	v_cvt_pk_fp8_f32 v220, v214, v215 op_sel:[0,0,1]
	v_cvt_pk_fp8_f32 v221, v216, v217 op_sel:[0,0,1]
	s_mov_b32 s2, 0x18000
	v_lshl_add_u64 v[212:213], v[210:211], 0, s[28:29]
	v_add_co_u32_e32 v210, vcc, s2, v210
	s_nop 1
	v_addc_co_u32_e32 v211, vcc, 0, v211, vcc
	global_store_dwordx2 v[210:211], v[218:219], off
	global_store_dwordx2 v[212:213], v[220:221], off offset:128
	s_branch .LBB0_1104

.LBB0_1294:
	s_mov_b64 s[56:57], s[40:41]
	s_add_u32 s2, s71, s56
	s_addc_u32 s22, s72, s57
	s_add_u32 s40, s56, 0x100
	s_addc_u32 s41, s57, 0
	s_cmp_eq_u32 s73, 28
	s_cselect_b64 s[8:9], -1, 0
	s_and_b64 s[12:13], s[8:9], exec
	s_cselect_b32 s61, s67, s22
	s_cselect_b32 s60, s68, s2
	s_cselect_b32 s2, 0, s40
	s_add_i32 s22, s86, s42
	s_add_i32 m0, s51, 0xc000
	s_add_i32 s13, s51, 0xe000
	s_add_i32 s23, s22, 0x2000
	s_add_u32 s62, s60, 0x80000
	s_addc_u32 s63, s61, 0
	s_add_i32 s24, s87, s42
	s_add_i32 s25, s24, 0x2000
	s_and_b64 s[8:9], s[6:7], s[8:9]
	ds_read_b128 v[130:133], v229
	ds_read_b128 v[134:137], v229 offset:1024
	ds_read_b128 v[138:141], v229 offset:2048
	ds_read_b128 v[142:145], v229 offset:3072
	ds_read_b128 v[146:149], v230
	ds_read_b128 v[150:153], v230 offset:1024
	ds_read_b128 v[154:157], v230 offset:2048
	ds_read_b128 v[158:161], v230 offset:3072
	s_and_b64 s[8:9], s[8:9], exec
	s_cselect_b32 s9, s30, s36
	s_cselect_b32 s8, s31, s37
	s_add_u32 s64, s9, s2
	s_addc_u32 s65, s8, 0
	s_add_i32 s82, 0, 0x18000
	s_add_i32 s83, 0, 0x1c000
	s_add_u32 s58, s64, 0x80000
	s_addc_u32 s59, s65, 0
	s_add_i32 s8, s82, s42
	s_add_i32 s2, s8, 0x2000
	s_add_u32 s54, s60, 0x80080
	s_addc_u32 s55, s61, 0
	s_add_i32 s12, s83, s42
	s_add_i32 s9, s12, 0x2000
	s_cmp_lg_u32 s73, 28
	v_lshl_add_u64 v[224:225], v[220:221], 0, s[56:57]
	ds_read_b128 v[162:165], v231
	ds_read_b128 v[166:169], v231 offset:1024
	ds_read_b128 v[170:173], v231 offset:2048
	ds_read_b128 v[174:177], v231 offset:3072
	ds_read_b128 v[178:181], v231 offset:4096
	ds_read_b128 v[182:185], v231 offset:5120
	ds_read_b128 v[186:189], v231 offset:6144
	ds_read_b128 v[190:193], v231 offset:7168
	global_load_lds_dwordx4 v[224:225], off
	v_lshl_add_u64 v[224:225], v[222:223], 0, s[56:57]
	s_mov_b32 m0, s13
	s_nop 0
	global_load_lds_dwordx4 v[224:225], off
	s_waitcnt vmcnt(8)
	s_waitcnt lgkmcnt(0)
	s_barrier
	s_waitcnt lgkmcnt(0)
	v_mfma_f32_16x16x32_bf16 v[62:65], v[130:133], v[162:165], v[62:65]
	v_mfma_f32_16x16x32_bf16 v[58:61], v[138:141], v[162:165], v[58:61]
	v_mfma_f32_16x16x32_bf16 v[54:57], v[130:133], v[170:173], v[54:57]
	v_mfma_f32_16x16x32_bf16 v[50:53], v[138:141], v[170:173], v[50:53]
	v_mfma_f32_16x16x32_bf16 v[46:49], v[130:133], v[178:181], v[46:49]
	v_mfma_f32_16x16x32_bf16 v[42:45], v[138:141], v[178:181], v[42:45]
	v_mfma_f32_16x16x32_bf16 v[38:41], v[130:133], v[186:189], v[38:41]
	v_mfma_f32_16x16x32_bf16 v[34:37], v[138:141], v[186:189], v[34:37]
	v_mfma_f32_16x16x32_bf16 v[62:65], v[134:137], v[166:169], v[62:65]
	v_mfma_f32_16x16x32_bf16 v[58:61], v[142:145], v[166:169], v[58:61]
	v_mfma_f32_16x16x32_bf16 v[54:57], v[134:137], v[174:177], v[54:57]
	v_mfma_f32_16x16x32_bf16 v[50:53], v[142:145], v[174:177], v[50:53]
	v_mfma_f32_16x16x32_bf16 v[46:49], v[134:137], v[182:185], v[46:49]
	v_mfma_f32_16x16x32_bf16 v[42:45], v[142:145], v[182:185], v[42:45]
	v_mfma_f32_16x16x32_bf16 v[38:41], v[134:137], v[190:193], v[38:41]
	v_mfma_f32_16x16x32_bf16 v[34:37], v[142:145], v[190:193], v[34:37]
	v_mfma_f32_16x16x32_bf16 v[30:33], v[146:149], v[162:165], v[30:33]
	v_mfma_f32_16x16x32_bf16 v[26:29], v[154:157], v[162:165], v[26:29]
	v_mfma_f32_16x16x32_bf16 v[22:25], v[146:149], v[170:173], v[22:25]
	v_mfma_f32_16x16x32_bf16 v[18:21], v[154:157], v[170:173], v[18:21]
	v_mfma_f32_16x16x32_bf16 v[14:17], v[146:149], v[178:181], v[14:17]
	v_mfma_f32_16x16x32_bf16 v[10:13], v[154:157], v[178:181], v[10:13]
	v_mfma_f32_16x16x32_bf16 v[6:9], v[146:149], v[186:189], v[6:9]
	v_mfma_f32_16x16x32_bf16 v[2:5], v[154:157], v[186:189], v[2:5]
	v_mfma_f32_16x16x32_bf16 v[30:33], v[150:153], v[166:169], v[30:33]
	v_mfma_f32_16x16x32_bf16 v[26:29], v[158:161], v[166:169], v[26:29]
	v_mfma_f32_16x16x32_bf16 v[22:25], v[150:153], v[174:177], v[22:25]
	v_mfma_f32_16x16x32_bf16 v[18:21], v[158:161], v[174:177], v[18:21]
	v_mfma_f32_16x16x32_bf16 v[14:17], v[150:153], v[182:185], v[14:17]
	v_mfma_f32_16x16x32_bf16 v[10:13], v[158:161], v[182:185], v[10:13]
	v_mfma_f32_16x16x32_bf16 v[6:9], v[150:153], v[190:193], v[6:9]
	v_mfma_f32_16x16x32_bf16 v[2:5], v[158:161], v[190:193], v[2:5]
	s_barrier
	s_mov_b32 m0, s22
	v_lshl_add_u64 v[224:225], s[60:61], 0, v[196:197]
	global_load_lds_dwordx4 v[224:225], off
	v_lshl_add_u64 v[232:233], s[60:61], 0, v[200:201]
	s_mov_b32 m0, s23
	v_lshl_add_u64 v[234:235], s[62:63], 0, v[196:197]
	global_load_lds_dwordx4 v[232:233], off
	s_mov_b32 m0, s24
	v_lshl_add_u64 v[236:237], s[64:65], 0, v[198:199]
	global_load_lds_dwordx4 v[234:235], off
	v_lshl_add_u64 v[234:235], s[62:63], 0, v[200:201]
	s_mov_b32 m0, s25
	s_nop 0
	global_load_lds_dwordx4 v[234:235], off
	v_lshl_add_u64 v[234:235], s[64:65], 0, v[194:195]
	s_mov_b32 m0, s51
	s_nop 0
	global_load_lds_dwordx4 v[234:235], off
	s_mov_b32 m0, s52
	s_nop 0
	global_load_lds_dwordx4 v[236:237], off
	ds_read_b128 v[162:165], v231 offset:16384
	ds_read_b128 v[166:169], v231 offset:17408
	ds_read_b128 v[170:173], v231 offset:18432
	ds_read_b128 v[174:177], v231 offset:19456
	ds_read_b128 v[178:181], v231 offset:20480
	ds_read_b128 v[182:185], v231 offset:21504
	ds_read_b128 v[186:189], v231 offset:22528
	ds_read_b128 v[190:193], v231 offset:23552
	s_waitcnt vmcnt(8)
	s_waitcnt lgkmcnt(0)
	s_barrier
	s_waitcnt lgkmcnt(0)
	v_mfma_f32_16x16x32_bf16 v[126:129], v[130:133], v[162:165], v[126:129]
	v_mfma_f32_16x16x32_bf16 v[122:125], v[138:141], v[162:165], v[122:125]
	v_mfma_f32_16x16x32_bf16 v[114:117], v[130:133], v[170:173], v[114:117]
	v_mfma_f32_16x16x32_bf16 v[106:109], v[138:141], v[170:173], v[106:109]
	v_mfma_f32_16x16x32_bf16 v[102:105], v[130:133], v[178:181], v[102:105]
	v_mfma_f32_16x16x32_bf16 v[94:97], v[138:141], v[178:181], v[94:97]
	v_mfma_f32_16x16x32_bf16 v[86:89], v[130:133], v[186:189], v[86:89]
	v_mfma_f32_16x16x32_bf16 v[78:81], v[138:141], v[186:189], v[78:81]
	v_mfma_f32_16x16x32_bf16 v[126:129], v[134:137], v[166:169], v[126:129]
	v_mfma_f32_16x16x32_bf16 v[122:125], v[142:145], v[166:169], v[122:125]
	v_mfma_f32_16x16x32_bf16 v[114:117], v[134:137], v[174:177], v[114:117]
	v_mfma_f32_16x16x32_bf16 v[106:109], v[142:145], v[174:177], v[106:109]
	v_mfma_f32_16x16x32_bf16 v[102:105], v[134:137], v[182:185], v[102:105]
	v_mfma_f32_16x16x32_bf16 v[94:97], v[142:145], v[182:185], v[94:97]
	v_mfma_f32_16x16x32_bf16 v[86:89], v[134:137], v[190:193], v[86:89]
	v_mfma_f32_16x16x32_bf16 v[78:81], v[142:145], v[190:193], v[78:81]
	v_mfma_f32_16x16x32_bf16 v[118:121], v[146:149], v[162:165], v[118:121]
	v_mfma_f32_16x16x32_bf16 v[110:113], v[154:157], v[162:165], v[110:113]
	v_mfma_f32_16x16x32_bf16 v[98:101], v[146:149], v[170:173], v[98:101]
	v_mfma_f32_16x16x32_bf16 v[90:93], v[154:157], v[170:173], v[90:93]
	v_mfma_f32_16x16x32_bf16 v[82:85], v[146:149], v[178:181], v[82:85]
	v_mfma_f32_16x16x32_bf16 v[74:77], v[154:157], v[178:181], v[74:77]
	v_mfma_f32_16x16x32_bf16 v[70:73], v[146:149], v[186:189], v[70:73]
	v_mfma_f32_16x16x32_bf16 v[66:69], v[154:157], v[186:189], v[66:69]
	v_mfma_f32_16x16x32_bf16 v[118:121], v[150:153], v[166:169], v[118:121]
	v_mfma_f32_16x16x32_bf16 v[110:113], v[158:161], v[166:169], v[110:113]
	v_mfma_f32_16x16x32_bf16 v[98:101], v[150:153], v[174:177], v[98:101]
	v_mfma_f32_16x16x32_bf16 v[90:93], v[158:161], v[174:177], v[90:93]
	v_mfma_f32_16x16x32_bf16 v[82:85], v[150:153], v[182:185], v[82:85]
	v_mfma_f32_16x16x32_bf16 v[74:77], v[158:161], v[182:185], v[74:77]
	v_mfma_f32_16x16x32_bf16 v[70:73], v[150:153], v[190:193], v[70:73]
	v_mfma_f32_16x16x32_bf16 v[66:69], v[158:161], v[190:193], v[66:69]
	s_barrier
	s_mov_b32 m0, s53
	v_lshl_add_u64 v[238:239], s[58:59], 0, v[194:195]
	global_load_lds_dwordx4 v[238:239], off
	v_lshl_add_u64 v[238:239], s[58:59], 0, v[198:199]
	s_mov_b32 m0, s74
	s_nop 0
	global_load_lds_dwordx4 v[238:239], off
	v_add_u32_e32 v130, s82, v227
	v_add_u32_e32 v142, s83, v227
	ds_read_b128 v[146:149], v130
	ds_read_b128 v[150:153], v130 offset:1024
	ds_read_b128 v[154:157], v130 offset:2048
	ds_read_b128 v[158:161], v130 offset:3072
	ds_read_b128 v[130:133], v142
	ds_read_b128 v[134:137], v142 offset:1024
	ds_read_b128 v[138:141], v142 offset:2048
	ds_read_b128 v[142:145], v142 offset:3072
	ds_read_b128 v[162:165], v231 offset:32768
	ds_read_b128 v[166:169], v231 offset:33792
	ds_read_b128 v[170:173], v231 offset:34816
	ds_read_b128 v[174:177], v231 offset:35840
	ds_read_b128 v[178:181], v231 offset:36864
	ds_read_b128 v[182:185], v231 offset:37888
	ds_read_b128 v[186:189], v231 offset:38912
	ds_read_b128 v[190:193], v231 offset:39936
	s_waitcnt vmcnt(8)
	s_waitcnt lgkmcnt(0)
	s_barrier
	s_waitcnt lgkmcnt(0)
	v_mfma_f32_16x16x32_bf16 v[62:65], v[146:149], v[162:165], v[62:65]
	v_mfma_f32_16x16x32_bf16 v[58:61], v[154:157], v[162:165], v[58:61]
	v_mfma_f32_16x16x32_bf16 v[54:57], v[146:149], v[170:173], v[54:57]
	v_mfma_f32_16x16x32_bf16 v[50:53], v[154:157], v[170:173], v[50:53]
	v_mfma_f32_16x16x32_bf16 v[46:49], v[146:149], v[178:181], v[46:49]
	v_mfma_f32_16x16x32_bf16 v[42:45], v[154:157], v[178:181], v[42:45]
	v_mfma_f32_16x16x32_bf16 v[38:41], v[146:149], v[186:189], v[38:41]
	v_mfma_f32_16x16x32_bf16 v[34:37], v[154:157], v[186:189], v[34:37]
	v_mfma_f32_16x16x32_bf16 v[62:65], v[150:153], v[166:169], v[62:65]
	v_mfma_f32_16x16x32_bf16 v[58:61], v[158:161], v[166:169], v[58:61]
	v_mfma_f32_16x16x32_bf16 v[54:57], v[150:153], v[174:177], v[54:57]
	v_mfma_f32_16x16x32_bf16 v[50:53], v[158:161], v[174:177], v[50:53]
	v_mfma_f32_16x16x32_bf16 v[46:49], v[150:153], v[182:185], v[46:49]
	v_mfma_f32_16x16x32_bf16 v[42:45], v[158:161], v[182:185], v[42:45]
	v_mfma_f32_16x16x32_bf16 v[38:41], v[150:153], v[190:193], v[38:41]
	v_mfma_f32_16x16x32_bf16 v[34:37], v[158:161], v[190:193], v[34:37]
	v_mfma_f32_16x16x32_bf16 v[30:33], v[130:133], v[162:165], v[30:33]
	v_mfma_f32_16x16x32_bf16 v[26:29], v[138:141], v[162:165], v[26:29]
	v_mfma_f32_16x16x32_bf16 v[22:25], v[130:133], v[170:173], v[22:25]
	v_mfma_f32_16x16x32_bf16 v[18:21], v[138:141], v[170:173], v[18:21]
	v_mfma_f32_16x16x32_bf16 v[14:17], v[130:133], v[178:181], v[14:17]
	v_mfma_f32_16x16x32_bf16 v[10:13], v[138:141], v[178:181], v[10:13]
	v_mfma_f32_16x16x32_bf16 v[6:9], v[130:133], v[186:189], v[6:9]
	v_mfma_f32_16x16x32_bf16 v[2:5], v[138:141], v[186:189], v[2:5]
	v_mfma_f32_16x16x32_bf16 v[30:33], v[134:137], v[166:169], v[30:33]
	v_mfma_f32_16x16x32_bf16 v[26:29], v[142:145], v[166:169], v[26:29]
	v_mfma_f32_16x16x32_bf16 v[22:25], v[134:137], v[174:177], v[22:25]
	v_mfma_f32_16x16x32_bf16 v[18:21], v[142:145], v[174:177], v[18:21]
	v_mfma_f32_16x16x32_bf16 v[14:17], v[134:137], v[182:185], v[14:17]
	v_mfma_f32_16x16x32_bf16 v[10:13], v[142:145], v[182:185], v[10:13]
	v_mfma_f32_16x16x32_bf16 v[6:9], v[134:137], v[190:193], v[6:9]
	v_mfma_f32_16x16x32_bf16 v[2:5], v[142:145], v[190:193], v[2:5]
	s_barrier
	s_mov_b32 m0, s8
	v_lshl_add_u64 v[224:225], v[224:225], 0, s[18:19]
	global_load_lds_dwordx4 v[224:225], off
	v_lshl_add_u64 v[224:225], v[232:233], 0, s[18:19]
	s_mov_b32 m0, s2
	s_nop 0
	global_load_lds_dwordx4 v[224:225], off
	v_lshl_add_u64 v[224:225], s[54:55], 0, v[196:197]
	s_mov_b32 m0, s12
	s_nop 0
	global_load_lds_dwordx4 v[224:225], off
	v_lshl_add_u64 v[224:225], s[54:55], 0, v[200:201]
	s_mov_b32 m0, s9
	s_nop 0
	global_load_lds_dwordx4 v[224:225], off
	v_lshl_add_u64 v[224:225], v[234:235], 0, s[18:19]
	s_mov_b32 m0, s78
	s_nop 0
	global_load_lds_dwordx4 v[224:225], off
	v_lshl_add_u64 v[224:225], v[236:237], 0, s[18:19]
	s_mov_b32 m0, s79
	s_nop 0
	global_load_lds_dwordx4 v[224:225], off
	ds_read_b128 v[186:189], v231 offset:49152
	ds_read_b128 v[190:193], v231 offset:50176
	ds_read_b128 v[178:181], v231 offset:51200
	ds_read_b128 v[182:185], v231 offset:52224
	ds_read_b128 v[170:173], v231 offset:53248
	ds_read_b128 v[174:177], v231 offset:54272
	ds_read_b128 v[162:165], v231 offset:55296
	ds_read_b128 v[166:169], v231 offset:56320
	s_waitcnt vmcnt(8)
	s_waitcnt lgkmcnt(0)
	s_barrier
	s_cbranch_scc1 .LBB0_1293
	v_mov_b32_e32 v202, v1
	v_mov_b32_e32 v224, v209
	s_mov_b64 s[54:55], -1
	v_add_u32_e32 v202, s69, v202
	v_lshlrev_b32_e32 v224, 3, v224
	s_and_b64 vcc, exec, s[38:39]
	v_add_u32_e32 v234, 16, v202
	v_add_u32_e32 v233, 32, v202
	v_add_u32_e32 v232, 48, v202
	s_cbranch_vccz .LBB0_1297
	v_add_u32_e32 v236, s70, v224
	v_ashrrev_i32_e32 v237, 31, v236
	v_mov_b64_e32 v[240:241], s[14:15]
	v_mad_i64_i32 v[238:239], s[8:9], v202, s88, v[240:241]
	v_lshlrev_b64 v[244:245], 1, v[236:237]
	v_lshl_add_u64 v[246:247], v[238:239], 0, v[244:245]
	v_cvt_pk_bf16_f32 v236, v62, v63
	v_cvt_pk_bf16_f32 v237, v64, v65
	v_cvt_pk_bf16_f32 v238, v58, v59
	v_cvt_pk_bf16_f32 v239, v60, v61
	global_store_dwordx4 v[246:247], v[236:239], off
	s_mov_b64 s[54:55], 0
	s_nop 0
	v_cvt_pk_bf16_f32 v236, v30, v31
	v_cvt_pk_bf16_f32 v237, v32, v33
	v_cvt_pk_bf16_f32 v238, v26, v27
	v_cvt_pk_bf16_f32 v239, v28, v29
	global_store_dwordx4 v[246:247], v[236:239], off offset:256
	s_nop 1
	v_mad_i64_i32 v[236:237], s[8:9], v234, s88, v[240:241]
	v_lshl_add_u64 v[246:247], v[236:237], 0, v[244:245]
	v_cvt_pk_bf16_f32 v236, v54, v55
	v_cvt_pk_bf16_f32 v237, v56, v57
	v_cvt_pk_bf16_f32 v238, v50, v51
	v_cvt_pk_bf16_f32 v239, v52, v53
	global_store_dwordx4 v[246:247], v[236:239], off
	s_nop 1
	v_cvt_pk_bf16_f32 v236, v22, v23
	v_cvt_pk_bf16_f32 v237, v24, v25
	v_cvt_pk_bf16_f32 v238, v18, v19
	v_cvt_pk_bf16_f32 v239, v20, v21
	global_store_dwordx4 v[246:247], v[236:239], off offset:256
	s_nop 1
	v_mad_i64_i32 v[236:237], s[8:9], v233, s88, v[240:241]
	v_lshl_add_u64 v[246:247], v[236:237], 0, v[244:245]
	v_cvt_pk_bf16_f32 v236, v46, v47
	v_cvt_pk_bf16_f32 v237, v48, v49
	v_cvt_pk_bf16_f32 v238, v42, v43
	v_cvt_pk_bf16_f32 v239, v44, v45
	global_store_dwordx4 v[246:247], v[236:239], off
	s_nop 1
	v_cvt_pk_bf16_f32 v236, v14, v15
	v_cvt_pk_bf16_f32 v237, v16, v17
	v_cvt_pk_bf16_f32 v238, v10, v11
	v_cvt_pk_bf16_f32 v239, v12, v13
	global_store_dwordx4 v[246:247], v[236:239], off offset:256
	s_nop 1
	v_mad_i64_i32 v[236:237], s[8:9], v232, s88, v[240:241]
	v_lshl_add_u64 v[240:241], v[236:237], 0, v[244:245]
	v_cvt_pk_bf16_f32 v236, v38, v39
	v_cvt_pk_bf16_f32 v237, v40, v41
	v_cvt_pk_bf16_f32 v238, v34, v35
	v_cvt_pk_bf16_f32 v239, v36, v37
	global_store_dwordx4 v[240:241], v[236:239], off
	s_nop 1
	v_cvt_pk_bf16_f32 v236, v6, v7
	v_cvt_pk_bf16_f32 v237, v8, v9
	v_cvt_pk_bf16_f32 v238, v2, v3
	v_cvt_pk_bf16_f32 v239, v4, v5
	global_store_dwordx4 v[240:241], v[236:239], off offset:256

.LBB0_1547:
	s_add_u32 s2, s66, s54
	s_addc_u32 s69, s67, s55
	s_add_u32 s56, s54, 0x100
	s_addc_u32 s57, s55, 0
	s_cmp_eq_u32 s68, 28
	s_cselect_b64 s[60:61], -1, 0
	s_and_b64 s[58:59], s[60:61], exec
	s_cselect_b32 s59, s31, s69
	s_cselect_b32 s58, s35, s2
	s_cselect_b32 s2, 0, s56
	v_lshl_add_u64 v[178:179], v[130:131], 0, s[54:55]
	s_add_i32 m0, s13, 0xc000
	s_nop 0
	global_load_lds_dwordx4 v[178:179], off
	v_lshl_add_u64 v[178:179], v[132:133], 0, s[54:55]
	s_add_i32 m0, s13, 0xe000
	s_nop 0
	global_load_lds_dwordx4 v[178:179], off
	ds_read_b128 v[134:137], v189
	ds_read_b128 v[138:141], v189 offset:1024
	ds_read_b128 v[142:145], v189 offset:2048
	ds_read_b128 v[146:149], v189 offset:3072
	ds_read_b128 v[150:153], v190
	ds_read_b128 v[170:173], v190 offset:1024
	ds_read_b128 v[174:177], v190 offset:2048
	ds_read_b128 v[194:197], v190 offset:3072
	ds_read_b128 v[198:201], v191
	ds_read_b128 v[202:205], v191 offset:1024
	ds_read_b128 v[206:209], v191 offset:2048
	ds_read_b128 v[210:213], v191 offset:3072
	ds_read_b128 v[214:217], v191 offset:4096
	ds_read_b128 v[218:221], v191 offset:5120
	ds_read_b128 v[222:225], v191 offset:6144
	ds_read_b128 v[226:229], v191 offset:7168
	s_waitcnt vmcnt(8)
	s_waitcnt lgkmcnt(0)
	s_barrier
	s_waitcnt lgkmcnt(0)
	v_mfma_f32_16x16x32_bf16 v[126:129], v[134:137], v[198:201], v[126:129]
	v_mfma_f32_16x16x32_bf16 v[122:125], v[142:145], v[198:201], v[122:125]
	v_mfma_f32_16x16x32_bf16 v[110:113], v[134:137], v[206:209], v[110:113]
	v_mfma_f32_16x16x32_bf16 v[106:109], v[142:145], v[206:209], v[106:109]
	v_mfma_f32_16x16x32_bf16 v[94:97], v[134:137], v[214:217], v[94:97]
	v_mfma_f32_16x16x32_bf16 v[90:93], v[142:145], v[214:217], v[90:93]
	v_mfma_f32_16x16x32_bf16 v[78:81], v[134:137], v[222:225], v[78:81]
	v_mfma_f32_16x16x32_bf16 v[74:77], v[142:145], v[222:225], v[74:77]
	v_mfma_f32_16x16x32_bf16 v[126:129], v[138:141], v[202:205], v[126:129]
	v_mfma_f32_16x16x32_bf16 v[122:125], v[146:149], v[202:205], v[122:125]
	v_mfma_f32_16x16x32_bf16 v[110:113], v[138:141], v[210:213], v[110:113]
	v_mfma_f32_16x16x32_bf16 v[106:109], v[146:149], v[210:213], v[106:109]
	v_mfma_f32_16x16x32_bf16 v[94:97], v[138:141], v[218:221], v[94:97]
	v_mfma_f32_16x16x32_bf16 v[90:93], v[146:149], v[218:221], v[90:93]
	v_mfma_f32_16x16x32_bf16 v[78:81], v[138:141], v[226:229], v[78:81]
	v_mfma_f32_16x16x32_bf16 v[74:77], v[146:149], v[226:229], v[74:77]
	v_mfma_f32_16x16x32_bf16 v[118:121], v[150:153], v[198:201], v[118:121]
	v_mfma_f32_16x16x32_bf16 v[114:117], v[174:177], v[198:201], v[114:117]
	v_mfma_f32_16x16x32_bf16 v[102:105], v[150:153], v[206:209], v[102:105]
	v_mfma_f32_16x16x32_bf16 v[98:101], v[174:177], v[206:209], v[98:101]
	v_mfma_f32_16x16x32_bf16 v[86:89], v[150:153], v[214:217], v[86:89]
	v_mfma_f32_16x16x32_bf16 v[82:85], v[174:177], v[214:217], v[82:85]
	v_mfma_f32_16x16x32_bf16 v[70:73], v[150:153], v[222:225], v[70:73]
	v_mfma_f32_16x16x32_bf16 v[66:69], v[174:177], v[222:225], v[66:69]
	v_mfma_f32_16x16x32_bf16 v[118:121], v[170:173], v[202:205], v[118:121]
	v_mfma_f32_16x16x32_bf16 v[114:117], v[194:197], v[202:205], v[114:117]
	v_mfma_f32_16x16x32_bf16 v[102:105], v[170:173], v[210:213], v[102:105]
	v_mfma_f32_16x16x32_bf16 v[98:101], v[194:197], v[210:213], v[98:101]
	v_mfma_f32_16x16x32_bf16 v[86:89], v[170:173], v[218:221], v[86:89]
	v_mfma_f32_16x16x32_bf16 v[82:85], v[194:197], v[218:221], v[82:85]
	v_mfma_f32_16x16x32_bf16 v[70:73], v[170:173], v[226:229], v[70:73]
	v_mfma_f32_16x16x32_bf16 v[66:69], v[194:197], v[226:229], v[66:69]
	s_barrier
	s_add_i32 s54, s63, s42
	v_lshl_add_u64 v[178:179], s[58:59], 0, v[156:157]
	s_mov_b32 m0, s54
	s_nop 0
	global_load_lds_dwordx4 v[178:179], off
	s_add_i32 m0, s54, 0x2000
	s_add_u32 s54, s58, 0x80000
	v_lshl_add_u64 v[182:183], s[58:59], 0, v[160:161]
	s_addc_u32 s55, s59, 0
	s_add_i32 s69, s64, s42
	global_load_lds_dwordx4 v[182:183], off
	v_lshl_add_u64 v[186:187], s[54:55], 0, v[156:157]
	s_mov_b32 m0, s69
	s_nop 0
	global_load_lds_dwordx4 v[186:187], off
	v_lshl_add_u64 v[186:187], s[54:55], 0, v[160:161]
	s_add_i32 m0, s69, 0x2000
	s_and_b64 s[54:55], s[8:9], s[60:61]
	s_and_b64 s[54:55], s[54:55], exec
	s_cselect_b32 s54, s36, s40
	s_cselect_b32 s55, s37, s41
	s_add_u32 s54, s54, s2
	s_addc_u32 s55, s55, 0
	global_load_lds_dwordx4 v[186:187], off
	v_lshl_add_u64 v[186:187], s[54:55], 0, v[154:155]
	s_mov_b32 m0, s13
	v_lshl_add_u64 v[230:231], s[54:55], 0, v[158:159]
	global_load_lds_dwordx4 v[186:187], off
	s_mov_b32 m0, s43
	s_nop 0
	global_load_lds_dwordx4 v[230:231], off
	ds_read_b128 v[198:201], v191 offset:16384
	ds_read_b128 v[202:205], v191 offset:17408
	ds_read_b128 v[206:209], v191 offset:18432
	ds_read_b128 v[210:213], v191 offset:19456
	ds_read_b128 v[214:217], v191 offset:20480
	ds_read_b128 v[218:221], v191 offset:21504
	ds_read_b128 v[222:225], v191 offset:22528
	ds_read_b128 v[226:229], v191 offset:23552
	s_waitcnt vmcnt(8)
	s_waitcnt lgkmcnt(0)
	s_barrier
	s_waitcnt lgkmcnt(0)
	v_mfma_f32_16x16x32_bf16 v[62:65], v[134:137], v[198:201], v[62:65]
	v_mfma_f32_16x16x32_bf16 v[58:61], v[142:145], v[198:201], v[58:61]
	v_mfma_f32_16x16x32_bf16 v[46:49], v[134:137], v[206:209], v[46:49]
	v_mfma_f32_16x16x32_bf16 v[42:45], v[142:145], v[206:209], v[42:45]
	v_mfma_f32_16x16x32_bf16 v[30:33], v[134:137], v[214:217], v[30:33]
	v_mfma_f32_16x16x32_bf16 v[26:29], v[142:145], v[214:217], v[26:29]
	v_mfma_f32_16x16x32_bf16 v[14:17], v[134:137], v[222:225], v[14:17]
	v_mfma_f32_16x16x32_bf16 v[10:13], v[142:145], v[222:225], v[10:13]
	v_mfma_f32_16x16x32_bf16 v[62:65], v[138:141], v[202:205], v[62:65]
	v_mfma_f32_16x16x32_bf16 v[58:61], v[146:149], v[202:205], v[58:61]
	v_mfma_f32_16x16x32_bf16 v[46:49], v[138:141], v[210:213], v[46:49]
	v_mfma_f32_16x16x32_bf16 v[42:45], v[146:149], v[210:213], v[42:45]
	v_mfma_f32_16x16x32_bf16 v[30:33], v[138:141], v[218:221], v[30:33]
	v_mfma_f32_16x16x32_bf16 v[26:29], v[146:149], v[218:221], v[26:29]
	v_mfma_f32_16x16x32_bf16 v[14:17], v[138:141], v[226:229], v[14:17]
	v_mfma_f32_16x16x32_bf16 v[10:13], v[146:149], v[226:229], v[10:13]
	v_mfma_f32_16x16x32_bf16 v[54:57], v[150:153], v[198:201], v[54:57]
	v_mfma_f32_16x16x32_bf16 v[50:53], v[174:177], v[198:201], v[50:53]
	v_mfma_f32_16x16x32_bf16 v[38:41], v[150:153], v[206:209], v[38:41]
	v_mfma_f32_16x16x32_bf16 v[34:37], v[174:177], v[206:209], v[34:37]
	v_mfma_f32_16x16x32_bf16 v[22:25], v[150:153], v[214:217], v[22:25]
	v_mfma_f32_16x16x32_bf16 v[18:21], v[174:177], v[214:217], v[18:21]
	v_mfma_f32_16x16x32_bf16 v[6:9], v[150:153], v[222:225], v[6:9]
	v_mfma_f32_16x16x32_bf16 v[2:5], v[174:177], v[222:225], v[2:5]
	v_mfma_f32_16x16x32_bf16 v[54:57], v[170:173], v[202:205], v[54:57]
	v_mfma_f32_16x16x32_bf16 v[50:53], v[194:197], v[202:205], v[50:53]
	v_mfma_f32_16x16x32_bf16 v[38:41], v[170:173], v[210:213], v[38:41]
	v_mfma_f32_16x16x32_bf16 v[34:37], v[194:197], v[210:213], v[34:37]
	v_mfma_f32_16x16x32_bf16 v[22:25], v[170:173], v[218:221], v[22:25]
	v_mfma_f32_16x16x32_bf16 v[18:21], v[194:197], v[218:221], v[18:21]
	v_mfma_f32_16x16x32_bf16 v[6:9], v[170:173], v[226:229], v[6:9]
	v_mfma_f32_16x16x32_bf16 v[2:5], v[194:197], v[226:229], v[2:5]
	s_barrier
	s_add_u32 s54, s54, 0x80000
	s_addc_u32 s55, s55, 0
	s_mov_b32 m0, s48
	v_lshl_add_u64 v[232:233], s[54:55], 0, v[154:155]
	global_load_lds_dwordx4 v[232:233], off
	v_lshl_add_u64 v[232:233], s[54:55], 0, v[158:159]
	s_mov_b32 m0, s49
	s_nop 0
	global_load_lds_dwordx4 v[232:233], off
	s_add_i32 s2, 0, 0x18000
	s_add_i32 s60, 0, 0x1c000
	v_add_u32_e32 v146, s2, v181
	v_add_u32_e32 v180, s60, v181
	ds_read_b128 v[134:137], v146
	ds_read_b128 v[138:141], v146 offset:1024
	ds_read_b128 v[142:145], v146 offset:2048
	ds_read_b128 v[146:149], v146 offset:3072
	ds_read_b128 v[150:153], v180
	ds_read_b128 v[170:173], v180 offset:1024
	ds_read_b128 v[174:177], v180 offset:2048
	ds_read_b128 v[194:197], v180 offset:3072
	ds_read_b128 v[198:201], v191 offset:32768
	ds_read_b128 v[202:205], v191 offset:33792
	ds_read_b128 v[206:209], v191 offset:34816
	ds_read_b128 v[210:213], v191 offset:35840
	ds_read_b128 v[214:217], v191 offset:36864
	ds_read_b128 v[218:221], v191 offset:37888
	ds_read_b128 v[222:225], v191 offset:38912
	ds_read_b128 v[226:229], v191 offset:39936
	s_waitcnt vmcnt(8)
	s_waitcnt lgkmcnt(0)
	s_barrier
	s_waitcnt lgkmcnt(0)
	v_mfma_f32_16x16x32_bf16 v[126:129], v[134:137], v[198:201], v[126:129]
	v_mfma_f32_16x16x32_bf16 v[122:125], v[142:145], v[198:201], v[122:125]
	v_mfma_f32_16x16x32_bf16 v[110:113], v[134:137], v[206:209], v[110:113]
	v_mfma_f32_16x16x32_bf16 v[106:109], v[142:145], v[206:209], v[106:109]
	v_mfma_f32_16x16x32_bf16 v[94:97], v[134:137], v[214:217], v[94:97]
	v_mfma_f32_16x16x32_bf16 v[90:93], v[142:145], v[214:217], v[90:93]
	v_mfma_f32_16x16x32_bf16 v[78:81], v[134:137], v[222:225], v[78:81]
	v_mfma_f32_16x16x32_bf16 v[74:77], v[142:145], v[222:225], v[74:77]
	v_mfma_f32_16x16x32_bf16 v[126:129], v[138:141], v[202:205], v[126:129]
	v_mfma_f32_16x16x32_bf16 v[122:125], v[146:149], v[202:205], v[122:125]
	v_mfma_f32_16x16x32_bf16 v[110:113], v[138:141], v[210:213], v[110:113]
	v_mfma_f32_16x16x32_bf16 v[106:109], v[146:149], v[210:213], v[106:109]
	v_mfma_f32_16x16x32_bf16 v[94:97], v[138:141], v[218:221], v[94:97]
	v_mfma_f32_16x16x32_bf16 v[90:93], v[146:149], v[218:221], v[90:93]
	v_mfma_f32_16x16x32_bf16 v[78:81], v[138:141], v[226:229], v[78:81]
	v_mfma_f32_16x16x32_bf16 v[74:77], v[146:149], v[226:229], v[74:77]
	v_mfma_f32_16x16x32_bf16 v[118:121], v[150:153], v[198:201], v[118:121]
	v_mfma_f32_16x16x32_bf16 v[114:117], v[174:177], v[198:201], v[114:117]
	v_mfma_f32_16x16x32_bf16 v[102:105], v[150:153], v[206:209], v[102:105]
	v_mfma_f32_16x16x32_bf16 v[98:101], v[174:177], v[206:209], v[98:101]
	v_mfma_f32_16x16x32_bf16 v[86:89], v[150:153], v[214:217], v[86:89]
	v_mfma_f32_16x16x32_bf16 v[82:85], v[174:177], v[214:217], v[82:85]
	v_mfma_f32_16x16x32_bf16 v[70:73], v[150:153], v[222:225], v[70:73]
	v_mfma_f32_16x16x32_bf16 v[66:69], v[174:177], v[222:225], v[66:69]
	v_mfma_f32_16x16x32_bf16 v[118:121], v[170:173], v[202:205], v[118:121]
	v_mfma_f32_16x16x32_bf16 v[114:117], v[194:197], v[202:205], v[114:117]
	v_mfma_f32_16x16x32_bf16 v[102:105], v[170:173], v[210:213], v[102:105]
	v_mfma_f32_16x16x32_bf16 v[98:101], v[194:197], v[210:213], v[98:101]
	v_mfma_f32_16x16x32_bf16 v[86:89], v[170:173], v[218:221], v[86:89]
	v_mfma_f32_16x16x32_bf16 v[82:85], v[194:197], v[218:221], v[82:85]
	v_mfma_f32_16x16x32_bf16 v[70:73], v[170:173], v[226:229], v[70:73]
	v_mfma_f32_16x16x32_bf16 v[66:69], v[194:197], v[226:229], v[66:69]
	s_barrier
	s_add_i32 s2, s2, s42
	v_lshl_add_u64 v[178:179], v[178:179], 0, s[26:27]
	s_mov_b32 m0, s2
	s_nop 0
	global_load_lds_dwordx4 v[178:179], off
	s_add_i32 m0, s2, 0x2000
	s_add_u32 s54, s58, 0x80080
	v_lshl_add_u64 v[178:179], v[182:183], 0, s[26:27]
	s_addc_u32 s55, s59, 0
	s_add_i32 s2, s60, s42
	global_load_lds_dwordx4 v[178:179], off
	v_lshl_add_u64 v[178:179], s[54:55], 0, v[156:157]
	s_mov_b32 m0, s2
	s_nop 0
	global_load_lds_dwordx4 v[178:179], off
	v_lshl_add_u64 v[178:179], s[54:55], 0, v[160:161]
	s_add_i32 m0, s2, 0x2000
	s_nop 0
	global_load_lds_dwordx4 v[178:179], off
	v_lshl_add_u64 v[178:179], v[186:187], 0, s[26:27]
	s_mov_b32 m0, s51
	s_nop 0
	global_load_lds_dwordx4 v[178:179], off
	v_lshl_add_u64 v[178:179], v[230:231], 0, s[26:27]
	s_mov_b32 m0, s52
	s_nop 0
	global_load_lds_dwordx4 v[178:179], off
	ds_read_b128 v[198:201], v191 offset:49152
	ds_read_b128 v[202:205], v191 offset:50176
	ds_read_b128 v[206:209], v191 offset:51200
	ds_read_b128 v[210:213], v191 offset:52224
	ds_read_b128 v[214:217], v191 offset:53248
	ds_read_b128 v[218:221], v191 offset:54272
	ds_read_b128 v[222:225], v191 offset:55296
	ds_read_b128 v[226:229], v191 offset:56320
	s_waitcnt vmcnt(8)
	s_waitcnt lgkmcnt(0)
	s_barrier
	s_waitcnt lgkmcnt(0)
	v_mfma_f32_16x16x32_bf16 v[62:65], v[134:137], v[198:201], v[62:65]
	v_mfma_f32_16x16x32_bf16 v[58:61], v[142:145], v[198:201], v[58:61]
	v_mfma_f32_16x16x32_bf16 v[46:49], v[134:137], v[206:209], v[46:49]
	v_mfma_f32_16x16x32_bf16 v[42:45], v[142:145], v[206:209], v[42:45]
	v_mfma_f32_16x16x32_bf16 v[30:33], v[134:137], v[214:217], v[30:33]
	v_mfma_f32_16x16x32_bf16 v[26:29], v[142:145], v[214:217], v[26:29]
	v_mfma_f32_16x16x32_bf16 v[14:17], v[134:137], v[222:225], v[14:17]
	v_mfma_f32_16x16x32_bf16 v[10:13], v[142:145], v[222:225], v[10:13]
	v_mfma_f32_16x16x32_bf16 v[62:65], v[138:141], v[202:205], v[62:65]
	v_mfma_f32_16x16x32_bf16 v[58:61], v[146:149], v[202:205], v[58:61]
	v_mfma_f32_16x16x32_bf16 v[46:49], v[138:141], v[210:213], v[46:49]
	v_mfma_f32_16x16x32_bf16 v[42:45], v[146:149], v[210:213], v[42:45]
	v_mfma_f32_16x16x32_bf16 v[30:33], v[138:141], v[218:221], v[30:33]
	v_mfma_f32_16x16x32_bf16 v[26:29], v[146:149], v[218:221], v[26:29]
	v_mfma_f32_16x16x32_bf16 v[14:17], v[138:141], v[226:229], v[14:17]
	v_mfma_f32_16x16x32_bf16 v[10:13], v[146:149], v[226:229], v[10:13]
	v_mfma_f32_16x16x32_bf16 v[54:57], v[150:153], v[198:201], v[54:57]
	v_mfma_f32_16x16x32_bf16 v[50:53], v[174:177], v[198:201], v[50:53]
	v_mfma_f32_16x16x32_bf16 v[38:41], v[150:153], v[206:209], v[38:41]
	v_mfma_f32_16x16x32_bf16 v[34:37], v[174:177], v[206:209], v[34:37]
	v_mfma_f32_16x16x32_bf16 v[22:25], v[150:153], v[214:217], v[22:25]
	v_mfma_f32_16x16x32_bf16 v[18:21], v[174:177], v[214:217], v[18:21]
	v_mfma_f32_16x16x32_bf16 v[6:9], v[150:153], v[222:225], v[6:9]
	v_mfma_f32_16x16x32_bf16 v[2:5], v[174:177], v[222:225], v[2:5]
	v_mfma_f32_16x16x32_bf16 v[54:57], v[170:173], v[202:205], v[54:57]
	v_mfma_f32_16x16x32_bf16 v[50:53], v[194:197], v[202:205], v[50:53]
	v_mfma_f32_16x16x32_bf16 v[38:41], v[170:173], v[210:213], v[38:41]
	v_mfma_f32_16x16x32_bf16 v[34:37], v[194:197], v[210:213], v[34:37]
	v_mfma_f32_16x16x32_bf16 v[22:25], v[170:173], v[218:221], v[22:25]
	v_mfma_f32_16x16x32_bf16 v[18:21], v[194:197], v[218:221], v[18:21]
	v_mfma_f32_16x16x32_bf16 v[6:9], v[170:173], v[226:229], v[6:9]
	v_mfma_f32_16x16x32_bf16 v[2:5], v[194:197], v[226:229], v[2:5]
	s_barrier
	s_add_i32 s68, s68, 2
	s_cmp_gt_u32 s68, 29
	s_mov_b64 s[54:55], s[56:57]
	s_cbranch_scc0 .LBB0_1547
	s_and_b64 vcc, exec, s[28:29]
	s_cbranch_vccz .LBB0_1550
	s_barrier

.LBB0_1954:
	s_lshl_b32 s2, s89, 7
	v_add_u32_e32 v142, s82, v205
	v_add_u32_e32 v158, s83, v205
	s_add_u32 s66, s40, s2
	ds_read_b128 v[130:133], v142
	ds_read_b128 v[134:137], v142 offset:1024
	ds_read_b128 v[138:141], v142 offset:2048
	ds_read_b128 v[142:145], v142 offset:3072
	ds_read_b128 v[146:149], v158
	ds_read_b128 v[150:153], v158 offset:1024
	ds_read_b128 v[154:157], v158 offset:2048
	ds_read_b128 v[158:161], v158 offset:3072
	s_addc_u32 s67, s41, 0
	s_add_u32 s68, s66, 0x100
	s_addc_u32 s69, s67, 0
	s_and_b64 s[66:67], s[62:63], exec
	s_cselect_b32 s67, s37, s69
	s_cselect_b32 s66, s85, s68
	s_add_i32 s70, s2, 0x100
	s_and_b64 s[68:69], s[62:63], exec
	s_cselect_b32 s70, 0, s70
	s_add_u32 s2, s38, s2
	s_addc_u32 s69, s39, 0
	s_add_u32 s68, s2, 0x20080
	s_addc_u32 s69, s69, 0
	v_lshl_add_u64 v[210:211], s[68:69], 0, v[194:195]
	s_add_i32 m0, s50, 0xc000
	ds_read_b128 v[162:165], v209
	ds_read_b128 v[166:169], v209 offset:1024
	ds_read_b128 v[170:173], v209 offset:2048
	ds_read_b128 v[174:177], v209 offset:3072
	ds_read_b128 v[178:181], v209 offset:4096
	ds_read_b128 v[182:185], v209 offset:5120
	ds_read_b128 v[186:189], v209 offset:6144
	ds_read_b128 v[190:193], v209 offset:7168
	global_load_lds_dwordx4 v[210:211], off
	v_lshl_add_u64 v[210:211], s[68:69], 0, v[198:199]
	s_add_i32 m0, s50, 0xe000
	s_nop 0
	global_load_lds_dwordx4 v[210:211], off
	s_waitcnt vmcnt(8)
	s_waitcnt lgkmcnt(0)
	s_barrier
	s_waitcnt lgkmcnt(0)
	v_mfma_f32_16x16x32_bf16 v[86:89], v[130:133], v[162:165], v[86:89]
	v_mfma_f32_16x16x32_bf16 v[82:85], v[138:141], v[162:165], v[82:85]
	v_mfma_f32_16x16x32_bf16 v[78:81], v[130:133], v[170:173], v[78:81]
	v_mfma_f32_16x16x32_bf16 v[74:77], v[138:141], v[170:173], v[74:77]
	v_mfma_f32_16x16x32_bf16 v[70:73], v[130:133], v[178:181], v[70:73]
	v_mfma_f32_16x16x32_bf16 v[66:69], v[138:141], v[178:181], v[66:69]
	v_mfma_f32_16x16x32_bf16 v[62:65], v[130:133], v[186:189], v[62:65]
	v_mfma_f32_16x16x32_bf16 v[58:61], v[138:141], v[186:189], v[58:61]
	v_mfma_f32_16x16x32_bf16 v[86:89], v[134:137], v[166:169], v[86:89]
	v_mfma_f32_16x16x32_bf16 v[82:85], v[142:145], v[166:169], v[82:85]
	v_mfma_f32_16x16x32_bf16 v[78:81], v[134:137], v[174:177], v[78:81]
	v_mfma_f32_16x16x32_bf16 v[74:77], v[142:145], v[174:177], v[74:77]
	v_mfma_f32_16x16x32_bf16 v[70:73], v[134:137], v[182:185], v[70:73]
	v_mfma_f32_16x16x32_bf16 v[66:69], v[142:145], v[182:185], v[66:69]
	v_mfma_f32_16x16x32_bf16 v[62:65], v[134:137], v[190:193], v[62:65]
	v_mfma_f32_16x16x32_bf16 v[58:61], v[142:145], v[190:193], v[58:61]
	v_mfma_f32_16x16x32_bf16 v[54:57], v[146:149], v[162:165], v[54:57]
	v_mfma_f32_16x16x32_bf16 v[50:53], v[154:157], v[162:165], v[50:53]
	v_mfma_f32_16x16x32_bf16 v[46:49], v[146:149], v[170:173], v[46:49]
	v_mfma_f32_16x16x32_bf16 v[42:45], v[154:157], v[170:173], v[42:45]
	v_mfma_f32_16x16x32_bf16 v[34:37], v[146:149], v[178:181], v[34:37]
	v_mfma_f32_16x16x32_bf16 v[30:33], v[154:157], v[178:181], v[30:33]
	v_mfma_f32_16x16x32_bf16 v[18:21], v[146:149], v[186:189], v[18:21]
	v_mfma_f32_16x16x32_bf16 v[14:17], v[154:157], v[186:189], v[14:17]
	v_mfma_f32_16x16x32_bf16 v[54:57], v[150:153], v[166:169], v[54:57]
	v_mfma_f32_16x16x32_bf16 v[50:53], v[158:161], v[166:169], v[50:53]
	v_mfma_f32_16x16x32_bf16 v[46:49], v[150:153], v[174:177], v[46:49]
	v_mfma_f32_16x16x32_bf16 v[42:45], v[158:161], v[174:177], v[42:45]
	v_mfma_f32_16x16x32_bf16 v[34:37], v[150:153], v[182:185], v[34:37]
	v_mfma_f32_16x16x32_bf16 v[30:33], v[158:161], v[182:185], v[30:33]
	v_mfma_f32_16x16x32_bf16 v[18:21], v[150:153], v[190:193], v[18:21]
	v_mfma_f32_16x16x32_bf16 v[14:17], v[158:161], v[190:193], v[14:17]
	s_barrier
	s_add_i32 s2, s82, s49
	v_lshl_add_u64 v[210:211], s[66:67], 0, v[196:197]
	s_mov_b32 m0, s2
	s_nop 0
	global_load_lds_dwordx4 v[210:211], off
	s_add_i32 m0, s2, 0x2000
	s_add_u32 s68, s66, 0x20000
	v_lshl_add_u64 v[212:213], s[66:67], 0, v[200:201]
	s_addc_u32 s69, s67, 0
	s_add_i32 s2, s83, s49
	global_load_lds_dwordx4 v[212:213], off
	v_lshl_add_u64 v[214:215], s[68:69], 0, v[196:197]
	s_mov_b32 m0, s2
	s_nop 0
	global_load_lds_dwordx4 v[214:215], off
	s_add_i32 m0, s2, 0x2000
	s_add_u32 s64, s64, s70
	v_lshl_add_u64 v[214:215], s[68:69], 0, v[200:201]
	s_addc_u32 s65, s65, 0
	global_load_lds_dwordx4 v[214:215], off
	v_lshl_add_u64 v[214:215], s[64:65], 0, v[194:195]
	s_mov_b32 m0, s50
	v_lshl_add_u64 v[216:217], s[64:65], 0, v[198:199]
	global_load_lds_dwordx4 v[214:215], off
	s_mov_b32 m0, s51
	s_nop 0
	global_load_lds_dwordx4 v[216:217], off
	ds_read_b128 v[162:165], v209 offset:16384
	ds_read_b128 v[166:169], v209 offset:17408
	ds_read_b128 v[170:173], v209 offset:18432
	ds_read_b128 v[174:177], v209 offset:19456
	ds_read_b128 v[178:181], v209 offset:20480
	ds_read_b128 v[182:185], v209 offset:21504
	ds_read_b128 v[186:189], v209 offset:22528
	ds_read_b128 v[190:193], v209 offset:23552
	s_waitcnt vmcnt(8)
	s_waitcnt lgkmcnt(0)
	s_barrier
	s_waitcnt lgkmcnt(0)
	v_mfma_f32_16x16x32_bf16 v[126:129], v[130:133], v[162:165], v[126:129]
	v_mfma_f32_16x16x32_bf16 v[122:125], v[138:141], v[162:165], v[122:125]
	v_mfma_f32_16x16x32_bf16 v[110:113], v[130:133], v[170:173], v[110:113]
	v_mfma_f32_16x16x32_bf16 v[106:109], v[138:141], v[170:173], v[106:109]
	v_mfma_f32_16x16x32_bf16 v[94:97], v[130:133], v[178:181], v[94:97]
	v_mfma_f32_16x16x32_bf16 v[90:93], v[138:141], v[178:181], v[90:93]
	v_mfma_f32_16x16x32_bf16 v[22:25], v[130:133], v[186:189], v[22:25]
	v_mfma_f32_16x16x32_bf16 v[10:13], v[138:141], v[186:189], v[10:13]
	v_mfma_f32_16x16x32_bf16 v[126:129], v[134:137], v[166:169], v[126:129]
	v_mfma_f32_16x16x32_bf16 v[122:125], v[142:145], v[166:169], v[122:125]
	v_mfma_f32_16x16x32_bf16 v[110:113], v[134:137], v[174:177], v[110:113]
	v_mfma_f32_16x16x32_bf16 v[106:109], v[142:145], v[174:177], v[106:109]
	v_mfma_f32_16x16x32_bf16 v[94:97], v[134:137], v[182:185], v[94:97]
	v_mfma_f32_16x16x32_bf16 v[90:93], v[142:145], v[182:185], v[90:93]
	v_mfma_f32_16x16x32_bf16 v[22:25], v[134:137], v[190:193], v[22:25]
	v_mfma_f32_16x16x32_bf16 v[10:13], v[142:145], v[190:193], v[10:13]
	v_mfma_f32_16x16x32_bf16 v[118:121], v[146:149], v[162:165], v[118:121]
	v_mfma_f32_16x16x32_bf16 v[114:117], v[154:157], v[162:165], v[114:117]
	v_mfma_f32_16x16x32_bf16 v[102:105], v[146:149], v[170:173], v[102:105]
	v_mfma_f32_16x16x32_bf16 v[98:101], v[154:157], v[170:173], v[98:101]
	v_mfma_f32_16x16x32_bf16 v[38:41], v[146:149], v[178:181], v[38:41]
	v_mfma_f32_16x16x32_bf16 v[26:29], v[154:157], v[178:181], v[26:29]
	v_mfma_f32_16x16x32_bf16 v[6:9], v[146:149], v[186:189], v[6:9]
	v_mfma_f32_16x16x32_bf16 v[2:5], v[154:157], v[186:189], v[2:5]
	v_mfma_f32_16x16x32_bf16 v[118:121], v[150:153], v[166:169], v[118:121]
	v_mfma_f32_16x16x32_bf16 v[114:117], v[158:161], v[166:169], v[114:117]
	v_mfma_f32_16x16x32_bf16 v[102:105], v[150:153], v[174:177], v[102:105]
	v_mfma_f32_16x16x32_bf16 v[98:101], v[158:161], v[174:177], v[98:101]
	v_mfma_f32_16x16x32_bf16 v[38:41], v[150:153], v[182:185], v[38:41]
	v_mfma_f32_16x16x32_bf16 v[26:29], v[158:161], v[182:185], v[26:29]
	v_mfma_f32_16x16x32_bf16 v[6:9], v[150:153], v[190:193], v[6:9]
	v_mfma_f32_16x16x32_bf16 v[2:5], v[158:161], v[190:193], v[2:5]
	s_barrier
	s_add_u32 s64, s64, 0x20000
	s_addc_u32 s65, s65, 0
	s_mov_b32 m0, s52
	v_lshl_add_u64 v[218:219], s[64:65], 0, v[194:195]
	global_load_lds_dwordx4 v[218:219], off
	v_lshl_add_u64 v[218:219], s[64:65], 0, v[198:199]
	s_mov_b32 m0, s53
	s_nop 0
	global_load_lds_dwordx4 v[218:219], off
	s_add_i32 s2, 0, 0x18000
	s_add_i32 s68, 0, 0x1c000
	v_add_u32_e32 v130, s2, v205
	v_add_u32_e32 v142, s68, v205
	ds_read_b128 v[146:149], v130
	ds_read_b128 v[150:153], v130 offset:1024
	ds_read_b128 v[154:157], v130 offset:2048
	ds_read_b128 v[158:161], v130 offset:3072
	ds_read_b128 v[130:133], v142
	ds_read_b128 v[134:137], v142 offset:1024
	ds_read_b128 v[138:141], v142 offset:2048
	ds_read_b128 v[142:145], v142 offset:3072
	ds_read_b128 v[162:165], v209 offset:32768
	ds_read_b128 v[166:169], v209 offset:33792
	ds_read_b128 v[170:173], v209 offset:34816
	ds_read_b128 v[174:177], v209 offset:35840
	ds_read_b128 v[178:181], v209 offset:36864
	ds_read_b128 v[182:185], v209 offset:37888
	ds_read_b128 v[186:189], v209 offset:38912
	ds_read_b128 v[190:193], v209 offset:39936
	s_waitcnt vmcnt(8)
	s_waitcnt lgkmcnt(0)
	s_barrier
	s_waitcnt lgkmcnt(0)
	v_mfma_f32_16x16x32_bf16 v[86:89], v[146:149], v[162:165], v[86:89]
	v_mfma_f32_16x16x32_bf16 v[82:85], v[154:157], v[162:165], v[82:85]
	v_mfma_f32_16x16x32_bf16 v[78:81], v[146:149], v[170:173], v[78:81]
	v_mfma_f32_16x16x32_bf16 v[74:77], v[154:157], v[170:173], v[74:77]
	v_mfma_f32_16x16x32_bf16 v[70:73], v[146:149], v[178:181], v[70:73]
	v_mfma_f32_16x16x32_bf16 v[66:69], v[154:157], v[178:181], v[66:69]
	v_mfma_f32_16x16x32_bf16 v[62:65], v[146:149], v[186:189], v[62:65]
	v_mfma_f32_16x16x32_bf16 v[58:61], v[154:157], v[186:189], v[58:61]
	v_mfma_f32_16x16x32_bf16 v[86:89], v[150:153], v[166:169], v[86:89]
	v_mfma_f32_16x16x32_bf16 v[82:85], v[158:161], v[166:169], v[82:85]
	v_mfma_f32_16x16x32_bf16 v[78:81], v[150:153], v[174:177], v[78:81]
	v_mfma_f32_16x16x32_bf16 v[74:77], v[158:161], v[174:177], v[74:77]
	v_mfma_f32_16x16x32_bf16 v[70:73], v[150:153], v[182:185], v[70:73]
	v_mfma_f32_16x16x32_bf16 v[66:69], v[158:161], v[182:185], v[66:69]
	v_mfma_f32_16x16x32_bf16 v[62:65], v[150:153], v[190:193], v[62:65]
	v_mfma_f32_16x16x32_bf16 v[58:61], v[158:161], v[190:193], v[58:61]
	v_mfma_f32_16x16x32_bf16 v[54:57], v[130:133], v[162:165], v[54:57]
	v_mfma_f32_16x16x32_bf16 v[50:53], v[138:141], v[162:165], v[50:53]
	v_mfma_f32_16x16x32_bf16 v[46:49], v[130:133], v[170:173], v[46:49]
	v_mfma_f32_16x16x32_bf16 v[42:45], v[138:141], v[170:173], v[42:45]
	v_mfma_f32_16x16x32_bf16 v[34:37], v[130:133], v[178:181], v[34:37]
	v_mfma_f32_16x16x32_bf16 v[30:33], v[138:141], v[178:181], v[30:33]
	v_mfma_f32_16x16x32_bf16 v[18:21], v[130:133], v[186:189], v[18:21]
	v_mfma_f32_16x16x32_bf16 v[14:17], v[138:141], v[186:189], v[14:17]
	v_mfma_f32_16x16x32_bf16 v[54:57], v[134:137], v[166:169], v[54:57]
	v_mfma_f32_16x16x32_bf16 v[50:53], v[142:145], v[166:169], v[50:53]
	v_mfma_f32_16x16x32_bf16 v[46:49], v[134:137], v[174:177], v[46:49]
	v_mfma_f32_16x16x32_bf16 v[42:45], v[142:145], v[174:177], v[42:45]
	v_mfma_f32_16x16x32_bf16 v[34:37], v[134:137], v[182:185], v[34:37]
	v_mfma_f32_16x16x32_bf16 v[30:33], v[142:145], v[182:185], v[30:33]
	v_mfma_f32_16x16x32_bf16 v[18:21], v[134:137], v[190:193], v[18:21]
	v_mfma_f32_16x16x32_bf16 v[14:17], v[142:145], v[190:193], v[14:17]
	s_barrier
	s_add_i32 s2, s2, s49
	v_lshl_add_u64 v[210:211], v[210:211], 0, s[12:13]
	s_mov_b32 m0, s2
	s_nop 0
	global_load_lds_dwordx4 v[210:211], off
	s_add_i32 m0, s2, 0x2000
	s_add_u32 s64, s66, 0x20080
	v_lshl_add_u64 v[210:211], v[212:213], 0, s[12:13]
	s_addc_u32 s65, s67, 0
	s_add_i32 s2, s68, s49
	global_load_lds_dwordx4 v[210:211], off
	v_lshl_add_u64 v[210:211], s[64:65], 0, v[196:197]
	s_mov_b32 m0, s2
	s_andn2_b64 vcc, exec, s[62:63]
	global_load_lds_dwordx4 v[210:211], off
	v_lshl_add_u64 v[210:211], s[64:65], 0, v[200:201]
	s_add_i32 m0, s2, 0x2000
	s_nop 0
	global_load_lds_dwordx4 v[210:211], off
	v_lshl_add_u64 v[210:211], v[214:215], 0, s[12:13]
	s_mov_b32 m0, s75
	s_nop 0
	global_load_lds_dwordx4 v[210:211], off
	v_lshl_add_u64 v[210:211], v[216:217], 0, s[12:13]
	s_mov_b32 m0, s76
	s_nop 0
	global_load_lds_dwordx4 v[210:211], off
	ds_read_b128 v[186:189], v209 offset:49152
	ds_read_b128 v[190:193], v209 offset:50176
	ds_read_b128 v[178:181], v209 offset:51200
	ds_read_b128 v[182:185], v209 offset:52224
	ds_read_b128 v[170:173], v209 offset:53248
	ds_read_b128 v[174:177], v209 offset:54272
	ds_read_b128 v[162:165], v209 offset:55296
	ds_read_b128 v[166:169], v209 offset:56320
	s_waitcnt vmcnt(8)
	s_waitcnt lgkmcnt(0)
	s_barrier
	s_cbranch_vccnz .LBB0_1936
	v_pk_mul_f32 v[214:215], v[86:87], s[20:21] op_sel_hi:[1,0]
	v_pk_mul_f32 v[216:217], v[82:83], s[20:21] op_sel_hi:[1,0]
	v_mov_b32_e32 v218, 0
	v_mov_b32_e32 v219, 0
	v_cvt_pk_fp8_f32 v218, v214, v215
	v_cvt_pk_fp8_f32 v219, v216, v217
	v_pk_mul_f32 v[214:215], v[88:89], s[20:21] op_sel_hi:[1,0]
	v_pk_mul_f32 v[216:217], v[84:85], s[20:21] op_sel_hi:[1,0]
	v_cvt_pk_fp8_f32 v218, v214, v215 op_sel:[0,0,1]
	v_cvt_pk_fp8_f32 v219, v216, v217 op_sel:[0,0,1]
	v_pk_mul_f32 v[214:215], v[54:55], s[20:21] op_sel_hi:[1,0]
	v_pk_mul_f32 v[216:217], v[50:51], s[20:21] op_sel_hi:[1,0]
	v_mov_b32_e32 v220, 0
	v_mov_b32_e32 v221, 0
	v_mov_b32_e32 v210, v1
	v_mov_b32_e32 v211, v204
	v_cvt_pk_fp8_f32 v220, v214, v215
	v_cvt_pk_fp8_f32 v221, v216, v217
	v_pk_mul_f32 v[214:215], v[56:57], s[20:21] op_sel_hi:[1,0]
	v_add_u32_e32 v210, s87, v210
	v_lshl_add_u32 v212, v211, 3, s88
	v_ashrrev_i32_e32 v211, 31, v210
	v_pk_mul_f32 v[216:217], v[52:53], s[20:21] op_sel_hi:[1,0]
	v_lshlrev_b64 v[210:211], 11, v[210:211]
	v_cvt_pk_fp8_f32 v220, v214, v215 op_sel:[0,0,1]
	v_cvt_pk_fp8_f32 v221, v216, v217 op_sel:[0,0,1]
	v_ashrrev_i32_e32 v213, 31, v212
	v_lshl_add_u64 v[210:211], s[10:11], 0, v[210:211]
	v_lshl_add_u64 v[210:211], v[210:211], 0, v[212:213]
	global_store_dwordx2 v[210:211], v[218:219], off
	global_store_dwordx2 v[210:211], v[220:221], off offset:128
	v_pk_mul_f32 v[214:215], v[78:79], s[20:21] op_sel_hi:[1,0]
	v_pk_mul_f32 v[216:217], v[74:75], s[20:21] op_sel_hi:[1,0]
	v_mov_b32_e32 v218, 0
	v_mov_b32_e32 v219, 0
	v_cvt_pk_fp8_f32 v218, v214, v215
	v_cvt_pk_fp8_f32 v219, v216, v217
	v_pk_mul_f32 v[214:215], v[80:81], s[20:21] op_sel_hi:[1,0]
	v_pk_mul_f32 v[216:217], v[76:77], s[20:21] op_sel_hi:[1,0]
	v_cvt_pk_fp8_f32 v218, v214, v215 op_sel:[0,0,1]
	v_cvt_pk_fp8_f32 v219, v216, v217 op_sel:[0,0,1]
	v_pk_mul_f32 v[214:215], v[46:47], s[20:21] op_sel_hi:[1,0]
	v_pk_mul_f32 v[216:217], v[42:43], s[20:21] op_sel_hi:[1,0]
	v_mov_b32_e32 v220, 0
	v_mov_b32_e32 v221, 0
	v_cvt_pk_fp8_f32 v220, v214, v215
	v_cvt_pk_fp8_f32 v221, v216, v217
	v_pk_mul_f32 v[214:215], v[48:49], s[20:21] op_sel_hi:[1,0]
	v_pk_mul_f32 v[216:217], v[44:45], s[20:21] op_sel_hi:[1,0]
	v_cvt_pk_fp8_f32 v220, v214, v215 op_sel:[0,0,1]
	v_cvt_pk_fp8_f32 v221, v216, v217 op_sel:[0,0,1]
	s_mov_b32 s2, 0x8000
	v_add_co_u32_e32 v214, vcc, s2, v210
	v_lshl_add_u64 v[212:213], v[210:211], 0, s[24:25]
	s_nop 0
	v_addc_co_u32_e32 v215, vcc, 0, v211, vcc
	global_store_dwordx2 v[214:215], v[218:219], off
	global_store_dwordx2 v[212:213], v[220:221], off offset:128
	v_pk_mul_f32 v[214:215], v[70:71], s[20:21] op_sel_hi:[1,0]
	v_pk_mul_f32 v[216:217], v[66:67], s[20:21] op_sel_hi:[1,0]
	v_mov_b32_e32 v218, 0
	v_mov_b32_e32 v219, 0
	v_cvt_pk_fp8_f32 v218, v214, v215
	v_cvt_pk_fp8_f32 v219, v216, v217
	v_pk_mul_f32 v[214:215], v[72:73], s[20:21] op_sel_hi:[1,0]
	v_pk_mul_f32 v[216:217], v[68:69], s[20:21] op_sel_hi:[1,0]
	v_cvt_pk_fp8_f32 v218, v214, v215 op_sel:[0,0,1]
	v_cvt_pk_fp8_f32 v219, v216, v217 op_sel:[0,0,1]
	v_pk_mul_f32 v[214:215], v[34:35], s[20:21] op_sel_hi:[1,0]
	v_pk_mul_f32 v[216:217], v[30:31], s[20:21] op_sel_hi:[1,0]
	v_mov_b32_e32 v220, 0
	v_mov_b32_e32 v221, 0
	v_cvt_pk_fp8_f32 v220, v214, v215
	v_cvt_pk_fp8_f32 v221, v216, v217
	v_pk_mul_f32 v[214:215], v[36:37], s[20:21] op_sel_hi:[1,0]
	v_pk_mul_f32 v[216:217], v[32:33], s[20:21] op_sel_hi:[1,0]
	v_cvt_pk_fp8_f32 v220, v214, v215 op_sel:[0,0,1]
	v_cvt_pk_fp8_f32 v221, v216, v217 op_sel:[0,0,1]
	s_mov_b32 s2, 0x10000
	v_add_co_u32_e32 v214, vcc, s2, v210
	v_lshl_add_u64 v[212:213], v[210:211], 0, s[28:29]
	s_nop 0
	v_addc_co_u32_e32 v215, vcc, 0, v211, vcc
	global_store_dwordx2 v[214:215], v[218:219], off
	global_store_dwordx2 v[212:213], v[220:221], off offset:128
	v_pk_mul_f32 v[214:215], v[62:63], s[20:21] op_sel_hi:[1,0]
	v_pk_mul_f32 v[216:217], v[58:59], s[20:21] op_sel_hi:[1,0]
	v_mov_b32_e32 v218, 0
	v_mov_b32_e32 v219, 0
	v_cvt_pk_fp8_f32 v218, v214, v215
	v_cvt_pk_fp8_f32 v219, v216, v217
	v_pk_mul_f32 v[214:215], v[64:65], s[20:21] op_sel_hi:[1,0]
	v_pk_mul_f32 v[216:217], v[60:61], s[20:21] op_sel_hi:[1,0]
	v_cvt_pk_fp8_f32 v218, v214, v215 op_sel:[0,0,1]
	v_cvt_pk_fp8_f32 v219, v216, v217 op_sel:[0,0,1]
	v_pk_mul_f32 v[214:215], v[18:19], s[20:21] op_sel_hi:[1,0]
	v_pk_mul_f32 v[216:217], v[14:15], s[20:21] op_sel_hi:[1,0]
	v_mov_b32_e32 v220, 0
	v_mov_b32_e32 v221, 0
	v_cvt_pk_fp8_f32 v220, v214, v215
	v_cvt_pk_fp8_f32 v221, v216, v217
	v_pk_mul_f32 v[214:215], v[20:21], s[20:21] op_sel_hi:[1,0]
	v_pk_mul_f32 v[216:217], v[16:17], s[20:21] op_sel_hi:[1,0]
	v_cvt_pk_fp8_f32 v220, v214, v215 op_sel:[0,0,1]
	v_cvt_pk_fp8_f32 v221, v216, v217 op_sel:[0,0,1]
	s_mov_b32 s2, 0x18000
	v_lshl_add_u64 v[212:213], v[210:211], 0, s[30:31]
	v_add_co_u32_e32 v210, vcc, s2, v210
	s_nop 1
	v_addc_co_u32_e32 v211, vcc, 0, v211, vcc
	global_store_dwordx2 v[210:211], v[218:219], off
	global_store_dwordx2 v[212:213], v[220:221], off offset:128
	s_branch .LBB0_1936
